# v66 + first K-iteration of every fp8 tile peeled (first 32 MFMAs take C=0): no VALU accumulator zeroing in the five non-merge fp8 GEMM calls
# speedup vs baseline: 1.0106x; 1.0106x over previous
; #define PG8_STAGE(bufoff, gbase, voff) do { _Pragma("unroll") for (int _i = 0; _i < 2; ++_i) \
;         __builtin_amdgcn_global_load_lds((const unsigned*)((const char*)(gbase) + (voff)[_i]), (PG8_LAS unsigned*)(lds + (bufoff) + ldsw + _i * 8192), 16, 0, 0); } while (0)
; #define PG8_WAIT_V(n) asm volatile("s_waitcnt vmcnt(" #n ")" ::: "memory")
; #define PG8_WAIT_L(n) asm volatile("s_waitcnt lgkmcnt(" #n ")" ::: "memory")
; #define PG8_BAR __builtin_amdgcn_s_barrier()
; #define PG8_SCHED __builtin_amdgcn_sched_barrier(0)
; template <class Epi, class Sched, bool ALIGN_EPI = true, bool F8 = false>
; __device__ __forceinline__ void gemm_phase(PG8_LAS unsigned char* lds, const Sched& S, const Epi& E) {
;     ...
;             PG8_LDB(B0, 0, 0); PG8_LDB(B1, 0, 1); PG8_SCHED; PG8_LDA(At, 0, 0); PG8_STAGE(PG8_SA(1, 1), a1, voffA[1]);
;             PG8_WAIT_V(8); PG8_WAIT_L(0); PG8_BAR; PG8_MMA(0, 0, At, B0); PG8_MMA(0, 1, At, B1); PG8_BAR; PG8_SCHED;
;             PG8_LDA(At, 0, 1); PG8_STAGE(PG8_SB(0, 0), b2, voffB[0]); PG8_STAGE(PG8_SB(0, 1), b2, voffB[1]); PG8_STAGE(PG8_SA(0, 0), a2, vA2[0]);
;             PG8_WAIT_V(8); PG8_WAIT_L(0); PG8_BAR; PG8_MMA(1, 0, At, B0); PG8_MMA(1, 1, At, B1); PG8_BAR; PG8_SCHED;
;     ...
;         for (int a = 0; a < 2; ++a)
; #pragma unroll
;             for (int b = 0; b < 2; ++b)
; #pragma unroll
;                 for (int m = 0; m < 4; ++m)
; #pragma unroll
;                     for (int n = 0; n < 2; ++n) acc[a][b][m][n] = (f32x4){0.f, 0.f, 0.f, 0.f};
.LBB0_371:
	s_add_u32 s5, s28, 0x10000
	s_addc_u32 s19, s29, 0
	s_add_u32 s26, s26, 0x8000
	s_addc_u32 s27, s27, 0
	s_mov_b32 s21, -2
	s_bitcmp1_b32 s3, 2
	s_cbranch_scc1 .Lh1e_9967
.Lpk0_372:
	ds_read_b128 v[18:21], v207
	ds_read_b128 v[22:25], v207 offset:1024
	ds_read_b128 v[26:29], v207 offset:2048
	ds_read_b128 v[30:33], v207 offset:3072
	ds_read_b128 v[2:5], v208
	ds_read_b128 v[6:9], v208 offset:1024
	ds_read_b128 v[10:13], v208 offset:2048
	ds_read_b128 v[14:17], v208 offset:3072
	s_add_u32 s28, s26, 0x8000
	s_addc_u32 s29, s27, 0
	s_cmp_eq_u32 s21, 12
	s_cselect_b32 s40, s22, s28
	s_cselect_b32 s41, s23, s29
	s_cselect_b32 s30, s24, s5
	s_cselect_b32 s31, s25, s19
	s_add_u32 s28, s40, 0x8000
	s_addc_u32 s29, s41, 0
	v_lshl_add_u64 v[244:245], s[26:27], 0, v[190:191]
	s_add_i32 m0, s46, 0xc000
	ds_read_b128 v[212:215], v209
	ds_read_b128 v[216:219], v209 offset:1024
	ds_read_b128 v[220:223], v209 offset:2048
	ds_read_b128 v[224:227], v209 offset:3072
	ds_read_b128 v[228:231], v209 offset:4096
	ds_read_b128 v[232:235], v209 offset:5120
	ds_read_b128 v[236:239], v209 offset:6144
	ds_read_b128 v[240:243], v209 offset:7168
	global_load_lds_dwordx4 v[244:245], off
	v_lshl_add_u64 v[244:245], s[26:27], 0, v[188:189]
	s_add_i32 m0, s46, 0xe000
	s_nop 0
	global_load_lds_dwordx4 v[244:245], off
	s_waitcnt vmcnt(8)
	s_waitcnt lgkmcnt(0)
	s_setprio 1
	v_mfma_scale_f32_16x16x128_f8f6f4 v[158:161], v[18:25], v[212:219], 0, v210, v210 op_sel_hi:[0,0,0]
	v_mfma_scale_f32_16x16x128_f8f6f4 v[154:157], v[26:33], v[212:219], 0, v210, v210 op_sel_hi:[0,0,0]
	v_mfma_scale_f32_16x16x128_f8f6f4 v[142:145], v[18:25], v[220:227], 0, v210, v210 op_sel_hi:[0,0,0]
	v_mfma_scale_f32_16x16x128_f8f6f4 v[138:141], v[26:33], v[220:227], 0, v210, v210 op_sel_hi:[0,0,0]
	v_mfma_scale_f32_16x16x128_f8f6f4 v[126:129], v[18:25], v[228:235], 0, v210, v210 op_sel_hi:[0,0,0]
	v_mfma_scale_f32_16x16x128_f8f6f4 v[122:125], v[26:33], v[228:235], 0, v210, v210 op_sel_hi:[0,0,0]
	v_mfma_scale_f32_16x16x128_f8f6f4 v[110:113], v[18:25], v[236:243], 0, v210, v210 op_sel_hi:[0,0,0]
	v_mfma_scale_f32_16x16x128_f8f6f4 v[106:109], v[26:33], v[236:243], 0, v210, v210 op_sel_hi:[0,0,0]
	s_nop 3
	s_setprio 0
	s_setprio 1
	v_mfma_scale_f32_16x16x128_f8f6f4 v[150:153], v[2:9], v[212:219], 0, v210, v210 op_sel_hi:[0,0,0]
	v_mfma_scale_f32_16x16x128_f8f6f4 v[146:149], v[10:17], v[212:219], 0, v210, v210 op_sel_hi:[0,0,0]
	v_mfma_scale_f32_16x16x128_f8f6f4 v[134:137], v[2:9], v[220:227], 0, v210, v210 op_sel_hi:[0,0,0]
	v_mfma_scale_f32_16x16x128_f8f6f4 v[130:133], v[10:17], v[220:227], 0, v210, v210 op_sel_hi:[0,0,0]
	v_mfma_scale_f32_16x16x128_f8f6f4 v[118:121], v[2:9], v[228:235], 0, v210, v210 op_sel_hi:[0,0,0]
	v_mfma_scale_f32_16x16x128_f8f6f4 v[114:117], v[10:17], v[228:235], 0, v210, v210 op_sel_hi:[0,0,0]
	v_mfma_scale_f32_16x16x128_f8f6f4 v[102:105], v[2:9], v[236:243], 0, v210, v210 op_sel_hi:[0,0,0]
	v_mfma_scale_f32_16x16x128_f8f6f4 v[98:101], v[10:17], v[236:243], 0, v210, v210 op_sel_hi:[0,0,0]
	s_setprio 0
	s_barrier
	s_add_i32 s67, s62, s45
	v_lshl_add_u64 v[244:245], s[30:31], 0, v[164:165]
	s_mov_b32 m0, s67
	ds_read_b128 v[212:215], v209 offset:16384
	ds_read_b128 v[216:219], v209 offset:17408
	ds_read_b128 v[220:223], v209 offset:18432
	ds_read_b128 v[224:227], v209 offset:19456
	ds_read_b128 v[228:231], v209 offset:20480
	ds_read_b128 v[232:235], v209 offset:21504
	ds_read_b128 v[236:239], v209 offset:22528
	ds_read_b128 v[240:243], v209 offset:23552
	global_load_lds_dwordx4 v[244:245], off
	v_lshl_add_u64 v[246:247], s[30:31], 0, v[166:167]
	s_add_i32 m0, s67, 0x2000
	s_add_i32 s67, s63, s45
	global_load_lds_dwordx4 v[246:247], off
	v_lshl_add_u64 v[244:245], v[244:245], 0, s[8:9]
	s_mov_b32 m0, s67
	s_nop 0
	global_load_lds_dwordx4 v[244:245], off
	v_lshl_add_u64 v[244:245], v[246:247], 0, s[8:9]
	s_add_i32 m0, s67, 0x2000
	s_nop 0
	global_load_lds_dwordx4 v[244:245], off
	v_lshl_add_u64 v[244:245], s[40:41], 0, v[174:175]
	s_mov_b32 m0, s46
	s_nop 0
	global_load_lds_dwordx4 v[244:245], off
	v_lshl_add_u64 v[244:245], s[40:41], 0, v[176:177]
	s_mov_b32 m0, s47
	s_nop 0
	global_load_lds_dwordx4 v[244:245], off
	s_waitcnt vmcnt(8)
	s_waitcnt lgkmcnt(0)
	s_setprio 1
	v_mfma_scale_f32_16x16x128_f8f6f4 v[94:97], v[18:25], v[212:219], 0, v210, v210 op_sel_hi:[0,0,0]
	v_mfma_scale_f32_16x16x128_f8f6f4 v[90:93], v[26:33], v[212:219], 0, v210, v210 op_sel_hi:[0,0,0]
	v_mfma_scale_f32_16x16x128_f8f6f4 v[78:81], v[18:25], v[220:227], 0, v210, v210 op_sel_hi:[0,0,0]
	v_mfma_scale_f32_16x16x128_f8f6f4 v[74:77], v[26:33], v[220:227], 0, v210, v210 op_sel_hi:[0,0,0]
	v_mfma_scale_f32_16x16x128_f8f6f4 v[62:65], v[18:25], v[228:235], 0, v210, v210 op_sel_hi:[0,0,0]
	v_mfma_scale_f32_16x16x128_f8f6f4 v[58:61], v[26:33], v[228:235], 0, v210, v210 op_sel_hi:[0,0,0]
	v_mfma_scale_f32_16x16x128_f8f6f4 v[46:49], v[18:25], v[236:243], 0, v210, v210 op_sel_hi:[0,0,0]
	v_mfma_scale_f32_16x16x128_f8f6f4 v[42:45], v[26:33], v[236:243], 0, v210, v210 op_sel_hi:[0,0,0]
	s_nop 3
	s_setprio 0
	s_setprio 1
	v_mfma_scale_f32_16x16x128_f8f6f4 v[86:89], v[2:9], v[212:219], 0, v210, v210 op_sel_hi:[0,0,0]
	v_mfma_scale_f32_16x16x128_f8f6f4 v[82:85], v[10:17], v[212:219], 0, v210, v210 op_sel_hi:[0,0,0]
	v_mfma_scale_f32_16x16x128_f8f6f4 v[70:73], v[2:9], v[220:227], 0, v210, v210 op_sel_hi:[0,0,0]
	v_mfma_scale_f32_16x16x128_f8f6f4 v[66:69], v[10:17], v[220:227], 0, v210, v210 op_sel_hi:[0,0,0]
	v_mfma_scale_f32_16x16x128_f8f6f4 v[54:57], v[2:9], v[228:235], 0, v210, v210 op_sel_hi:[0,0,0]
	v_mfma_scale_f32_16x16x128_f8f6f4 v[50:53], v[10:17], v[228:235], 0, v210, v210 op_sel_hi:[0,0,0]
	v_mfma_scale_f32_16x16x128_f8f6f4 v[38:41], v[2:9], v[236:243], 0, v210, v210 op_sel_hi:[0,0,0]
	v_mfma_scale_f32_16x16x128_f8f6f4 v[34:37], v[10:17], v[236:243], 0, v210, v210 op_sel_hi:[0,0,0]
	s_setprio 0
	s_barrier
; #define PG8_STAGE(bufoff, gbase, voff) do { _Pragma("unroll") for (int _i = 0; _i < 2; ++_i) \
;         __builtin_amdgcn_global_load_lds((const unsigned*)((const char*)(gbase) + (voff)[_i]), (PG8_LAS unsigned*)(lds + (bufoff) + ldsw + _i * 8192), 16, 0, 0); } while (0)
; #define PG8_WAIT_V(n) asm volatile("s_waitcnt vmcnt(" #n ")" ::: "memory")
; #define PG8_WAIT_L(n) asm volatile("s_waitcnt lgkmcnt(" #n ")" ::: "memory")
; #define PG8_BAR __builtin_amdgcn_s_barrier()
; #define PG8_SCHED __builtin_amdgcn_sched_barrier(0)
; template <class Epi, class Sched, bool ALIGN_EPI = true, bool F8 = false>
; __device__ __forceinline__ void gemm_phase(PG8_LAS unsigned char* lds, const Sched& S, const Epi& E) {
;     ...
;             PG8_LDB(B0, 1, 0); PG8_LDB(B1, 1, 1); PG8_SCHED; PG8_LDA(At, 1, 0); PG8_STAGE(PG8_SA(0, 1), a2, vA2[1]);
;             PG8_WAIT_V(8); PG8_WAIT_L(0); PG8_BAR; PG8_MMA(0, 0, At, B0); PG8_MMA(0, 1, At, B1); PG8_BAR; PG8_SCHED;
;             PG8_LDA(At, 1, 1); PG8_STAGE(PG8_SB(1, 0), b3, voffB[0]); PG8_STAGE(PG8_SB(1, 1), b3, voffB[1]); PG8_STAGE(PG8_SA(1, 0), a3, vA2[0]);
;             PG8_WAIT_V(8); PG8_WAIT_L(0); PG8_BAR; PG8_MMA(1, 0, At, B0); PG8_MMA(1, 1, At, B1); PG8_BAR; PG8_SCHED;
	s_add_i32 s67, 0, 0x18000
	s_add_i32 s68, 0, 0x1c000
	v_add_u32_e32 v14, s67, v202
	v_add_u32_e32 v30, s68, v202
	ds_read_b128 v[2:5], v14
	ds_read_b128 v[6:9], v14 offset:1024
	ds_read_b128 v[10:13], v14 offset:2048
	ds_read_b128 v[14:17], v14 offset:3072
	ds_read_b128 v[18:21], v30
	ds_read_b128 v[22:25], v30 offset:1024
	ds_read_b128 v[26:29], v30 offset:2048
	ds_read_b128 v[30:33], v30 offset:3072
	s_mov_b32 m0, s48
	v_lshl_add_u64 v[244:245], s[40:41], 0, v[178:179]
	ds_read_b128 v[212:215], v209 offset:32768
	ds_read_b128 v[216:219], v209 offset:33792
	ds_read_b128 v[220:223], v209 offset:34816
	ds_read_b128 v[224:227], v209 offset:35840
	ds_read_b128 v[228:231], v209 offset:36864
	ds_read_b128 v[232:235], v209 offset:37888
	ds_read_b128 v[236:239], v209 offset:38912
	ds_read_b128 v[240:243], v209 offset:39936
	global_load_lds_dwordx4 v[244:245], off
	v_lshl_add_u64 v[244:245], s[40:41], 0, v[180:181]
	s_mov_b32 m0, s49
	s_nop 0
	global_load_lds_dwordx4 v[244:245], off
	s_waitcnt vmcnt(8)
	s_waitcnt lgkmcnt(0)
	s_setprio 1
	v_mfma_scale_f32_16x16x128_f8f6f4 v[158:161], v[2:9], v[212:219], v[158:161], v210, v210 op_sel_hi:[0,0,0]
	v_mfma_scale_f32_16x16x128_f8f6f4 v[154:157], v[10:17], v[212:219], v[154:157], v210, v210 op_sel_hi:[0,0,0]
	v_mfma_scale_f32_16x16x128_f8f6f4 v[142:145], v[2:9], v[220:227], v[142:145], v210, v210 op_sel_hi:[0,0,0]
	v_mfma_scale_f32_16x16x128_f8f6f4 v[138:141], v[10:17], v[220:227], v[138:141], v210, v210 op_sel_hi:[0,0,0]
	v_mfma_scale_f32_16x16x128_f8f6f4 v[126:129], v[2:9], v[228:235], v[126:129], v210, v210 op_sel_hi:[0,0,0]
	v_mfma_scale_f32_16x16x128_f8f6f4 v[122:125], v[10:17], v[228:235], v[122:125], v210, v210 op_sel_hi:[0,0,0]
	v_mfma_scale_f32_16x16x128_f8f6f4 v[110:113], v[2:9], v[236:243], v[110:113], v210, v210 op_sel_hi:[0,0,0]
	v_mfma_scale_f32_16x16x128_f8f6f4 v[106:109], v[10:17], v[236:243], v[106:109], v210, v210 op_sel_hi:[0,0,0]
	s_nop 3
	s_setprio 0
	s_setprio 1
	v_mfma_scale_f32_16x16x128_f8f6f4 v[150:153], v[18:25], v[212:219], v[150:153], v210, v210 op_sel_hi:[0,0,0]
	v_mfma_scale_f32_16x16x128_f8f6f4 v[146:149], v[26:33], v[212:219], v[146:149], v210, v210 op_sel_hi:[0,0,0]
	v_mfma_scale_f32_16x16x128_f8f6f4 v[134:137], v[18:25], v[220:227], v[134:137], v210, v210 op_sel_hi:[0,0,0]
	v_mfma_scale_f32_16x16x128_f8f6f4 v[130:133], v[26:33], v[220:227], v[130:133], v210, v210 op_sel_hi:[0,0,0]
	v_mfma_scale_f32_16x16x128_f8f6f4 v[118:121], v[18:25], v[228:235], v[118:121], v210, v210 op_sel_hi:[0,0,0]
	v_mfma_scale_f32_16x16x128_f8f6f4 v[114:117], v[26:33], v[228:235], v[114:117], v210, v210 op_sel_hi:[0,0,0]
	v_mfma_scale_f32_16x16x128_f8f6f4 v[102:105], v[18:25], v[236:243], v[102:105], v210, v210 op_sel_hi:[0,0,0]
	v_mfma_scale_f32_16x16x128_f8f6f4 v[98:101], v[26:33], v[236:243], v[98:101], v210, v210 op_sel_hi:[0,0,0]
	s_setprio 0
	s_barrier
	s_add_u32 s30, s30, 0x8000
	s_addc_u32 s31, s31, 0
	s_add_i32 s40, s67, s45
	v_lshl_add_u64 v[244:245], s[30:31], 0, v[164:165]
	s_mov_b32 m0, s40
	ds_read_b128 v[212:215], v209 offset:49152
	ds_read_b128 v[216:219], v209 offset:50176
	ds_read_b128 v[220:223], v209 offset:51200
	ds_read_b128 v[224:227], v209 offset:52224
	ds_read_b128 v[228:231], v209 offset:53248
	ds_read_b128 v[232:235], v209 offset:54272
	ds_read_b128 v[236:239], v209 offset:55296
	ds_read_b128 v[240:243], v209 offset:56320
	global_load_lds_dwordx4 v[244:245], off
	v_lshl_add_u64 v[244:245], s[30:31], 0, v[166:167]
	s_add_i32 m0, s40, 0x2000
	s_add_i32 s40, s68, s45
	global_load_lds_dwordx4 v[244:245], off
	v_lshl_add_u64 v[244:245], s[30:31], 0, v[168:169]
	s_mov_b32 m0, s40
	s_nop 0
	global_load_lds_dwordx4 v[244:245], off
	v_lshl_add_u64 v[244:245], s[30:31], 0, v[172:173]
	s_add_i32 m0, s40, 0x2000
	s_nop 0
	global_load_lds_dwordx4 v[244:245], off
	v_lshl_add_u64 v[244:245], s[28:29], 0, v[174:175]
	s_mov_b32 m0, s52
	s_nop 0
	global_load_lds_dwordx4 v[244:245], off
	v_lshl_add_u64 v[244:245], s[28:29], 0, v[176:177]
	s_mov_b32 m0, s53
	s_nop 0
	global_load_lds_dwordx4 v[244:245], off
	s_waitcnt vmcnt(8)
	s_waitcnt lgkmcnt(0)
	s_setprio 1
	v_mfma_scale_f32_16x16x128_f8f6f4 v[94:97], v[2:9], v[212:219], v[94:97], v210, v210 op_sel_hi:[0,0,0]
	v_mfma_scale_f32_16x16x128_f8f6f4 v[90:93], v[10:17], v[212:219], v[90:93], v210, v210 op_sel_hi:[0,0,0]
	v_mfma_scale_f32_16x16x128_f8f6f4 v[78:81], v[2:9], v[220:227], v[78:81], v210, v210 op_sel_hi:[0,0,0]
	v_mfma_scale_f32_16x16x128_f8f6f4 v[74:77], v[10:17], v[220:227], v[74:77], v210, v210 op_sel_hi:[0,0,0]
	v_mfma_scale_f32_16x16x128_f8f6f4 v[62:65], v[2:9], v[228:235], v[62:65], v210, v210 op_sel_hi:[0,0,0]
	v_mfma_scale_f32_16x16x128_f8f6f4 v[58:61], v[10:17], v[228:235], v[58:61], v210, v210 op_sel_hi:[0,0,0]
	v_mfma_scale_f32_16x16x128_f8f6f4 v[46:49], v[2:9], v[236:243], v[46:49], v210, v210 op_sel_hi:[0,0,0]
	v_mfma_scale_f32_16x16x128_f8f6f4 v[42:45], v[10:17], v[236:243], v[42:45], v210, v210 op_sel_hi:[0,0,0]
	s_nop 3
	s_setprio 0
	s_setprio 1
	v_mfma_scale_f32_16x16x128_f8f6f4 v[86:89], v[18:25], v[212:219], v[86:89], v210, v210 op_sel_hi:[0,0,0]
	v_mfma_scale_f32_16x16x128_f8f6f4 v[82:85], v[26:33], v[212:219], v[82:85], v210, v210 op_sel_hi:[0,0,0]
	v_mfma_scale_f32_16x16x128_f8f6f4 v[70:73], v[18:25], v[220:227], v[70:73], v210, v210 op_sel_hi:[0,0,0]
	v_mfma_scale_f32_16x16x128_f8f6f4 v[66:69], v[26:33], v[220:227], v[66:69], v210, v210 op_sel_hi:[0,0,0]
	v_mfma_scale_f32_16x16x128_f8f6f4 v[54:57], v[18:25], v[228:235], v[54:57], v210, v210 op_sel_hi:[0,0,0]
	v_mfma_scale_f32_16x16x128_f8f6f4 v[50:53], v[26:33], v[228:235], v[50:53], v210, v210 op_sel_hi:[0,0,0]
	v_mfma_scale_f32_16x16x128_f8f6f4 v[38:41], v[18:25], v[236:243], v[38:41], v210, v210 op_sel_hi:[0,0,0]
	v_mfma_scale_f32_16x16x128_f8f6f4 v[34:37], v[26:33], v[236:243], v[34:37], v210, v210 op_sel_hi:[0,0,0]
	s_setprio 0
	s_barrier
	s_add_i32 s21, s21, 2
	s_add_u32 s5, s5, 0x10000
	s_addc_u32 s19, s19, 0
	s_add_u32 s26, s26, 0x10000
	s_addc_u32 s27, s27, 0
	s_cmp_gt_u32 s21, 13
	s_cbranch_scc0 .LBB0_372
	s_branch .Lfx_9967

; #define PG8_STAGE(bufoff, gbase, voff) do { _Pragma("unroll") for (int _i = 0; _i < 2; ++_i) \
;         __builtin_amdgcn_global_load_lds((const unsigned*)((const char*)(gbase) + (voff)[_i]), (PG8_LAS unsigned*)(lds + (bufoff) + ldsw + _i * 8192), 16, 0, 0); } while (0)
; #define PG8_WAIT_V(n) asm volatile("s_waitcnt vmcnt(" #n ")" ::: "memory")
; #define PG8_WAIT_L(n) asm volatile("s_waitcnt lgkmcnt(" #n ")" ::: "memory")
; #define PG8_BAR __builtin_amdgcn_s_barrier()
; #define PG8_SCHED __builtin_amdgcn_sched_barrier(0)
; template <class Epi, class Sched, bool ALIGN_EPI = true, bool F8 = false>
; __device__ __forceinline__ void gemm_phase(PG8_LAS unsigned char* lds, const Sched& S, const Epi& E) {
;     ...
;             PG8_LDB(B0, 0, 0); PG8_LDB(B1, 0, 1); PG8_SCHED; PG8_LDA(At, 0, 0); PG8_STAGE(PG8_SA(1, 1), a1, voffA[1]);
;             PG8_WAIT_V(8); PG8_WAIT_L(0); PG8_BAR; PG8_MMA(0, 0, At, B0); PG8_MMA(0, 1, At, B1); PG8_BAR; PG8_SCHED;
;             PG8_LDA(At, 0, 1); PG8_STAGE(PG8_SB(0, 0), b2, voffB[0]); PG8_STAGE(PG8_SB(0, 1), b2, voffB[1]); PG8_STAGE(PG8_SA(0, 0), a2, vA2[0]);
;             PG8_WAIT_V(8); PG8_WAIT_L(0); PG8_BAR; PG8_MMA(1, 0, At, B0); PG8_MMA(1, 1, At, B1); PG8_BAR; PG8_SCHED;
;             PG8_LDB(B0, 1, 0); PG8_LDB(B1, 1, 1); PG8_SCHED; PG8_LDA(At, 1, 0); PG8_STAGE(PG8_SA(0, 1), a2, vA2[1]);
;             PG8_WAIT_V(8); PG8_WAIT_L(0); PG8_BAR; PG8_MMA(0, 0, At, B0); PG8_MMA(0, 1, At, B1); PG8_BAR; PG8_SCHED;
.Lh1e_9967:
.Lpk1_372:
	ds_read_b128 v[18:21], v207
	ds_read_b128 v[22:25], v207 offset:1024
	ds_read_b128 v[26:29], v207 offset:2048
	ds_read_b128 v[30:33], v207 offset:3072
	ds_read_b128 v[2:5], v208
	ds_read_b128 v[6:9], v208 offset:1024
	ds_read_b128 v[10:13], v208 offset:2048
	ds_read_b128 v[14:17], v208 offset:3072
	s_add_u32 s28, s26, 0x8000
	s_addc_u32 s29, s27, 0
	s_cmp_eq_u32 s21, 12
	s_cselect_b32 s40, s22, s28
	s_cselect_b32 s41, s23, s29
	s_cselect_b32 s30, s24, s5
	s_cselect_b32 s31, s25, s19
	s_add_u32 s28, s40, 0x8000
	s_addc_u32 s29, s41, 0
	v_lshl_add_u64 v[244:245], s[26:27], 0, v[190:191]
	s_add_i32 m0, s46, 0xc000
	ds_read_b128 v[212:215], v209
	ds_read_b128 v[216:219], v209 offset:1024
	ds_read_b128 v[220:223], v209 offset:2048
	ds_read_b128 v[224:227], v209 offset:3072
	ds_read_b128 v[228:231], v209 offset:4096
	ds_read_b128 v[232:235], v209 offset:5120
	ds_read_b128 v[236:239], v209 offset:6144
	ds_read_b128 v[240:243], v209 offset:7168
	global_load_lds_dwordx4 v[244:245], off
	v_lshl_add_u64 v[244:245], s[26:27], 0, v[188:189]
	s_add_i32 m0, s46, 0xe000
	s_nop 0
	global_load_lds_dwordx4 v[244:245], off
	s_waitcnt vmcnt(8)
	s_waitcnt lgkmcnt(0)
	s_barrier
	s_setprio 2
	v_mfma_scale_f32_16x16x128_f8f6f4 v[158:161], v[18:25], v[212:219], 0, v210, v210 op_sel_hi:[0,0,0]
	v_mfma_scale_f32_16x16x128_f8f6f4 v[154:157], v[26:33], v[212:219], 0, v210, v210 op_sel_hi:[0,0,0]
	v_mfma_scale_f32_16x16x128_f8f6f4 v[142:145], v[18:25], v[220:227], 0, v210, v210 op_sel_hi:[0,0,0]
	v_mfma_scale_f32_16x16x128_f8f6f4 v[138:141], v[26:33], v[220:227], 0, v210, v210 op_sel_hi:[0,0,0]
	v_mfma_scale_f32_16x16x128_f8f6f4 v[126:129], v[18:25], v[228:235], 0, v210, v210 op_sel_hi:[0,0,0]
	v_mfma_scale_f32_16x16x128_f8f6f4 v[122:125], v[26:33], v[228:235], 0, v210, v210 op_sel_hi:[0,0,0]
	v_mfma_scale_f32_16x16x128_f8f6f4 v[110:113], v[18:25], v[236:243], 0, v210, v210 op_sel_hi:[0,0,0]
	v_mfma_scale_f32_16x16x128_f8f6f4 v[106:109], v[26:33], v[236:243], 0, v210, v210 op_sel_hi:[0,0,0]
	s_nop 3
	s_setprio 0
	s_setprio 2
	v_mfma_scale_f32_16x16x128_f8f6f4 v[150:153], v[2:9], v[212:219], 0, v210, v210 op_sel_hi:[0,0,0]
	v_mfma_scale_f32_16x16x128_f8f6f4 v[146:149], v[10:17], v[212:219], 0, v210, v210 op_sel_hi:[0,0,0]
	v_mfma_scale_f32_16x16x128_f8f6f4 v[134:137], v[2:9], v[220:227], 0, v210, v210 op_sel_hi:[0,0,0]
	v_mfma_scale_f32_16x16x128_f8f6f4 v[130:133], v[10:17], v[220:227], 0, v210, v210 op_sel_hi:[0,0,0]
	v_mfma_scale_f32_16x16x128_f8f6f4 v[118:121], v[2:9], v[228:235], 0, v210, v210 op_sel_hi:[0,0,0]
	v_mfma_scale_f32_16x16x128_f8f6f4 v[114:117], v[10:17], v[228:235], 0, v210, v210 op_sel_hi:[0,0,0]
	v_mfma_scale_f32_16x16x128_f8f6f4 v[102:105], v[2:9], v[236:243], 0, v210, v210 op_sel_hi:[0,0,0]
	v_mfma_scale_f32_16x16x128_f8f6f4 v[98:101], v[10:17], v[236:243], 0, v210, v210 op_sel_hi:[0,0,0]
	s_setprio 0
	s_add_i32 s67, s62, s45
	v_lshl_add_u64 v[244:245], s[30:31], 0, v[164:165]
	s_mov_b32 m0, s67
	ds_read_b128 v[212:215], v209 offset:16384
	ds_read_b128 v[216:219], v209 offset:17408
	ds_read_b128 v[220:223], v209 offset:18432
	ds_read_b128 v[224:227], v209 offset:19456
	ds_read_b128 v[228:231], v209 offset:20480
	ds_read_b128 v[232:235], v209 offset:21504
	ds_read_b128 v[236:239], v209 offset:22528
	ds_read_b128 v[240:243], v209 offset:23552
	global_load_lds_dwordx4 v[244:245], off
	v_lshl_add_u64 v[246:247], s[30:31], 0, v[166:167]
	s_add_i32 m0, s67, 0x2000
	s_add_i32 s67, s63, s45
	global_load_lds_dwordx4 v[246:247], off
	v_lshl_add_u64 v[244:245], v[244:245], 0, s[8:9]
	s_mov_b32 m0, s67
	s_nop 0
	global_load_lds_dwordx4 v[244:245], off
	v_lshl_add_u64 v[244:245], v[246:247], 0, s[8:9]
	s_add_i32 m0, s67, 0x2000
	s_nop 0
	global_load_lds_dwordx4 v[244:245], off
	v_lshl_add_u64 v[244:245], s[40:41], 0, v[174:175]
	s_mov_b32 m0, s46
	s_nop 0
	global_load_lds_dwordx4 v[244:245], off
	v_lshl_add_u64 v[244:245], s[40:41], 0, v[176:177]
	s_mov_b32 m0, s47
	s_nop 0
	global_load_lds_dwordx4 v[244:245], off
	s_waitcnt vmcnt(8)
	s_waitcnt lgkmcnt(0)
	s_barrier
	s_setprio 2
	v_mfma_scale_f32_16x16x128_f8f6f4 v[94:97], v[18:25], v[212:219], 0, v210, v210 op_sel_hi:[0,0,0]
	v_mfma_scale_f32_16x16x128_f8f6f4 v[90:93], v[26:33], v[212:219], 0, v210, v210 op_sel_hi:[0,0,0]
	v_mfma_scale_f32_16x16x128_f8f6f4 v[78:81], v[18:25], v[220:227], 0, v210, v210 op_sel_hi:[0,0,0]
	v_mfma_scale_f32_16x16x128_f8f6f4 v[74:77], v[26:33], v[220:227], 0, v210, v210 op_sel_hi:[0,0,0]
	v_mfma_scale_f32_16x16x128_f8f6f4 v[62:65], v[18:25], v[228:235], 0, v210, v210 op_sel_hi:[0,0,0]
	v_mfma_scale_f32_16x16x128_f8f6f4 v[58:61], v[26:33], v[228:235], 0, v210, v210 op_sel_hi:[0,0,0]
	v_mfma_scale_f32_16x16x128_f8f6f4 v[46:49], v[18:25], v[236:243], 0, v210, v210 op_sel_hi:[0,0,0]
	v_mfma_scale_f32_16x16x128_f8f6f4 v[42:45], v[26:33], v[236:243], 0, v210, v210 op_sel_hi:[0,0,0]
	s_nop 3
	s_setprio 0
	s_setprio 2
	v_mfma_scale_f32_16x16x128_f8f6f4 v[86:89], v[2:9], v[212:219], 0, v210, v210 op_sel_hi:[0,0,0]
	v_mfma_scale_f32_16x16x128_f8f6f4 v[82:85], v[10:17], v[212:219], 0, v210, v210 op_sel_hi:[0,0,0]
	v_mfma_scale_f32_16x16x128_f8f6f4 v[70:73], v[2:9], v[220:227], 0, v210, v210 op_sel_hi:[0,0,0]
	v_mfma_scale_f32_16x16x128_f8f6f4 v[66:69], v[10:17], v[220:227], 0, v210, v210 op_sel_hi:[0,0,0]
	v_mfma_scale_f32_16x16x128_f8f6f4 v[54:57], v[2:9], v[228:235], 0, v210, v210 op_sel_hi:[0,0,0]
	v_mfma_scale_f32_16x16x128_f8f6f4 v[50:53], v[10:17], v[228:235], 0, v210, v210 op_sel_hi:[0,0,0]
	v_mfma_scale_f32_16x16x128_f8f6f4 v[38:41], v[2:9], v[236:243], 0, v210, v210 op_sel_hi:[0,0,0]
	v_mfma_scale_f32_16x16x128_f8f6f4 v[34:37], v[10:17], v[236:243], 0, v210, v210 op_sel_hi:[0,0,0]
	s_setprio 0
	s_add_i32 s67, 0, 0x18000
	s_add_i32 s68, 0, 0x1c000
	v_add_u32_e32 v14, s67, v202
	v_add_u32_e32 v30, s68, v202
	ds_read_b128 v[2:5], v14
	ds_read_b128 v[6:9], v14 offset:1024
	ds_read_b128 v[10:13], v14 offset:2048
	ds_read_b128 v[14:17], v14 offset:3072
	ds_read_b128 v[18:21], v30
	ds_read_b128 v[22:25], v30 offset:1024
	ds_read_b128 v[26:29], v30 offset:2048
	ds_read_b128 v[30:33], v30 offset:3072
	s_mov_b32 m0, s48
	v_lshl_add_u64 v[244:245], s[40:41], 0, v[178:179]
	ds_read_b128 v[212:215], v209 offset:32768
	ds_read_b128 v[216:219], v209 offset:33792
	ds_read_b128 v[220:223], v209 offset:34816
	ds_read_b128 v[224:227], v209 offset:35840
	ds_read_b128 v[228:231], v209 offset:36864
	ds_read_b128 v[232:235], v209 offset:37888
	ds_read_b128 v[236:239], v209 offset:38912
	ds_read_b128 v[240:243], v209 offset:39936
	global_load_lds_dwordx4 v[244:245], off
	v_lshl_add_u64 v[244:245], s[40:41], 0, v[180:181]
	s_mov_b32 m0, s49
	s_nop 0
	global_load_lds_dwordx4 v[244:245], off
	s_waitcnt vmcnt(8)
	s_waitcnt lgkmcnt(0)
	s_barrier
; #define PG8_STAGE(bufoff, gbase, voff) do { _Pragma("unroll") for (int _i = 0; _i < 2; ++_i) \
;         __builtin_amdgcn_global_load_lds((const unsigned*)((const char*)(gbase) + (voff)[_i]), (PG8_LAS unsigned*)(lds + (bufoff) + ldsw + _i * 8192), 16, 0, 0); } while (0)
; #define PG8_WAIT_V(n) asm volatile("s_waitcnt vmcnt(" #n ")" ::: "memory")
; #define PG8_WAIT_L(n) asm volatile("s_waitcnt lgkmcnt(" #n ")" ::: "memory")
; #define PG8_BAR __builtin_amdgcn_s_barrier()
; #define PG8_SCHED __builtin_amdgcn_sched_barrier(0)
; template <class Epi, class Sched, bool ALIGN_EPI = true, bool F8 = false>
; __device__ __forceinline__ void gemm_phase(PG8_LAS unsigned char* lds, const Sched& S, const Epi& E) {
;     ...
;             PG8_WAIT_V(8); PG8_WAIT_L(0); PG8_BAR; PG8_MMA(0, 0, At, B0); PG8_MMA(0, 1, At, B1); PG8_BAR; PG8_SCHED;
;             PG8_LDA(At, 1, 1); PG8_STAGE(PG8_SB(1, 0), b3, voffB[0]); PG8_STAGE(PG8_SB(1, 1), b3, voffB[1]); PG8_STAGE(PG8_SA(1, 0), a3, vA2[0]);
;             PG8_WAIT_V(8); PG8_WAIT_L(0); PG8_BAR; PG8_MMA(1, 0, At, B0); PG8_MMA(1, 1, At, B1); PG8_BAR; PG8_SCHED;
	s_setprio 2
	v_mfma_scale_f32_16x16x128_f8f6f4 v[158:161], v[2:9], v[212:219], v[158:161], v210, v210 op_sel_hi:[0,0,0]
	v_mfma_scale_f32_16x16x128_f8f6f4 v[154:157], v[10:17], v[212:219], v[154:157], v210, v210 op_sel_hi:[0,0,0]
	v_mfma_scale_f32_16x16x128_f8f6f4 v[142:145], v[2:9], v[220:227], v[142:145], v210, v210 op_sel_hi:[0,0,0]
	v_mfma_scale_f32_16x16x128_f8f6f4 v[138:141], v[10:17], v[220:227], v[138:141], v210, v210 op_sel_hi:[0,0,0]
	v_mfma_scale_f32_16x16x128_f8f6f4 v[126:129], v[2:9], v[228:235], v[126:129], v210, v210 op_sel_hi:[0,0,0]
	v_mfma_scale_f32_16x16x128_f8f6f4 v[122:125], v[10:17], v[228:235], v[122:125], v210, v210 op_sel_hi:[0,0,0]
	v_mfma_scale_f32_16x16x128_f8f6f4 v[110:113], v[2:9], v[236:243], v[110:113], v210, v210 op_sel_hi:[0,0,0]
	v_mfma_scale_f32_16x16x128_f8f6f4 v[106:109], v[10:17], v[236:243], v[106:109], v210, v210 op_sel_hi:[0,0,0]
	s_nop 3
	s_setprio 0
	s_setprio 2
	v_mfma_scale_f32_16x16x128_f8f6f4 v[150:153], v[18:25], v[212:219], v[150:153], v210, v210 op_sel_hi:[0,0,0]
	v_mfma_scale_f32_16x16x128_f8f6f4 v[146:149], v[26:33], v[212:219], v[146:149], v210, v210 op_sel_hi:[0,0,0]
	v_mfma_scale_f32_16x16x128_f8f6f4 v[134:137], v[18:25], v[220:227], v[134:137], v210, v210 op_sel_hi:[0,0,0]
	v_mfma_scale_f32_16x16x128_f8f6f4 v[130:133], v[26:33], v[220:227], v[130:133], v210, v210 op_sel_hi:[0,0,0]
	v_mfma_scale_f32_16x16x128_f8f6f4 v[118:121], v[18:25], v[228:235], v[118:121], v210, v210 op_sel_hi:[0,0,0]
	v_mfma_scale_f32_16x16x128_f8f6f4 v[114:117], v[26:33], v[228:235], v[114:117], v210, v210 op_sel_hi:[0,0,0]
	v_mfma_scale_f32_16x16x128_f8f6f4 v[102:105], v[18:25], v[236:243], v[102:105], v210, v210 op_sel_hi:[0,0,0]
	v_mfma_scale_f32_16x16x128_f8f6f4 v[98:101], v[26:33], v[236:243], v[98:101], v210, v210 op_sel_hi:[0,0,0]
	s_setprio 0
	s_add_u32 s30, s30, 0x8000
	s_addc_u32 s31, s31, 0
	s_add_i32 s40, s67, s45
	v_lshl_add_u64 v[244:245], s[30:31], 0, v[164:165]
	s_mov_b32 m0, s40
	ds_read_b128 v[212:215], v209 offset:49152
	ds_read_b128 v[216:219], v209 offset:50176
	ds_read_b128 v[220:223], v209 offset:51200
	ds_read_b128 v[224:227], v209 offset:52224
	ds_read_b128 v[228:231], v209 offset:53248
	ds_read_b128 v[232:235], v209 offset:54272
	ds_read_b128 v[236:239], v209 offset:55296
	ds_read_b128 v[240:243], v209 offset:56320
	global_load_lds_dwordx4 v[244:245], off
	v_lshl_add_u64 v[244:245], s[30:31], 0, v[166:167]
	s_add_i32 m0, s40, 0x2000
	s_add_i32 s40, s68, s45
	global_load_lds_dwordx4 v[244:245], off
	v_lshl_add_u64 v[244:245], s[30:31], 0, v[168:169]
	s_mov_b32 m0, s40
	s_nop 0
	global_load_lds_dwordx4 v[244:245], off
	v_lshl_add_u64 v[244:245], s[30:31], 0, v[172:173]
	s_add_i32 m0, s40, 0x2000
	s_nop 0
	global_load_lds_dwordx4 v[244:245], off
	v_lshl_add_u64 v[244:245], s[28:29], 0, v[174:175]
	s_mov_b32 m0, s52
	s_nop 0
	global_load_lds_dwordx4 v[244:245], off
	v_lshl_add_u64 v[244:245], s[28:29], 0, v[176:177]
	s_mov_b32 m0, s53
	s_nop 0
	global_load_lds_dwordx4 v[244:245], off
	s_waitcnt vmcnt(8)
	s_waitcnt lgkmcnt(0)
	s_barrier
	s_setprio 2
	v_mfma_scale_f32_16x16x128_f8f6f4 v[94:97], v[2:9], v[212:219], v[94:97], v210, v210 op_sel_hi:[0,0,0]
	v_mfma_scale_f32_16x16x128_f8f6f4 v[90:93], v[10:17], v[212:219], v[90:93], v210, v210 op_sel_hi:[0,0,0]
	v_mfma_scale_f32_16x16x128_f8f6f4 v[78:81], v[2:9], v[220:227], v[78:81], v210, v210 op_sel_hi:[0,0,0]
	v_mfma_scale_f32_16x16x128_f8f6f4 v[74:77], v[10:17], v[220:227], v[74:77], v210, v210 op_sel_hi:[0,0,0]
	v_mfma_scale_f32_16x16x128_f8f6f4 v[62:65], v[2:9], v[228:235], v[62:65], v210, v210 op_sel_hi:[0,0,0]
	v_mfma_scale_f32_16x16x128_f8f6f4 v[58:61], v[10:17], v[228:235], v[58:61], v210, v210 op_sel_hi:[0,0,0]
	v_mfma_scale_f32_16x16x128_f8f6f4 v[46:49], v[2:9], v[236:243], v[46:49], v210, v210 op_sel_hi:[0,0,0]
	v_mfma_scale_f32_16x16x128_f8f6f4 v[42:45], v[10:17], v[236:243], v[42:45], v210, v210 op_sel_hi:[0,0,0]
	s_nop 3
	s_setprio 0
	s_setprio 2
	v_mfma_scale_f32_16x16x128_f8f6f4 v[86:89], v[18:25], v[212:219], v[86:89], v210, v210 op_sel_hi:[0,0,0]
	v_mfma_scale_f32_16x16x128_f8f6f4 v[82:85], v[26:33], v[212:219], v[82:85], v210, v210 op_sel_hi:[0,0,0]
	v_mfma_scale_f32_16x16x128_f8f6f4 v[70:73], v[18:25], v[220:227], v[70:73], v210, v210 op_sel_hi:[0,0,0]
	v_mfma_scale_f32_16x16x128_f8f6f4 v[66:69], v[26:33], v[220:227], v[66:69], v210, v210 op_sel_hi:[0,0,0]
	v_mfma_scale_f32_16x16x128_f8f6f4 v[54:57], v[18:25], v[228:235], v[54:57], v210, v210 op_sel_hi:[0,0,0]
	v_mfma_scale_f32_16x16x128_f8f6f4 v[50:53], v[26:33], v[228:235], v[50:53], v210, v210 op_sel_hi:[0,0,0]
	v_mfma_scale_f32_16x16x128_f8f6f4 v[38:41], v[18:25], v[236:243], v[38:41], v210, v210 op_sel_hi:[0,0,0]
	v_mfma_scale_f32_16x16x128_f8f6f4 v[34:37], v[26:33], v[236:243], v[34:37], v210, v210 op_sel_hi:[0,0,0]
	s_setprio 0
	s_add_i32 s21, s21, 2
	s_add_u32 s5, s5, 0x10000
	s_addc_u32 s19, s19, 0
	s_add_u32 s26, s26, 0x10000
	s_addc_u32 s27, s27, 0
	s_cmp_gt_u32 s21, 13
	s_cbranch_scc0 .Lh1_372
	s_branch .Lfx_9967

; #define PG8_STAGE(bufoff, gbase, voff) do { _Pragma("unroll") for (int _i = 0; _i < 2; ++_i) \
;         __builtin_amdgcn_global_load_lds((const unsigned*)((const char*)(gbase) + (voff)[_i]), (PG8_LAS unsigned*)(lds + (bufoff) + ldsw + _i * 8192), 16, 0, 0); } while (0)
; #define PG8_WAIT_V(n) asm volatile("s_waitcnt vmcnt(" #n ")" ::: "memory")
; #define PG8_WAIT_L(n) asm volatile("s_waitcnt lgkmcnt(" #n ")" ::: "memory")
; #define PG8_BAR __builtin_amdgcn_s_barrier()
; #define PG8_SCHED __builtin_amdgcn_sched_barrier(0)
; template <class Epi, class Sched, bool ALIGN_EPI = true, bool F8 = false>
; __device__ __forceinline__ void gemm_phase(PG8_LAS unsigned char* lds, const Sched& S, const Epi& E) {
;     ...
;             PG8_LDB(B0, 0, 0); PG8_LDB(B1, 0, 1); PG8_SCHED; PG8_LDA(At, 0, 0); PG8_STAGE(PG8_SA(1, 1), a1, voffA[1]);
;             PG8_WAIT_V(8); PG8_WAIT_L(0); PG8_BAR; PG8_MMA(0, 0, At, B0); PG8_MMA(0, 1, At, B1); PG8_BAR; PG8_SCHED;
;             PG8_LDA(At, 0, 1); PG8_STAGE(PG8_SB(0, 0), b2, voffB[0]); PG8_STAGE(PG8_SB(0, 1), b2, voffB[1]); PG8_STAGE(PG8_SA(0, 0), a2, vA2[0]);
;             PG8_WAIT_V(8); PG8_WAIT_L(0); PG8_BAR; PG8_MMA(1, 0, At, B0); PG8_MMA(1, 1, At, B1); PG8_BAR; PG8_SCHED;
;     ...
;         for (int a = 0; a < 2; ++a)
; #pragma unroll
;             for (int b = 0; b < 2; ++b)
; #pragma unroll
;                 for (int m = 0; m < 4; ++m)
; #pragma unroll
;                     for (int n = 0; n < 2; ++n) acc[a][b][m][n] = (f32x4){0.f, 0.f, 0.f, 0.f};
.LBB0_427:
	s_add_u32 s17, s26, 0x10000
	s_addc_u32 s19, s27, 0
	s_add_u32 s24, s24, 0x8000
	s_addc_u32 s25, s25, 0
	s_mov_b32 s74, -2
	s_bitcmp1_b32 s3, 2
	s_cbranch_scc1 .Lh1e_11141
.Lpk0_428:
	ds_read_b128 v[18:21], v192
	ds_read_b128 v[22:25], v192 offset:1024
	ds_read_b128 v[26:29], v192 offset:2048
	ds_read_b128 v[30:33], v192 offset:3072
	ds_read_b128 v[2:5], v193
	ds_read_b128 v[6:9], v193 offset:1024
	ds_read_b128 v[10:13], v193 offset:2048
	ds_read_b128 v[14:17], v193 offset:3072
	s_add_u32 s26, s24, 0x8000
	s_addc_u32 s27, s25, 0
	s_cmp_eq_u32 s74, 12
	s_cselect_b32 s30, s20, s26
	s_cselect_b32 s31, s21, s27
	s_cselect_b32 s28, s22, s17
	s_cselect_b32 s29, s23, s19
	s_add_u32 s26, s30, 0x8000
	s_addc_u32 s27, s31, 0
	v_lshl_add_u64 v[230:231], s[24:25], 0, v[184:185]
	s_add_i32 m0, s48, 0xc000
	ds_read_b128 v[198:201], v194
	ds_read_b128 v[202:205], v194 offset:1024
	ds_read_b128 v[206:209], v194 offset:2048
	ds_read_b128 v[210:213], v194 offset:3072
	ds_read_b128 v[214:217], v194 offset:4096
	ds_read_b128 v[218:221], v194 offset:5120
	ds_read_b128 v[222:225], v194 offset:6144
	ds_read_b128 v[226:229], v194 offset:7168
	global_load_lds_dwordx4 v[230:231], off
	v_lshl_add_u64 v[230:231], s[24:25], 0, v[182:183]
	s_add_i32 m0, s48, 0xe000
	s_nop 0
	global_load_lds_dwordx4 v[230:231], off
	s_waitcnt vmcnt(8)
	s_waitcnt lgkmcnt(0)
	s_setprio 1
	v_mfma_scale_f32_16x16x128_f8f6f4 v[158:161], v[18:25], v[198:205], 0, v195, v195 op_sel_hi:[0,0,0]
	v_mfma_scale_f32_16x16x128_f8f6f4 v[154:157], v[26:33], v[198:205], 0, v195, v195 op_sel_hi:[0,0,0]
	v_mfma_scale_f32_16x16x128_f8f6f4 v[142:145], v[18:25], v[206:213], 0, v195, v195 op_sel_hi:[0,0,0]
	v_mfma_scale_f32_16x16x128_f8f6f4 v[138:141], v[26:33], v[206:213], 0, v195, v195 op_sel_hi:[0,0,0]
	v_mfma_scale_f32_16x16x128_f8f6f4 v[126:129], v[18:25], v[214:221], 0, v195, v195 op_sel_hi:[0,0,0]
	v_mfma_scale_f32_16x16x128_f8f6f4 v[122:125], v[26:33], v[214:221], 0, v195, v195 op_sel_hi:[0,0,0]
	v_mfma_scale_f32_16x16x128_f8f6f4 v[110:113], v[18:25], v[222:229], 0, v195, v195 op_sel_hi:[0,0,0]
	v_mfma_scale_f32_16x16x128_f8f6f4 v[106:109], v[26:33], v[222:229], 0, v195, v195 op_sel_hi:[0,0,0]
	s_nop 3
	s_setprio 0
	s_setprio 1
	v_mfma_scale_f32_16x16x128_f8f6f4 v[150:153], v[2:9], v[198:205], 0, v195, v195 op_sel_hi:[0,0,0]
	v_mfma_scale_f32_16x16x128_f8f6f4 v[146:149], v[10:17], v[198:205], 0, v195, v195 op_sel_hi:[0,0,0]
	v_mfma_scale_f32_16x16x128_f8f6f4 v[134:137], v[2:9], v[206:213], 0, v195, v195 op_sel_hi:[0,0,0]
	v_mfma_scale_f32_16x16x128_f8f6f4 v[130:133], v[10:17], v[206:213], 0, v195, v195 op_sel_hi:[0,0,0]
	v_mfma_scale_f32_16x16x128_f8f6f4 v[118:121], v[2:9], v[214:221], 0, v195, v195 op_sel_hi:[0,0,0]
	v_mfma_scale_f32_16x16x128_f8f6f4 v[114:117], v[10:17], v[214:221], 0, v195, v195 op_sel_hi:[0,0,0]
	v_mfma_scale_f32_16x16x128_f8f6f4 v[102:105], v[2:9], v[222:229], 0, v195, v195 op_sel_hi:[0,0,0]
	v_mfma_scale_f32_16x16x128_f8f6f4 v[98:101], v[10:17], v[222:229], 0, v195, v195 op_sel_hi:[0,0,0]
	s_setprio 0
	s_barrier
	s_add_i32 s75, s65, s47
	v_lshl_add_u64 v[230:231], s[28:29], 0, v[164:165]
	s_mov_b32 m0, s75
	ds_read_b128 v[198:201], v194 offset:16384
	ds_read_b128 v[202:205], v194 offset:17408
	ds_read_b128 v[206:209], v194 offset:18432
	ds_read_b128 v[210:213], v194 offset:19456
	ds_read_b128 v[214:217], v194 offset:20480
	ds_read_b128 v[218:221], v194 offset:21504
	ds_read_b128 v[222:225], v194 offset:22528
	ds_read_b128 v[226:229], v194 offset:23552
	global_load_lds_dwordx4 v[230:231], off
	v_lshl_add_u64 v[232:233], s[28:29], 0, v[166:167]
	s_add_i32 m0, s75, 0x2000
	s_add_i32 s75, s66, s47
	global_load_lds_dwordx4 v[232:233], off
	v_lshl_add_u64 v[230:231], v[230:231], 0, s[4:5]
	s_mov_b32 m0, s75
	s_nop 0
	global_load_lds_dwordx4 v[230:231], off
	v_lshl_add_u64 v[230:231], v[232:233], 0, s[4:5]
	s_add_i32 m0, s75, 0x2000
	s_nop 0
	global_load_lds_dwordx4 v[230:231], off
	v_lshl_add_u64 v[230:231], s[30:31], 0, v[174:175]
	s_mov_b32 m0, s48
	s_nop 0
	global_load_lds_dwordx4 v[230:231], off
	v_lshl_add_u64 v[230:231], s[30:31], 0, v[176:177]
	s_mov_b32 m0, s49
	s_nop 0
	global_load_lds_dwordx4 v[230:231], off
	s_waitcnt vmcnt(8)
	s_waitcnt lgkmcnt(0)
	s_setprio 1
	v_mfma_scale_f32_16x16x128_f8f6f4 v[94:97], v[18:25], v[198:205], 0, v195, v195 op_sel_hi:[0,0,0]
	v_mfma_scale_f32_16x16x128_f8f6f4 v[90:93], v[26:33], v[198:205], 0, v195, v195 op_sel_hi:[0,0,0]
	v_mfma_scale_f32_16x16x128_f8f6f4 v[78:81], v[18:25], v[206:213], 0, v195, v195 op_sel_hi:[0,0,0]
	v_mfma_scale_f32_16x16x128_f8f6f4 v[74:77], v[26:33], v[206:213], 0, v195, v195 op_sel_hi:[0,0,0]
	v_mfma_scale_f32_16x16x128_f8f6f4 v[62:65], v[18:25], v[214:221], 0, v195, v195 op_sel_hi:[0,0,0]
	v_mfma_scale_f32_16x16x128_f8f6f4 v[58:61], v[26:33], v[214:221], 0, v195, v195 op_sel_hi:[0,0,0]
	v_mfma_scale_f32_16x16x128_f8f6f4 v[46:49], v[18:25], v[222:229], 0, v195, v195 op_sel_hi:[0,0,0]
	v_mfma_scale_f32_16x16x128_f8f6f4 v[42:45], v[26:33], v[222:229], 0, v195, v195 op_sel_hi:[0,0,0]
	s_nop 3
	s_setprio 0
	s_setprio 1
	v_mfma_scale_f32_16x16x128_f8f6f4 v[86:89], v[2:9], v[198:205], 0, v195, v195 op_sel_hi:[0,0,0]
	v_mfma_scale_f32_16x16x128_f8f6f4 v[82:85], v[10:17], v[198:205], 0, v195, v195 op_sel_hi:[0,0,0]
	v_mfma_scale_f32_16x16x128_f8f6f4 v[70:73], v[2:9], v[206:213], 0, v195, v195 op_sel_hi:[0,0,0]
	v_mfma_scale_f32_16x16x128_f8f6f4 v[66:69], v[10:17], v[206:213], 0, v195, v195 op_sel_hi:[0,0,0]
	v_mfma_scale_f32_16x16x128_f8f6f4 v[54:57], v[2:9], v[214:221], 0, v195, v195 op_sel_hi:[0,0,0]
	v_mfma_scale_f32_16x16x128_f8f6f4 v[50:53], v[10:17], v[214:221], 0, v195, v195 op_sel_hi:[0,0,0]
	v_mfma_scale_f32_16x16x128_f8f6f4 v[38:41], v[2:9], v[222:229], 0, v195, v195 op_sel_hi:[0,0,0]
	v_mfma_scale_f32_16x16x128_f8f6f4 v[34:37], v[10:17], v[222:229], 0, v195, v195 op_sel_hi:[0,0,0]
	s_setprio 0
	s_barrier
; #define PG8_STAGE(bufoff, gbase, voff) do { _Pragma("unroll") for (int _i = 0; _i < 2; ++_i) \
;         __builtin_amdgcn_global_load_lds((const unsigned*)((const char*)(gbase) + (voff)[_i]), (PG8_LAS unsigned*)(lds + (bufoff) + ldsw + _i * 8192), 16, 0, 0); } while (0)
; #define PG8_WAIT_V(n) asm volatile("s_waitcnt vmcnt(" #n ")" ::: "memory")
; #define PG8_WAIT_L(n) asm volatile("s_waitcnt lgkmcnt(" #n ")" ::: "memory")
; #define PG8_BAR __builtin_amdgcn_s_barrier()
; #define PG8_SCHED __builtin_amdgcn_sched_barrier(0)
; template <class Epi, class Sched, bool ALIGN_EPI = true, bool F8 = false>
; __device__ __forceinline__ void gemm_phase(PG8_LAS unsigned char* lds, const Sched& S, const Epi& E) {
;     ...
;             PG8_LDB(B0, 1, 0); PG8_LDB(B1, 1, 1); PG8_SCHED; PG8_LDA(At, 1, 0); PG8_STAGE(PG8_SA(0, 1), a2, vA2[1]);
;             PG8_WAIT_V(8); PG8_WAIT_L(0); PG8_BAR; PG8_MMA(0, 0, At, B0); PG8_MMA(0, 1, At, B1); PG8_BAR; PG8_SCHED;
;             PG8_LDA(At, 1, 1); PG8_STAGE(PG8_SB(1, 0), b3, voffB[0]); PG8_STAGE(PG8_SB(1, 1), b3, voffB[1]); PG8_STAGE(PG8_SA(1, 0), a3, vA2[0]);
;             PG8_WAIT_V(8); PG8_WAIT_L(0); PG8_BAR; PG8_MMA(1, 0, At, B0); PG8_MMA(1, 1, At, B1); PG8_BAR; PG8_SCHED;
	s_add_i32 s75, 0, 0x18000
	s_add_i32 s76, 0, 0x1c000
	v_add_u32_e32 v14, s75, v191
	v_add_u32_e32 v30, s76, v191
	ds_read_b128 v[2:5], v14
	ds_read_b128 v[6:9], v14 offset:1024
	ds_read_b128 v[10:13], v14 offset:2048
	ds_read_b128 v[14:17], v14 offset:3072
	ds_read_b128 v[18:21], v30
	ds_read_b128 v[22:25], v30 offset:1024
	ds_read_b128 v[26:29], v30 offset:2048
	ds_read_b128 v[30:33], v30 offset:3072
	s_mov_b32 m0, s50
	v_lshl_add_u64 v[230:231], s[30:31], 0, v[178:179]
	ds_read_b128 v[198:201], v194 offset:32768
	ds_read_b128 v[202:205], v194 offset:33792
	ds_read_b128 v[206:209], v194 offset:34816
	ds_read_b128 v[210:213], v194 offset:35840
	ds_read_b128 v[214:217], v194 offset:36864
	ds_read_b128 v[218:221], v194 offset:37888
	ds_read_b128 v[222:225], v194 offset:38912
	ds_read_b128 v[226:229], v194 offset:39936
	global_load_lds_dwordx4 v[230:231], off
	v_lshl_add_u64 v[230:231], s[30:31], 0, v[180:181]
	s_mov_b32 m0, s51
	s_nop 0
	global_load_lds_dwordx4 v[230:231], off
	s_waitcnt vmcnt(8)
	s_waitcnt lgkmcnt(0)
	s_setprio 1
	v_mfma_scale_f32_16x16x128_f8f6f4 v[158:161], v[2:9], v[198:205], v[158:161], v195, v195 op_sel_hi:[0,0,0]
	v_mfma_scale_f32_16x16x128_f8f6f4 v[154:157], v[10:17], v[198:205], v[154:157], v195, v195 op_sel_hi:[0,0,0]
	v_mfma_scale_f32_16x16x128_f8f6f4 v[142:145], v[2:9], v[206:213], v[142:145], v195, v195 op_sel_hi:[0,0,0]
	v_mfma_scale_f32_16x16x128_f8f6f4 v[138:141], v[10:17], v[206:213], v[138:141], v195, v195 op_sel_hi:[0,0,0]
	v_mfma_scale_f32_16x16x128_f8f6f4 v[126:129], v[2:9], v[214:221], v[126:129], v195, v195 op_sel_hi:[0,0,0]
	v_mfma_scale_f32_16x16x128_f8f6f4 v[122:125], v[10:17], v[214:221], v[122:125], v195, v195 op_sel_hi:[0,0,0]
	v_mfma_scale_f32_16x16x128_f8f6f4 v[110:113], v[2:9], v[222:229], v[110:113], v195, v195 op_sel_hi:[0,0,0]
	v_mfma_scale_f32_16x16x128_f8f6f4 v[106:109], v[10:17], v[222:229], v[106:109], v195, v195 op_sel_hi:[0,0,0]
	s_nop 3
	s_setprio 0
	s_setprio 1
	v_mfma_scale_f32_16x16x128_f8f6f4 v[150:153], v[18:25], v[198:205], v[150:153], v195, v195 op_sel_hi:[0,0,0]
	v_mfma_scale_f32_16x16x128_f8f6f4 v[146:149], v[26:33], v[198:205], v[146:149], v195, v195 op_sel_hi:[0,0,0]
	v_mfma_scale_f32_16x16x128_f8f6f4 v[134:137], v[18:25], v[206:213], v[134:137], v195, v195 op_sel_hi:[0,0,0]
	v_mfma_scale_f32_16x16x128_f8f6f4 v[130:133], v[26:33], v[206:213], v[130:133], v195, v195 op_sel_hi:[0,0,0]
	v_mfma_scale_f32_16x16x128_f8f6f4 v[118:121], v[18:25], v[214:221], v[118:121], v195, v195 op_sel_hi:[0,0,0]
	v_mfma_scale_f32_16x16x128_f8f6f4 v[114:117], v[26:33], v[214:221], v[114:117], v195, v195 op_sel_hi:[0,0,0]
	v_mfma_scale_f32_16x16x128_f8f6f4 v[102:105], v[18:25], v[222:229], v[102:105], v195, v195 op_sel_hi:[0,0,0]
	v_mfma_scale_f32_16x16x128_f8f6f4 v[98:101], v[26:33], v[222:229], v[98:101], v195, v195 op_sel_hi:[0,0,0]
	s_setprio 0
	s_barrier
	s_add_u32 s28, s28, 0x8000
	s_addc_u32 s29, s29, 0
	s_add_i32 s30, s75, s47
	v_lshl_add_u64 v[230:231], s[28:29], 0, v[164:165]
	s_mov_b32 m0, s30
	ds_read_b128 v[198:201], v194 offset:49152
	ds_read_b128 v[202:205], v194 offset:50176
	ds_read_b128 v[206:209], v194 offset:51200
	ds_read_b128 v[210:213], v194 offset:52224
	ds_read_b128 v[214:217], v194 offset:53248
	ds_read_b128 v[218:221], v194 offset:54272
	ds_read_b128 v[222:225], v194 offset:55296
	ds_read_b128 v[226:229], v194 offset:56320
	global_load_lds_dwordx4 v[230:231], off
	v_lshl_add_u64 v[230:231], s[28:29], 0, v[166:167]
	s_add_i32 m0, s30, 0x2000
	s_add_i32 s30, s76, s47
	global_load_lds_dwordx4 v[230:231], off
	v_lshl_add_u64 v[230:231], s[28:29], 0, v[168:169]
	s_mov_b32 m0, s30
	s_nop 0
	global_load_lds_dwordx4 v[230:231], off
	v_lshl_add_u64 v[230:231], s[28:29], 0, v[172:173]
	s_add_i32 m0, s30, 0x2000
	s_nop 0
	global_load_lds_dwordx4 v[230:231], off
	v_lshl_add_u64 v[230:231], s[26:27], 0, v[174:175]
	s_mov_b32 m0, s60
	s_nop 0
	global_load_lds_dwordx4 v[230:231], off
	v_lshl_add_u64 v[230:231], s[26:27], 0, v[176:177]
	s_mov_b32 m0, s61
	s_nop 0
	global_load_lds_dwordx4 v[230:231], off
	s_waitcnt vmcnt(8)
	s_waitcnt lgkmcnt(0)
	s_setprio 1
	v_mfma_scale_f32_16x16x128_f8f6f4 v[94:97], v[2:9], v[198:205], v[94:97], v195, v195 op_sel_hi:[0,0,0]
	v_mfma_scale_f32_16x16x128_f8f6f4 v[90:93], v[10:17], v[198:205], v[90:93], v195, v195 op_sel_hi:[0,0,0]
	v_mfma_scale_f32_16x16x128_f8f6f4 v[78:81], v[2:9], v[206:213], v[78:81], v195, v195 op_sel_hi:[0,0,0]
	v_mfma_scale_f32_16x16x128_f8f6f4 v[74:77], v[10:17], v[206:213], v[74:77], v195, v195 op_sel_hi:[0,0,0]
	v_mfma_scale_f32_16x16x128_f8f6f4 v[62:65], v[2:9], v[214:221], v[62:65], v195, v195 op_sel_hi:[0,0,0]
	v_mfma_scale_f32_16x16x128_f8f6f4 v[58:61], v[10:17], v[214:221], v[58:61], v195, v195 op_sel_hi:[0,0,0]
	v_mfma_scale_f32_16x16x128_f8f6f4 v[46:49], v[2:9], v[222:229], v[46:49], v195, v195 op_sel_hi:[0,0,0]
	v_mfma_scale_f32_16x16x128_f8f6f4 v[42:45], v[10:17], v[222:229], v[42:45], v195, v195 op_sel_hi:[0,0,0]
	s_nop 3
	s_setprio 0
	s_setprio 1
	v_mfma_scale_f32_16x16x128_f8f6f4 v[86:89], v[18:25], v[198:205], v[86:89], v195, v195 op_sel_hi:[0,0,0]
	v_mfma_scale_f32_16x16x128_f8f6f4 v[82:85], v[26:33], v[198:205], v[82:85], v195, v195 op_sel_hi:[0,0,0]
	v_mfma_scale_f32_16x16x128_f8f6f4 v[70:73], v[18:25], v[206:213], v[70:73], v195, v195 op_sel_hi:[0,0,0]
	v_mfma_scale_f32_16x16x128_f8f6f4 v[66:69], v[26:33], v[206:213], v[66:69], v195, v195 op_sel_hi:[0,0,0]
	v_mfma_scale_f32_16x16x128_f8f6f4 v[54:57], v[18:25], v[214:221], v[54:57], v195, v195 op_sel_hi:[0,0,0]
	v_mfma_scale_f32_16x16x128_f8f6f4 v[50:53], v[26:33], v[214:221], v[50:53], v195, v195 op_sel_hi:[0,0,0]
	v_mfma_scale_f32_16x16x128_f8f6f4 v[38:41], v[18:25], v[222:229], v[38:41], v195, v195 op_sel_hi:[0,0,0]
	v_mfma_scale_f32_16x16x128_f8f6f4 v[34:37], v[26:33], v[222:229], v[34:37], v195, v195 op_sel_hi:[0,0,0]
	s_setprio 0
	s_barrier
	s_add_i32 s74, s74, 2
	s_add_u32 s17, s17, 0x10000
	s_addc_u32 s19, s19, 0
	s_add_u32 s24, s24, 0x10000
	s_addc_u32 s25, s25, 0
	s_cmp_gt_u32 s74, 13
	s_cbranch_scc0 .LBB0_428
	s_branch .Lfx_11141

; #define PG8_STAGE(bufoff, gbase, voff) do { _Pragma("unroll") for (int _i = 0; _i < 2; ++_i) \
;         __builtin_amdgcn_global_load_lds((const unsigned*)((const char*)(gbase) + (voff)[_i]), (PG8_LAS unsigned*)(lds + (bufoff) + ldsw + _i * 8192), 16, 0, 0); } while (0)
; #define PG8_WAIT_V(n) asm volatile("s_waitcnt vmcnt(" #n ")" ::: "memory")
; #define PG8_WAIT_L(n) asm volatile("s_waitcnt lgkmcnt(" #n ")" ::: "memory")
; #define PG8_BAR __builtin_amdgcn_s_barrier()
; #define PG8_SCHED __builtin_amdgcn_sched_barrier(0)
; template <class Epi, class Sched, bool ALIGN_EPI = true, bool F8 = false>
; __device__ __forceinline__ void gemm_phase(PG8_LAS unsigned char* lds, const Sched& S, const Epi& E) {
;     ...
;             PG8_LDB(B0, 0, 0); PG8_LDB(B1, 0, 1); PG8_SCHED; PG8_LDA(At, 0, 0); PG8_STAGE(PG8_SA(1, 1), a1, voffA[1]);
;             PG8_WAIT_V(8); PG8_WAIT_L(0); PG8_BAR; PG8_MMA(0, 0, At, B0); PG8_MMA(0, 1, At, B1); PG8_BAR; PG8_SCHED;
;             PG8_LDA(At, 0, 1); PG8_STAGE(PG8_SB(0, 0), b2, voffB[0]); PG8_STAGE(PG8_SB(0, 1), b2, voffB[1]); PG8_STAGE(PG8_SA(0, 0), a2, vA2[0]);
;             PG8_WAIT_V(8); PG8_WAIT_L(0); PG8_BAR; PG8_MMA(1, 0, At, B0); PG8_MMA(1, 1, At, B1); PG8_BAR; PG8_SCHED;
;             PG8_LDB(B0, 1, 0); PG8_LDB(B1, 1, 1); PG8_SCHED; PG8_LDA(At, 1, 0); PG8_STAGE(PG8_SA(0, 1), a2, vA2[1]);
;             PG8_WAIT_V(8); PG8_WAIT_L(0); PG8_BAR; PG8_MMA(0, 0, At, B0); PG8_MMA(0, 1, At, B1); PG8_BAR; PG8_SCHED;
.Lh1e_11141:
.Lpk1_428:
	ds_read_b128 v[18:21], v192
	ds_read_b128 v[22:25], v192 offset:1024
	ds_read_b128 v[26:29], v192 offset:2048
	ds_read_b128 v[30:33], v192 offset:3072
	ds_read_b128 v[2:5], v193
	ds_read_b128 v[6:9], v193 offset:1024
	ds_read_b128 v[10:13], v193 offset:2048
	ds_read_b128 v[14:17], v193 offset:3072
	s_add_u32 s26, s24, 0x8000
	s_addc_u32 s27, s25, 0
	s_cmp_eq_u32 s74, 12
	s_cselect_b32 s30, s20, s26
	s_cselect_b32 s31, s21, s27
	s_cselect_b32 s28, s22, s17
	s_cselect_b32 s29, s23, s19
	s_add_u32 s26, s30, 0x8000
	s_addc_u32 s27, s31, 0
	v_lshl_add_u64 v[230:231], s[24:25], 0, v[184:185]
	s_add_i32 m0, s48, 0xc000
	ds_read_b128 v[198:201], v194
	ds_read_b128 v[202:205], v194 offset:1024
	ds_read_b128 v[206:209], v194 offset:2048
	ds_read_b128 v[210:213], v194 offset:3072
	ds_read_b128 v[214:217], v194 offset:4096
	ds_read_b128 v[218:221], v194 offset:5120
	ds_read_b128 v[222:225], v194 offset:6144
	ds_read_b128 v[226:229], v194 offset:7168
	global_load_lds_dwordx4 v[230:231], off
	v_lshl_add_u64 v[230:231], s[24:25], 0, v[182:183]
	s_add_i32 m0, s48, 0xe000
	s_nop 0
	global_load_lds_dwordx4 v[230:231], off
	s_waitcnt vmcnt(8)
	s_waitcnt lgkmcnt(0)
	s_barrier
	s_setprio 2
	v_mfma_scale_f32_16x16x128_f8f6f4 v[158:161], v[18:25], v[198:205], 0, v195, v195 op_sel_hi:[0,0,0]
	v_mfma_scale_f32_16x16x128_f8f6f4 v[154:157], v[26:33], v[198:205], 0, v195, v195 op_sel_hi:[0,0,0]
	v_mfma_scale_f32_16x16x128_f8f6f4 v[142:145], v[18:25], v[206:213], 0, v195, v195 op_sel_hi:[0,0,0]
	v_mfma_scale_f32_16x16x128_f8f6f4 v[138:141], v[26:33], v[206:213], 0, v195, v195 op_sel_hi:[0,0,0]
	v_mfma_scale_f32_16x16x128_f8f6f4 v[126:129], v[18:25], v[214:221], 0, v195, v195 op_sel_hi:[0,0,0]
	v_mfma_scale_f32_16x16x128_f8f6f4 v[122:125], v[26:33], v[214:221], 0, v195, v195 op_sel_hi:[0,0,0]
	v_mfma_scale_f32_16x16x128_f8f6f4 v[110:113], v[18:25], v[222:229], 0, v195, v195 op_sel_hi:[0,0,0]
	v_mfma_scale_f32_16x16x128_f8f6f4 v[106:109], v[26:33], v[222:229], 0, v195, v195 op_sel_hi:[0,0,0]
	s_nop 3
	s_setprio 0
	s_setprio 2
	v_mfma_scale_f32_16x16x128_f8f6f4 v[150:153], v[2:9], v[198:205], 0, v195, v195 op_sel_hi:[0,0,0]
	v_mfma_scale_f32_16x16x128_f8f6f4 v[146:149], v[10:17], v[198:205], 0, v195, v195 op_sel_hi:[0,0,0]
	v_mfma_scale_f32_16x16x128_f8f6f4 v[134:137], v[2:9], v[206:213], 0, v195, v195 op_sel_hi:[0,0,0]
	v_mfma_scale_f32_16x16x128_f8f6f4 v[130:133], v[10:17], v[206:213], 0, v195, v195 op_sel_hi:[0,0,0]
	v_mfma_scale_f32_16x16x128_f8f6f4 v[118:121], v[2:9], v[214:221], 0, v195, v195 op_sel_hi:[0,0,0]
	v_mfma_scale_f32_16x16x128_f8f6f4 v[114:117], v[10:17], v[214:221], 0, v195, v195 op_sel_hi:[0,0,0]
	v_mfma_scale_f32_16x16x128_f8f6f4 v[102:105], v[2:9], v[222:229], 0, v195, v195 op_sel_hi:[0,0,0]
	v_mfma_scale_f32_16x16x128_f8f6f4 v[98:101], v[10:17], v[222:229], 0, v195, v195 op_sel_hi:[0,0,0]
	s_setprio 0
	s_add_i32 s75, s65, s47
	v_lshl_add_u64 v[230:231], s[28:29], 0, v[164:165]
	s_mov_b32 m0, s75
	ds_read_b128 v[198:201], v194 offset:16384
	ds_read_b128 v[202:205], v194 offset:17408
	ds_read_b128 v[206:209], v194 offset:18432
	ds_read_b128 v[210:213], v194 offset:19456
	ds_read_b128 v[214:217], v194 offset:20480
	ds_read_b128 v[218:221], v194 offset:21504
	ds_read_b128 v[222:225], v194 offset:22528
	ds_read_b128 v[226:229], v194 offset:23552
	global_load_lds_dwordx4 v[230:231], off
	v_lshl_add_u64 v[232:233], s[28:29], 0, v[166:167]
	s_add_i32 m0, s75, 0x2000
	s_add_i32 s75, s66, s47
	global_load_lds_dwordx4 v[232:233], off
	v_lshl_add_u64 v[230:231], v[230:231], 0, s[4:5]
	s_mov_b32 m0, s75
	s_nop 0
	global_load_lds_dwordx4 v[230:231], off
	v_lshl_add_u64 v[230:231], v[232:233], 0, s[4:5]
	s_add_i32 m0, s75, 0x2000
	s_nop 0
	global_load_lds_dwordx4 v[230:231], off
	v_lshl_add_u64 v[230:231], s[30:31], 0, v[174:175]
	s_mov_b32 m0, s48
	s_nop 0
	global_load_lds_dwordx4 v[230:231], off
	v_lshl_add_u64 v[230:231], s[30:31], 0, v[176:177]
	s_mov_b32 m0, s49
	s_nop 0
	global_load_lds_dwordx4 v[230:231], off
	s_waitcnt vmcnt(8)
	s_waitcnt lgkmcnt(0)
	s_barrier
	s_setprio 2
	v_mfma_scale_f32_16x16x128_f8f6f4 v[94:97], v[18:25], v[198:205], 0, v195, v195 op_sel_hi:[0,0,0]
	v_mfma_scale_f32_16x16x128_f8f6f4 v[90:93], v[26:33], v[198:205], 0, v195, v195 op_sel_hi:[0,0,0]
	v_mfma_scale_f32_16x16x128_f8f6f4 v[78:81], v[18:25], v[206:213], 0, v195, v195 op_sel_hi:[0,0,0]
	v_mfma_scale_f32_16x16x128_f8f6f4 v[74:77], v[26:33], v[206:213], 0, v195, v195 op_sel_hi:[0,0,0]
	v_mfma_scale_f32_16x16x128_f8f6f4 v[62:65], v[18:25], v[214:221], 0, v195, v195 op_sel_hi:[0,0,0]
	v_mfma_scale_f32_16x16x128_f8f6f4 v[58:61], v[26:33], v[214:221], 0, v195, v195 op_sel_hi:[0,0,0]
	v_mfma_scale_f32_16x16x128_f8f6f4 v[46:49], v[18:25], v[222:229], 0, v195, v195 op_sel_hi:[0,0,0]
	v_mfma_scale_f32_16x16x128_f8f6f4 v[42:45], v[26:33], v[222:229], 0, v195, v195 op_sel_hi:[0,0,0]
	s_nop 3
	s_setprio 0
	s_setprio 2
	v_mfma_scale_f32_16x16x128_f8f6f4 v[86:89], v[2:9], v[198:205], 0, v195, v195 op_sel_hi:[0,0,0]
	v_mfma_scale_f32_16x16x128_f8f6f4 v[82:85], v[10:17], v[198:205], 0, v195, v195 op_sel_hi:[0,0,0]
	v_mfma_scale_f32_16x16x128_f8f6f4 v[70:73], v[2:9], v[206:213], 0, v195, v195 op_sel_hi:[0,0,0]
	v_mfma_scale_f32_16x16x128_f8f6f4 v[66:69], v[10:17], v[206:213], 0, v195, v195 op_sel_hi:[0,0,0]
	v_mfma_scale_f32_16x16x128_f8f6f4 v[54:57], v[2:9], v[214:221], 0, v195, v195 op_sel_hi:[0,0,0]
	v_mfma_scale_f32_16x16x128_f8f6f4 v[50:53], v[10:17], v[214:221], 0, v195, v195 op_sel_hi:[0,0,0]
	v_mfma_scale_f32_16x16x128_f8f6f4 v[38:41], v[2:9], v[222:229], 0, v195, v195 op_sel_hi:[0,0,0]
	v_mfma_scale_f32_16x16x128_f8f6f4 v[34:37], v[10:17], v[222:229], 0, v195, v195 op_sel_hi:[0,0,0]
	s_setprio 0
	s_add_i32 s75, 0, 0x18000
	s_add_i32 s76, 0, 0x1c000
	v_add_u32_e32 v14, s75, v191
	v_add_u32_e32 v30, s76, v191
	ds_read_b128 v[2:5], v14
	ds_read_b128 v[6:9], v14 offset:1024
	ds_read_b128 v[10:13], v14 offset:2048
	ds_read_b128 v[14:17], v14 offset:3072
	ds_read_b128 v[18:21], v30
	ds_read_b128 v[22:25], v30 offset:1024
	ds_read_b128 v[26:29], v30 offset:2048
	ds_read_b128 v[30:33], v30 offset:3072
	s_mov_b32 m0, s50
	v_lshl_add_u64 v[230:231], s[30:31], 0, v[178:179]
	ds_read_b128 v[198:201], v194 offset:32768
	ds_read_b128 v[202:205], v194 offset:33792
	ds_read_b128 v[206:209], v194 offset:34816
	ds_read_b128 v[210:213], v194 offset:35840
	ds_read_b128 v[214:217], v194 offset:36864
	ds_read_b128 v[218:221], v194 offset:37888
	ds_read_b128 v[222:225], v194 offset:38912
	ds_read_b128 v[226:229], v194 offset:39936
	global_load_lds_dwordx4 v[230:231], off
	v_lshl_add_u64 v[230:231], s[30:31], 0, v[180:181]
	s_mov_b32 m0, s51
	s_nop 0
	global_load_lds_dwordx4 v[230:231], off
	s_waitcnt vmcnt(8)
	s_waitcnt lgkmcnt(0)
	s_barrier
; #define PG8_STAGE(bufoff, gbase, voff) do { _Pragma("unroll") for (int _i = 0; _i < 2; ++_i) \
;         __builtin_amdgcn_global_load_lds((const unsigned*)((const char*)(gbase) + (voff)[_i]), (PG8_LAS unsigned*)(lds + (bufoff) + ldsw + _i * 8192), 16, 0, 0); } while (0)
; #define PG8_WAIT_V(n) asm volatile("s_waitcnt vmcnt(" #n ")" ::: "memory")
; #define PG8_WAIT_L(n) asm volatile("s_waitcnt lgkmcnt(" #n ")" ::: "memory")
; #define PG8_BAR __builtin_amdgcn_s_barrier()
; #define PG8_SCHED __builtin_amdgcn_sched_barrier(0)
; template <class Epi, class Sched, bool ALIGN_EPI = true, bool F8 = false>
; __device__ __forceinline__ void gemm_phase(PG8_LAS unsigned char* lds, const Sched& S, const Epi& E) {
;     ...
;             PG8_WAIT_V(8); PG8_WAIT_L(0); PG8_BAR; PG8_MMA(0, 0, At, B0); PG8_MMA(0, 1, At, B1); PG8_BAR; PG8_SCHED;
;             PG8_LDA(At, 1, 1); PG8_STAGE(PG8_SB(1, 0), b3, voffB[0]); PG8_STAGE(PG8_SB(1, 1), b3, voffB[1]); PG8_STAGE(PG8_SA(1, 0), a3, vA2[0]);
;             PG8_WAIT_V(8); PG8_WAIT_L(0); PG8_BAR; PG8_MMA(1, 0, At, B0); PG8_MMA(1, 1, At, B1); PG8_BAR; PG8_SCHED;
	s_setprio 2
	v_mfma_scale_f32_16x16x128_f8f6f4 v[158:161], v[2:9], v[198:205], v[158:161], v195, v195 op_sel_hi:[0,0,0]
	v_mfma_scale_f32_16x16x128_f8f6f4 v[154:157], v[10:17], v[198:205], v[154:157], v195, v195 op_sel_hi:[0,0,0]
	v_mfma_scale_f32_16x16x128_f8f6f4 v[142:145], v[2:9], v[206:213], v[142:145], v195, v195 op_sel_hi:[0,0,0]
	v_mfma_scale_f32_16x16x128_f8f6f4 v[138:141], v[10:17], v[206:213], v[138:141], v195, v195 op_sel_hi:[0,0,0]
	v_mfma_scale_f32_16x16x128_f8f6f4 v[126:129], v[2:9], v[214:221], v[126:129], v195, v195 op_sel_hi:[0,0,0]
	v_mfma_scale_f32_16x16x128_f8f6f4 v[122:125], v[10:17], v[214:221], v[122:125], v195, v195 op_sel_hi:[0,0,0]
	v_mfma_scale_f32_16x16x128_f8f6f4 v[110:113], v[2:9], v[222:229], v[110:113], v195, v195 op_sel_hi:[0,0,0]
	v_mfma_scale_f32_16x16x128_f8f6f4 v[106:109], v[10:17], v[222:229], v[106:109], v195, v195 op_sel_hi:[0,0,0]
	s_nop 3
	s_setprio 0
	s_setprio 2
	v_mfma_scale_f32_16x16x128_f8f6f4 v[150:153], v[18:25], v[198:205], v[150:153], v195, v195 op_sel_hi:[0,0,0]
	v_mfma_scale_f32_16x16x128_f8f6f4 v[146:149], v[26:33], v[198:205], v[146:149], v195, v195 op_sel_hi:[0,0,0]
	v_mfma_scale_f32_16x16x128_f8f6f4 v[134:137], v[18:25], v[206:213], v[134:137], v195, v195 op_sel_hi:[0,0,0]
	v_mfma_scale_f32_16x16x128_f8f6f4 v[130:133], v[26:33], v[206:213], v[130:133], v195, v195 op_sel_hi:[0,0,0]
	v_mfma_scale_f32_16x16x128_f8f6f4 v[118:121], v[18:25], v[214:221], v[118:121], v195, v195 op_sel_hi:[0,0,0]
	v_mfma_scale_f32_16x16x128_f8f6f4 v[114:117], v[26:33], v[214:221], v[114:117], v195, v195 op_sel_hi:[0,0,0]
	v_mfma_scale_f32_16x16x128_f8f6f4 v[102:105], v[18:25], v[222:229], v[102:105], v195, v195 op_sel_hi:[0,0,0]
	v_mfma_scale_f32_16x16x128_f8f6f4 v[98:101], v[26:33], v[222:229], v[98:101], v195, v195 op_sel_hi:[0,0,0]
	s_setprio 0
	s_add_u32 s28, s28, 0x8000
	s_addc_u32 s29, s29, 0
	s_add_i32 s30, s75, s47
	v_lshl_add_u64 v[230:231], s[28:29], 0, v[164:165]
	s_mov_b32 m0, s30
	ds_read_b128 v[198:201], v194 offset:49152
	ds_read_b128 v[202:205], v194 offset:50176
	ds_read_b128 v[206:209], v194 offset:51200
	ds_read_b128 v[210:213], v194 offset:52224
	ds_read_b128 v[214:217], v194 offset:53248
	ds_read_b128 v[218:221], v194 offset:54272
	ds_read_b128 v[222:225], v194 offset:55296
	ds_read_b128 v[226:229], v194 offset:56320
	global_load_lds_dwordx4 v[230:231], off
	v_lshl_add_u64 v[230:231], s[28:29], 0, v[166:167]
	s_add_i32 m0, s30, 0x2000
	s_add_i32 s30, s76, s47
	global_load_lds_dwordx4 v[230:231], off
	v_lshl_add_u64 v[230:231], s[28:29], 0, v[168:169]
	s_mov_b32 m0, s30
	s_nop 0
	global_load_lds_dwordx4 v[230:231], off
	v_lshl_add_u64 v[230:231], s[28:29], 0, v[172:173]
	s_add_i32 m0, s30, 0x2000
	s_nop 0
	global_load_lds_dwordx4 v[230:231], off
	v_lshl_add_u64 v[230:231], s[26:27], 0, v[174:175]
	s_mov_b32 m0, s60
	s_nop 0
	global_load_lds_dwordx4 v[230:231], off
	v_lshl_add_u64 v[230:231], s[26:27], 0, v[176:177]
	s_mov_b32 m0, s61
	s_nop 0
	global_load_lds_dwordx4 v[230:231], off
	s_waitcnt vmcnt(8)
	s_waitcnt lgkmcnt(0)
	s_barrier
	s_setprio 2
	v_mfma_scale_f32_16x16x128_f8f6f4 v[94:97], v[2:9], v[198:205], v[94:97], v195, v195 op_sel_hi:[0,0,0]
	v_mfma_scale_f32_16x16x128_f8f6f4 v[90:93], v[10:17], v[198:205], v[90:93], v195, v195 op_sel_hi:[0,0,0]
	v_mfma_scale_f32_16x16x128_f8f6f4 v[78:81], v[2:9], v[206:213], v[78:81], v195, v195 op_sel_hi:[0,0,0]
	v_mfma_scale_f32_16x16x128_f8f6f4 v[74:77], v[10:17], v[206:213], v[74:77], v195, v195 op_sel_hi:[0,0,0]
	v_mfma_scale_f32_16x16x128_f8f6f4 v[62:65], v[2:9], v[214:221], v[62:65], v195, v195 op_sel_hi:[0,0,0]
	v_mfma_scale_f32_16x16x128_f8f6f4 v[58:61], v[10:17], v[214:221], v[58:61], v195, v195 op_sel_hi:[0,0,0]
	v_mfma_scale_f32_16x16x128_f8f6f4 v[46:49], v[2:9], v[222:229], v[46:49], v195, v195 op_sel_hi:[0,0,0]
	v_mfma_scale_f32_16x16x128_f8f6f4 v[42:45], v[10:17], v[222:229], v[42:45], v195, v195 op_sel_hi:[0,0,0]
	s_nop 3
	s_setprio 0
	s_setprio 2
	v_mfma_scale_f32_16x16x128_f8f6f4 v[86:89], v[18:25], v[198:205], v[86:89], v195, v195 op_sel_hi:[0,0,0]
	v_mfma_scale_f32_16x16x128_f8f6f4 v[82:85], v[26:33], v[198:205], v[82:85], v195, v195 op_sel_hi:[0,0,0]
	v_mfma_scale_f32_16x16x128_f8f6f4 v[70:73], v[18:25], v[206:213], v[70:73], v195, v195 op_sel_hi:[0,0,0]
	v_mfma_scale_f32_16x16x128_f8f6f4 v[66:69], v[26:33], v[206:213], v[66:69], v195, v195 op_sel_hi:[0,0,0]
	v_mfma_scale_f32_16x16x128_f8f6f4 v[54:57], v[18:25], v[214:221], v[54:57], v195, v195 op_sel_hi:[0,0,0]
	v_mfma_scale_f32_16x16x128_f8f6f4 v[50:53], v[26:33], v[214:221], v[50:53], v195, v195 op_sel_hi:[0,0,0]
	v_mfma_scale_f32_16x16x128_f8f6f4 v[38:41], v[18:25], v[222:229], v[38:41], v195, v195 op_sel_hi:[0,0,0]
	v_mfma_scale_f32_16x16x128_f8f6f4 v[34:37], v[26:33], v[222:229], v[34:37], v195, v195 op_sel_hi:[0,0,0]
	s_setprio 0
	s_add_i32 s74, s74, 2
	s_add_u32 s17, s17, 0x10000
	s_addc_u32 s19, s19, 0
	s_add_u32 s24, s24, 0x10000
	s_addc_u32 s25, s25, 0
	s_cmp_gt_u32 s74, 13
	s_cbranch_scc0 .Lh1_428
	s_branch .Lfx_11141

; #define PG8_STAGE(bufoff, gbase, voff) do { _Pragma("unroll") for (int _i = 0; _i < 2; ++_i) \
;         __builtin_amdgcn_global_load_lds((const unsigned*)((const char*)(gbase) + (voff)[_i]), (PG8_LAS unsigned*)(lds + (bufoff) + ldsw + _i * 8192), 16, 0, 0); } while (0)
; #define PG8_WAIT_V(n) asm volatile("s_waitcnt vmcnt(" #n ")" ::: "memory")
; #define PG8_WAIT_L(n) asm volatile("s_waitcnt lgkmcnt(" #n ")" ::: "memory")
; #define PG8_BAR __builtin_amdgcn_s_barrier()
; #define PG8_SCHED __builtin_amdgcn_sched_barrier(0)
; template <class Epi, class Sched, bool ALIGN_EPI = true, bool F8 = false>
; __device__ __forceinline__ void gemm_phase(PG8_LAS unsigned char* lds, const Sched& S, const Epi& E) {
;     ...
;             PG8_LDB(B0, 0, 0); PG8_LDB(B1, 0, 1); PG8_SCHED; PG8_LDA(At, 0, 0); PG8_STAGE(PG8_SA(1, 1), a1, voffA[1]);
;             PG8_WAIT_V(8); PG8_WAIT_L(0); PG8_BAR; PG8_MMA(0, 0, At, B0); PG8_MMA(0, 1, At, B1); PG8_BAR; PG8_SCHED;
;             PG8_LDA(At, 0, 1); PG8_STAGE(PG8_SB(0, 0), b2, voffB[0]); PG8_STAGE(PG8_SB(0, 1), b2, voffB[1]); PG8_STAGE(PG8_SA(0, 0), a2, vA2[0]);
;             PG8_WAIT_V(8); PG8_WAIT_L(0); PG8_BAR; PG8_MMA(1, 0, At, B0); PG8_MMA(1, 1, At, B1); PG8_BAR; PG8_SCHED;
;     ...
;         for (int a = 0; a < 2; ++a)
; #pragma unroll
;             for (int b = 0; b < 2; ++b)
; #pragma unroll
;                 for (int m = 0; m < 4; ++m)
; #pragma unroll
;                     for (int n = 0; n < 2; ++n) acc[a][b][m][n] = (f32x4){0.f, 0.f, 0.f, 0.f};
.LBB0_910:
	s_add_u32 s19, s30, 0x10000
	s_addc_u32 s21, s31, 0
	s_add_u32 s28, s28, 0x8000
	s_addc_u32 s29, s29, 0
	s_mov_b32 s65, -2
	s_bitcmp1_b32 s3, 2
	s_cbranch_scc1 .Lh1e_26630
.Lpk0_911:
	ds_read_b128 v[18:21], v191
	ds_read_b128 v[22:25], v191 offset:1024
	ds_read_b128 v[26:29], v191 offset:2048
	ds_read_b128 v[30:33], v191 offset:3072
	ds_read_b128 v[2:5], v192
	ds_read_b128 v[6:9], v192 offset:1024
	ds_read_b128 v[10:13], v192 offset:2048
	ds_read_b128 v[14:17], v192 offset:3072
	s_add_u32 s30, s28, 0x8000
	s_addc_u32 s31, s29, 0
	s_cmp_eq_u32 s65, 12
	s_cselect_b32 s42, s22, s30
	s_cselect_b32 s43, s23, s31
	s_cselect_b32 s40, s24, s19
	s_cselect_b32 s41, s25, s21
	s_add_u32 s30, s42, 0x8000
	s_addc_u32 s31, s43, 0
	v_lshl_add_u64 v[228:229], s[28:29], 0, v[182:183]
	s_add_i32 m0, s27, 0xc000
	ds_read_b128 v[196:199], v193
	ds_read_b128 v[200:203], v193 offset:1024
	ds_read_b128 v[204:207], v193 offset:2048
	ds_read_b128 v[208:211], v193 offset:3072
	ds_read_b128 v[212:215], v193 offset:4096
	ds_read_b128 v[216:219], v193 offset:5120
	ds_read_b128 v[220:223], v193 offset:6144
	ds_read_b128 v[224:227], v193 offset:7168
	global_load_lds_dwordx4 v[228:229], off
	v_lshl_add_u64 v[228:229], s[28:29], 0, v[180:181]
	s_add_i32 m0, s27, 0xe000
	s_nop 0
	global_load_lds_dwordx4 v[228:229], off
	s_waitcnt vmcnt(8)
	s_waitcnt lgkmcnt(0)
	s_setprio 1
	v_mfma_scale_f32_16x16x128_f8f6f4 v[158:161], v[18:25], v[196:203], 0, v194, v194 op_sel_hi:[0,0,0]
	v_mfma_scale_f32_16x16x128_f8f6f4 v[154:157], v[26:33], v[196:203], 0, v194, v194 op_sel_hi:[0,0,0]
	v_mfma_scale_f32_16x16x128_f8f6f4 v[150:153], v[18:25], v[204:211], 0, v194, v194 op_sel_hi:[0,0,0]
	v_mfma_scale_f32_16x16x128_f8f6f4 v[146:149], v[26:33], v[204:211], 0, v194, v194 op_sel_hi:[0,0,0]
	v_mfma_scale_f32_16x16x128_f8f6f4 v[130:133], v[18:25], v[212:219], 0, v194, v194 op_sel_hi:[0,0,0]
	v_mfma_scale_f32_16x16x128_f8f6f4 v[122:125], v[26:33], v[212:219], 0, v194, v194 op_sel_hi:[0,0,0]
	v_mfma_scale_f32_16x16x128_f8f6f4 v[114:117], v[18:25], v[220:227], 0, v194, v194 op_sel_hi:[0,0,0]
	v_mfma_scale_f32_16x16x128_f8f6f4 v[106:109], v[26:33], v[220:227], 0, v194, v194 op_sel_hi:[0,0,0]
	s_nop 3
	s_setprio 0
	s_setprio 1
	v_mfma_scale_f32_16x16x128_f8f6f4 v[142:145], v[2:9], v[196:203], 0, v194, v194 op_sel_hi:[0,0,0]
	v_mfma_scale_f32_16x16x128_f8f6f4 v[138:141], v[10:17], v[196:203], 0, v194, v194 op_sel_hi:[0,0,0]
	v_mfma_scale_f32_16x16x128_f8f6f4 v[134:137], v[2:9], v[204:211], 0, v194, v194 op_sel_hi:[0,0,0]
	v_mfma_scale_f32_16x16x128_f8f6f4 v[126:129], v[10:17], v[204:211], 0, v194, v194 op_sel_hi:[0,0,0]
	v_mfma_scale_f32_16x16x128_f8f6f4 v[118:121], v[2:9], v[212:219], 0, v194, v194 op_sel_hi:[0,0,0]
	v_mfma_scale_f32_16x16x128_f8f6f4 v[110:113], v[10:17], v[212:219], 0, v194, v194 op_sel_hi:[0,0,0]
	v_mfma_scale_f32_16x16x128_f8f6f4 v[102:105], v[2:9], v[220:227], 0, v194, v194 op_sel_hi:[0,0,0]
	v_mfma_scale_f32_16x16x128_f8f6f4 v[98:101], v[10:17], v[220:227], 0, v194, v194 op_sel_hi:[0,0,0]
	s_setprio 0
	s_barrier
	s_add_i32 s66, s60, s48
	v_lshl_add_u64 v[228:229], s[40:41], 0, v[162:163]
	s_mov_b32 m0, s66
	ds_read_b128 v[196:199], v193 offset:16384
	ds_read_b128 v[200:203], v193 offset:17408
	ds_read_b128 v[204:207], v193 offset:18432
	ds_read_b128 v[208:211], v193 offset:19456
	ds_read_b128 v[212:215], v193 offset:20480
	ds_read_b128 v[216:219], v193 offset:21504
	ds_read_b128 v[220:223], v193 offset:22528
	ds_read_b128 v[224:227], v193 offset:23552
	global_load_lds_dwordx4 v[228:229], off
	v_lshl_add_u64 v[230:231], s[40:41], 0, v[164:165]
	s_add_i32 m0, s66, 0x2000
	s_add_i32 s66, s61, s48
	global_load_lds_dwordx4 v[230:231], off
	v_lshl_add_u64 v[228:229], v[228:229], 0, s[6:7]
	s_mov_b32 m0, s66
	s_nop 0
	global_load_lds_dwordx4 v[228:229], off
	v_lshl_add_u64 v[228:229], v[230:231], 0, s[6:7]
	s_add_i32 m0, s66, 0x2000
	s_nop 0
	global_load_lds_dwordx4 v[228:229], off
	v_lshl_add_u64 v[228:229], s[42:43], 0, v[166:167]
	s_mov_b32 m0, s27
	s_nop 0
	global_load_lds_dwordx4 v[228:229], off
	v_lshl_add_u64 v[228:229], s[42:43], 0, v[168:169]
	s_mov_b32 m0, s49
	s_nop 0
	global_load_lds_dwordx4 v[228:229], off
	s_waitcnt vmcnt(8)
	s_waitcnt lgkmcnt(0)
	s_setprio 1
	v_mfma_scale_f32_16x16x128_f8f6f4 v[94:97], v[18:25], v[196:203], 0, v194, v194 op_sel_hi:[0,0,0]
	v_mfma_scale_f32_16x16x128_f8f6f4 v[90:93], v[26:33], v[196:203], 0, v194, v194 op_sel_hi:[0,0,0]
	v_mfma_scale_f32_16x16x128_f8f6f4 v[82:85], v[18:25], v[204:211], 0, v194, v194 op_sel_hi:[0,0,0]
	v_mfma_scale_f32_16x16x128_f8f6f4 v[74:77], v[26:33], v[204:211], 0, v194, v194 op_sel_hi:[0,0,0]
	v_mfma_scale_f32_16x16x128_f8f6f4 v[66:69], v[18:25], v[212:219], 0, v194, v194 op_sel_hi:[0,0,0]
	v_mfma_scale_f32_16x16x128_f8f6f4 v[58:61], v[26:33], v[212:219], 0, v194, v194 op_sel_hi:[0,0,0]
	v_mfma_scale_f32_16x16x128_f8f6f4 v[50:53], v[18:25], v[220:227], 0, v194, v194 op_sel_hi:[0,0,0]
	v_mfma_scale_f32_16x16x128_f8f6f4 v[42:45], v[26:33], v[220:227], 0, v194, v194 op_sel_hi:[0,0,0]
	s_nop 3
	s_setprio 0
	s_setprio 1
	v_mfma_scale_f32_16x16x128_f8f6f4 v[86:89], v[2:9], v[196:203], 0, v194, v194 op_sel_hi:[0,0,0]
	v_mfma_scale_f32_16x16x128_f8f6f4 v[78:81], v[10:17], v[196:203], 0, v194, v194 op_sel_hi:[0,0,0]
	v_mfma_scale_f32_16x16x128_f8f6f4 v[70:73], v[2:9], v[204:211], 0, v194, v194 op_sel_hi:[0,0,0]
	v_mfma_scale_f32_16x16x128_f8f6f4 v[62:65], v[10:17], v[204:211], 0, v194, v194 op_sel_hi:[0,0,0]
	v_mfma_scale_f32_16x16x128_f8f6f4 v[54:57], v[2:9], v[212:219], 0, v194, v194 op_sel_hi:[0,0,0]
	v_mfma_scale_f32_16x16x128_f8f6f4 v[46:49], v[10:17], v[212:219], 0, v194, v194 op_sel_hi:[0,0,0]
	v_mfma_scale_f32_16x16x128_f8f6f4 v[38:41], v[2:9], v[220:227], 0, v194, v194 op_sel_hi:[0,0,0]
	v_mfma_scale_f32_16x16x128_f8f6f4 v[34:37], v[10:17], v[220:227], 0, v194, v194 op_sel_hi:[0,0,0]
	s_setprio 0
	s_barrier
; #define PG8_STAGE(bufoff, gbase, voff) do { _Pragma("unroll") for (int _i = 0; _i < 2; ++_i) \
;         __builtin_amdgcn_global_load_lds((const unsigned*)((const char*)(gbase) + (voff)[_i]), (PG8_LAS unsigned*)(lds + (bufoff) + ldsw + _i * 8192), 16, 0, 0); } while (0)
; #define PG8_WAIT_V(n) asm volatile("s_waitcnt vmcnt(" #n ")" ::: "memory")
; #define PG8_WAIT_L(n) asm volatile("s_waitcnt lgkmcnt(" #n ")" ::: "memory")
; #define PG8_BAR __builtin_amdgcn_s_barrier()
; #define PG8_SCHED __builtin_amdgcn_sched_barrier(0)
; template <class Epi, class Sched, bool ALIGN_EPI = true, bool F8 = false>
; __device__ __forceinline__ void gemm_phase(PG8_LAS unsigned char* lds, const Sched& S, const Epi& E) {
;     ...
;             PG8_LDB(B0, 1, 0); PG8_LDB(B1, 1, 1); PG8_SCHED; PG8_LDA(At, 1, 0); PG8_STAGE(PG8_SA(0, 1), a2, vA2[1]);
;             PG8_WAIT_V(8); PG8_WAIT_L(0); PG8_BAR; PG8_MMA(0, 0, At, B0); PG8_MMA(0, 1, At, B1); PG8_BAR; PG8_SCHED;
;             PG8_LDA(At, 1, 1); PG8_STAGE(PG8_SB(1, 0), b3, voffB[0]); PG8_STAGE(PG8_SB(1, 1), b3, voffB[1]); PG8_STAGE(PG8_SA(1, 0), a3, vA2[0]);
;             PG8_WAIT_V(8); PG8_WAIT_L(0); PG8_BAR; PG8_MMA(1, 0, At, B0); PG8_MMA(1, 1, At, B1); PG8_BAR; PG8_SCHED;
	s_add_i32 s66, 0, 0x18000
	s_add_i32 s67, 0, 0x1c000
	v_add_u32_e32 v14, s66, v189
	v_add_u32_e32 v30, s67, v189
	ds_read_b128 v[2:5], v14
	ds_read_b128 v[6:9], v14 offset:1024
	ds_read_b128 v[10:13], v14 offset:2048
	ds_read_b128 v[14:17], v14 offset:3072
	ds_read_b128 v[18:21], v30
	ds_read_b128 v[22:25], v30 offset:1024
	ds_read_b128 v[26:29], v30 offset:2048
	ds_read_b128 v[30:33], v30 offset:3072
	s_mov_b32 m0, s50
	v_lshl_add_u64 v[228:229], s[42:43], 0, v[172:173]
	ds_read_b128 v[196:199], v193 offset:32768
	ds_read_b128 v[200:203], v193 offset:33792
	ds_read_b128 v[204:207], v193 offset:34816
	ds_read_b128 v[208:211], v193 offset:35840
	ds_read_b128 v[212:215], v193 offset:36864
	ds_read_b128 v[216:219], v193 offset:37888
	ds_read_b128 v[220:223], v193 offset:38912
	ds_read_b128 v[224:227], v193 offset:39936
	global_load_lds_dwordx4 v[228:229], off
	v_lshl_add_u64 v[228:229], s[42:43], 0, v[174:175]
	s_mov_b32 m0, s51
	s_nop 0
	global_load_lds_dwordx4 v[228:229], off
	s_waitcnt vmcnt(8)
	s_waitcnt lgkmcnt(0)
	s_setprio 1
	v_mfma_scale_f32_16x16x128_f8f6f4 v[158:161], v[2:9], v[196:203], v[158:161], v194, v194 op_sel_hi:[0,0,0]
	v_mfma_scale_f32_16x16x128_f8f6f4 v[154:157], v[10:17], v[196:203], v[154:157], v194, v194 op_sel_hi:[0,0,0]
	v_mfma_scale_f32_16x16x128_f8f6f4 v[150:153], v[2:9], v[204:211], v[150:153], v194, v194 op_sel_hi:[0,0,0]
	v_mfma_scale_f32_16x16x128_f8f6f4 v[146:149], v[10:17], v[204:211], v[146:149], v194, v194 op_sel_hi:[0,0,0]
	v_mfma_scale_f32_16x16x128_f8f6f4 v[130:133], v[2:9], v[212:219], v[130:133], v194, v194 op_sel_hi:[0,0,0]
	v_mfma_scale_f32_16x16x128_f8f6f4 v[122:125], v[10:17], v[212:219], v[122:125], v194, v194 op_sel_hi:[0,0,0]
	v_mfma_scale_f32_16x16x128_f8f6f4 v[114:117], v[2:9], v[220:227], v[114:117], v194, v194 op_sel_hi:[0,0,0]
	v_mfma_scale_f32_16x16x128_f8f6f4 v[106:109], v[10:17], v[220:227], v[106:109], v194, v194 op_sel_hi:[0,0,0]
	s_nop 3
	s_setprio 0
	s_setprio 1
	v_mfma_scale_f32_16x16x128_f8f6f4 v[142:145], v[18:25], v[196:203], v[142:145], v194, v194 op_sel_hi:[0,0,0]
	v_mfma_scale_f32_16x16x128_f8f6f4 v[138:141], v[26:33], v[196:203], v[138:141], v194, v194 op_sel_hi:[0,0,0]
	v_mfma_scale_f32_16x16x128_f8f6f4 v[134:137], v[18:25], v[204:211], v[134:137], v194, v194 op_sel_hi:[0,0,0]
	v_mfma_scale_f32_16x16x128_f8f6f4 v[126:129], v[26:33], v[204:211], v[126:129], v194, v194 op_sel_hi:[0,0,0]
	v_mfma_scale_f32_16x16x128_f8f6f4 v[118:121], v[18:25], v[212:219], v[118:121], v194, v194 op_sel_hi:[0,0,0]
	v_mfma_scale_f32_16x16x128_f8f6f4 v[110:113], v[26:33], v[212:219], v[110:113], v194, v194 op_sel_hi:[0,0,0]
	v_mfma_scale_f32_16x16x128_f8f6f4 v[102:105], v[18:25], v[220:227], v[102:105], v194, v194 op_sel_hi:[0,0,0]
	v_mfma_scale_f32_16x16x128_f8f6f4 v[98:101], v[26:33], v[220:227], v[98:101], v194, v194 op_sel_hi:[0,0,0]
	s_setprio 0
	s_barrier
	s_add_u32 s40, s40, 0x8000
	s_addc_u32 s41, s41, 0
	s_add_i32 s42, s66, s48
	v_lshl_add_u64 v[228:229], s[40:41], 0, v[162:163]
	s_mov_b32 m0, s42
	ds_read_b128 v[196:199], v193 offset:49152
	ds_read_b128 v[200:203], v193 offset:50176
	ds_read_b128 v[204:207], v193 offset:51200
	ds_read_b128 v[208:211], v193 offset:52224
	ds_read_b128 v[212:215], v193 offset:53248
	ds_read_b128 v[216:219], v193 offset:54272
	ds_read_b128 v[220:223], v193 offset:55296
	ds_read_b128 v[224:227], v193 offset:56320
	global_load_lds_dwordx4 v[228:229], off
	v_lshl_add_u64 v[228:229], s[40:41], 0, v[164:165]
	s_add_i32 m0, s42, 0x2000
	s_add_i32 s42, s67, s48
	global_load_lds_dwordx4 v[228:229], off
	v_lshl_add_u64 v[228:229], s[40:41], 0, v[176:177]
	s_mov_b32 m0, s42
	s_nop 0
	global_load_lds_dwordx4 v[228:229], off
	v_lshl_add_u64 v[228:229], s[40:41], 0, v[178:179]
	s_add_i32 m0, s42, 0x2000
	s_nop 0
	global_load_lds_dwordx4 v[228:229], off
	v_lshl_add_u64 v[228:229], s[30:31], 0, v[166:167]
	s_mov_b32 m0, s53
	s_nop 0
	global_load_lds_dwordx4 v[228:229], off
	v_lshl_add_u64 v[228:229], s[30:31], 0, v[168:169]
	s_mov_b32 m0, s58
	s_nop 0
	global_load_lds_dwordx4 v[228:229], off
	s_waitcnt vmcnt(8)
	s_waitcnt lgkmcnt(0)
	s_setprio 1
	v_mfma_scale_f32_16x16x128_f8f6f4 v[94:97], v[2:9], v[196:203], v[94:97], v194, v194 op_sel_hi:[0,0,0]
	v_mfma_scale_f32_16x16x128_f8f6f4 v[90:93], v[10:17], v[196:203], v[90:93], v194, v194 op_sel_hi:[0,0,0]
	v_mfma_scale_f32_16x16x128_f8f6f4 v[82:85], v[2:9], v[204:211], v[82:85], v194, v194 op_sel_hi:[0,0,0]
	v_mfma_scale_f32_16x16x128_f8f6f4 v[74:77], v[10:17], v[204:211], v[74:77], v194, v194 op_sel_hi:[0,0,0]
	v_mfma_scale_f32_16x16x128_f8f6f4 v[66:69], v[2:9], v[212:219], v[66:69], v194, v194 op_sel_hi:[0,0,0]
	v_mfma_scale_f32_16x16x128_f8f6f4 v[58:61], v[10:17], v[212:219], v[58:61], v194, v194 op_sel_hi:[0,0,0]
	v_mfma_scale_f32_16x16x128_f8f6f4 v[50:53], v[2:9], v[220:227], v[50:53], v194, v194 op_sel_hi:[0,0,0]
	v_mfma_scale_f32_16x16x128_f8f6f4 v[42:45], v[10:17], v[220:227], v[42:45], v194, v194 op_sel_hi:[0,0,0]
	s_nop 3
	s_setprio 0
	s_setprio 1
	v_mfma_scale_f32_16x16x128_f8f6f4 v[86:89], v[18:25], v[196:203], v[86:89], v194, v194 op_sel_hi:[0,0,0]
	v_mfma_scale_f32_16x16x128_f8f6f4 v[78:81], v[26:33], v[196:203], v[78:81], v194, v194 op_sel_hi:[0,0,0]
	v_mfma_scale_f32_16x16x128_f8f6f4 v[70:73], v[18:25], v[204:211], v[70:73], v194, v194 op_sel_hi:[0,0,0]
	v_mfma_scale_f32_16x16x128_f8f6f4 v[62:65], v[26:33], v[204:211], v[62:65], v194, v194 op_sel_hi:[0,0,0]
	v_mfma_scale_f32_16x16x128_f8f6f4 v[54:57], v[18:25], v[212:219], v[54:57], v194, v194 op_sel_hi:[0,0,0]
	v_mfma_scale_f32_16x16x128_f8f6f4 v[46:49], v[26:33], v[212:219], v[46:49], v194, v194 op_sel_hi:[0,0,0]
	v_mfma_scale_f32_16x16x128_f8f6f4 v[38:41], v[18:25], v[220:227], v[38:41], v194, v194 op_sel_hi:[0,0,0]
	v_mfma_scale_f32_16x16x128_f8f6f4 v[34:37], v[26:33], v[220:227], v[34:37], v194, v194 op_sel_hi:[0,0,0]
	s_setprio 0
	s_barrier
	s_add_i32 s65, s65, 2
	s_add_u32 s19, s19, 0x10000
	s_addc_u32 s21, s21, 0
	s_add_u32 s28, s28, 0x10000
	s_addc_u32 s29, s29, 0
	s_cmp_gt_u32 s65, 13
	s_cbranch_scc0 .LBB0_911
	s_branch .Lfx_26630

; #define PG8_STAGE(bufoff, gbase, voff) do { _Pragma("unroll") for (int _i = 0; _i < 2; ++_i) \
;         __builtin_amdgcn_global_load_lds((const unsigned*)((const char*)(gbase) + (voff)[_i]), (PG8_LAS unsigned*)(lds + (bufoff) + ldsw + _i * 8192), 16, 0, 0); } while (0)
; #define PG8_WAIT_V(n) asm volatile("s_waitcnt vmcnt(" #n ")" ::: "memory")
; #define PG8_WAIT_L(n) asm volatile("s_waitcnt lgkmcnt(" #n ")" ::: "memory")
; #define PG8_BAR __builtin_amdgcn_s_barrier()
; #define PG8_SCHED __builtin_amdgcn_sched_barrier(0)
; template <class Epi, class Sched, bool ALIGN_EPI = true, bool F8 = false>
; __device__ __forceinline__ void gemm_phase(PG8_LAS unsigned char* lds, const Sched& S, const Epi& E) {
;     ...
;             PG8_LDB(B0, 0, 0); PG8_LDB(B1, 0, 1); PG8_SCHED; PG8_LDA(At, 0, 0); PG8_STAGE(PG8_SA(1, 1), a1, voffA[1]);
;             PG8_WAIT_V(8); PG8_WAIT_L(0); PG8_BAR; PG8_MMA(0, 0, At, B0); PG8_MMA(0, 1, At, B1); PG8_BAR; PG8_SCHED;
;             PG8_LDA(At, 0, 1); PG8_STAGE(PG8_SB(0, 0), b2, voffB[0]); PG8_STAGE(PG8_SB(0, 1), b2, voffB[1]); PG8_STAGE(PG8_SA(0, 0), a2, vA2[0]);
;             PG8_WAIT_V(8); PG8_WAIT_L(0); PG8_BAR; PG8_MMA(1, 0, At, B0); PG8_MMA(1, 1, At, B1); PG8_BAR; PG8_SCHED;
;             PG8_LDB(B0, 1, 0); PG8_LDB(B1, 1, 1); PG8_SCHED; PG8_LDA(At, 1, 0); PG8_STAGE(PG8_SA(0, 1), a2, vA2[1]);
;             PG8_WAIT_V(8); PG8_WAIT_L(0); PG8_BAR; PG8_MMA(0, 0, At, B0); PG8_MMA(0, 1, At, B1); PG8_BAR; PG8_SCHED;
.Lh1e_26630:
.Lpk1_911:
	ds_read_b128 v[18:21], v191
	ds_read_b128 v[22:25], v191 offset:1024
	ds_read_b128 v[26:29], v191 offset:2048
	ds_read_b128 v[30:33], v191 offset:3072
	ds_read_b128 v[2:5], v192
	ds_read_b128 v[6:9], v192 offset:1024
	ds_read_b128 v[10:13], v192 offset:2048
	ds_read_b128 v[14:17], v192 offset:3072
	s_add_u32 s30, s28, 0x8000
	s_addc_u32 s31, s29, 0
	s_cmp_eq_u32 s65, 12
	s_cselect_b32 s42, s22, s30
	s_cselect_b32 s43, s23, s31
	s_cselect_b32 s40, s24, s19
	s_cselect_b32 s41, s25, s21
	s_add_u32 s30, s42, 0x8000
	s_addc_u32 s31, s43, 0
	v_lshl_add_u64 v[228:229], s[28:29], 0, v[182:183]
	s_add_i32 m0, s27, 0xc000
	ds_read_b128 v[196:199], v193
	ds_read_b128 v[200:203], v193 offset:1024
	ds_read_b128 v[204:207], v193 offset:2048
	ds_read_b128 v[208:211], v193 offset:3072
	ds_read_b128 v[212:215], v193 offset:4096
	ds_read_b128 v[216:219], v193 offset:5120
	ds_read_b128 v[220:223], v193 offset:6144
	ds_read_b128 v[224:227], v193 offset:7168
	global_load_lds_dwordx4 v[228:229], off
	v_lshl_add_u64 v[228:229], s[28:29], 0, v[180:181]
	s_add_i32 m0, s27, 0xe000
	s_nop 0
	global_load_lds_dwordx4 v[228:229], off
	s_waitcnt vmcnt(8)
	s_waitcnt lgkmcnt(0)
	s_barrier
	s_setprio 2
	v_mfma_scale_f32_16x16x128_f8f6f4 v[158:161], v[18:25], v[196:203], 0, v194, v194 op_sel_hi:[0,0,0]
	v_mfma_scale_f32_16x16x128_f8f6f4 v[154:157], v[26:33], v[196:203], 0, v194, v194 op_sel_hi:[0,0,0]
	v_mfma_scale_f32_16x16x128_f8f6f4 v[150:153], v[18:25], v[204:211], 0, v194, v194 op_sel_hi:[0,0,0]
	v_mfma_scale_f32_16x16x128_f8f6f4 v[146:149], v[26:33], v[204:211], 0, v194, v194 op_sel_hi:[0,0,0]
	v_mfma_scale_f32_16x16x128_f8f6f4 v[130:133], v[18:25], v[212:219], 0, v194, v194 op_sel_hi:[0,0,0]
	v_mfma_scale_f32_16x16x128_f8f6f4 v[122:125], v[26:33], v[212:219], 0, v194, v194 op_sel_hi:[0,0,0]
	v_mfma_scale_f32_16x16x128_f8f6f4 v[114:117], v[18:25], v[220:227], 0, v194, v194 op_sel_hi:[0,0,0]
	v_mfma_scale_f32_16x16x128_f8f6f4 v[106:109], v[26:33], v[220:227], 0, v194, v194 op_sel_hi:[0,0,0]
	s_nop 3
	s_setprio 0
	s_setprio 2
	v_mfma_scale_f32_16x16x128_f8f6f4 v[142:145], v[2:9], v[196:203], 0, v194, v194 op_sel_hi:[0,0,0]
	v_mfma_scale_f32_16x16x128_f8f6f4 v[138:141], v[10:17], v[196:203], 0, v194, v194 op_sel_hi:[0,0,0]
	v_mfma_scale_f32_16x16x128_f8f6f4 v[134:137], v[2:9], v[204:211], 0, v194, v194 op_sel_hi:[0,0,0]
	v_mfma_scale_f32_16x16x128_f8f6f4 v[126:129], v[10:17], v[204:211], 0, v194, v194 op_sel_hi:[0,0,0]
	v_mfma_scale_f32_16x16x128_f8f6f4 v[118:121], v[2:9], v[212:219], 0, v194, v194 op_sel_hi:[0,0,0]
	v_mfma_scale_f32_16x16x128_f8f6f4 v[110:113], v[10:17], v[212:219], 0, v194, v194 op_sel_hi:[0,0,0]
	v_mfma_scale_f32_16x16x128_f8f6f4 v[102:105], v[2:9], v[220:227], 0, v194, v194 op_sel_hi:[0,0,0]
	v_mfma_scale_f32_16x16x128_f8f6f4 v[98:101], v[10:17], v[220:227], 0, v194, v194 op_sel_hi:[0,0,0]
	s_setprio 0
	s_add_i32 s66, s60, s48
	v_lshl_add_u64 v[228:229], s[40:41], 0, v[162:163]
	s_mov_b32 m0, s66
	ds_read_b128 v[196:199], v193 offset:16384
	ds_read_b128 v[200:203], v193 offset:17408
	ds_read_b128 v[204:207], v193 offset:18432
	ds_read_b128 v[208:211], v193 offset:19456
	ds_read_b128 v[212:215], v193 offset:20480
	ds_read_b128 v[216:219], v193 offset:21504
	ds_read_b128 v[220:223], v193 offset:22528
	ds_read_b128 v[224:227], v193 offset:23552
	global_load_lds_dwordx4 v[228:229], off
	v_lshl_add_u64 v[230:231], s[40:41], 0, v[164:165]
	s_add_i32 m0, s66, 0x2000
	s_add_i32 s66, s61, s48
	global_load_lds_dwordx4 v[230:231], off
	v_lshl_add_u64 v[228:229], v[228:229], 0, s[6:7]
	s_mov_b32 m0, s66
	s_nop 0
	global_load_lds_dwordx4 v[228:229], off
	v_lshl_add_u64 v[228:229], v[230:231], 0, s[6:7]
	s_add_i32 m0, s66, 0x2000
	s_nop 0
	global_load_lds_dwordx4 v[228:229], off
	v_lshl_add_u64 v[228:229], s[42:43], 0, v[166:167]
	s_mov_b32 m0, s27
	s_nop 0
	global_load_lds_dwordx4 v[228:229], off
	v_lshl_add_u64 v[228:229], s[42:43], 0, v[168:169]
	s_mov_b32 m0, s49
	s_nop 0
	global_load_lds_dwordx4 v[228:229], off
	s_waitcnt vmcnt(8)
	s_waitcnt lgkmcnt(0)
	s_barrier
	s_setprio 2
	v_mfma_scale_f32_16x16x128_f8f6f4 v[94:97], v[18:25], v[196:203], 0, v194, v194 op_sel_hi:[0,0,0]
	v_mfma_scale_f32_16x16x128_f8f6f4 v[90:93], v[26:33], v[196:203], 0, v194, v194 op_sel_hi:[0,0,0]
	v_mfma_scale_f32_16x16x128_f8f6f4 v[82:85], v[18:25], v[204:211], 0, v194, v194 op_sel_hi:[0,0,0]
	v_mfma_scale_f32_16x16x128_f8f6f4 v[74:77], v[26:33], v[204:211], 0, v194, v194 op_sel_hi:[0,0,0]
	v_mfma_scale_f32_16x16x128_f8f6f4 v[66:69], v[18:25], v[212:219], 0, v194, v194 op_sel_hi:[0,0,0]
	v_mfma_scale_f32_16x16x128_f8f6f4 v[58:61], v[26:33], v[212:219], 0, v194, v194 op_sel_hi:[0,0,0]
	v_mfma_scale_f32_16x16x128_f8f6f4 v[50:53], v[18:25], v[220:227], 0, v194, v194 op_sel_hi:[0,0,0]
	v_mfma_scale_f32_16x16x128_f8f6f4 v[42:45], v[26:33], v[220:227], 0, v194, v194 op_sel_hi:[0,0,0]
	s_nop 3
	s_setprio 0
	s_setprio 2
	v_mfma_scale_f32_16x16x128_f8f6f4 v[86:89], v[2:9], v[196:203], 0, v194, v194 op_sel_hi:[0,0,0]
	v_mfma_scale_f32_16x16x128_f8f6f4 v[78:81], v[10:17], v[196:203], 0, v194, v194 op_sel_hi:[0,0,0]
	v_mfma_scale_f32_16x16x128_f8f6f4 v[70:73], v[2:9], v[204:211], 0, v194, v194 op_sel_hi:[0,0,0]
	v_mfma_scale_f32_16x16x128_f8f6f4 v[62:65], v[10:17], v[204:211], 0, v194, v194 op_sel_hi:[0,0,0]
	v_mfma_scale_f32_16x16x128_f8f6f4 v[54:57], v[2:9], v[212:219], 0, v194, v194 op_sel_hi:[0,0,0]
	v_mfma_scale_f32_16x16x128_f8f6f4 v[46:49], v[10:17], v[212:219], 0, v194, v194 op_sel_hi:[0,0,0]
	v_mfma_scale_f32_16x16x128_f8f6f4 v[38:41], v[2:9], v[220:227], 0, v194, v194 op_sel_hi:[0,0,0]
	v_mfma_scale_f32_16x16x128_f8f6f4 v[34:37], v[10:17], v[220:227], 0, v194, v194 op_sel_hi:[0,0,0]
	s_setprio 0
	s_add_i32 s66, 0, 0x18000
	s_add_i32 s67, 0, 0x1c000
	v_add_u32_e32 v14, s66, v189
	v_add_u32_e32 v30, s67, v189
	ds_read_b128 v[2:5], v14
	ds_read_b128 v[6:9], v14 offset:1024
	ds_read_b128 v[10:13], v14 offset:2048
	ds_read_b128 v[14:17], v14 offset:3072
	ds_read_b128 v[18:21], v30
	ds_read_b128 v[22:25], v30 offset:1024
	ds_read_b128 v[26:29], v30 offset:2048
	ds_read_b128 v[30:33], v30 offset:3072
	s_mov_b32 m0, s50
	v_lshl_add_u64 v[228:229], s[42:43], 0, v[172:173]
	ds_read_b128 v[196:199], v193 offset:32768
	ds_read_b128 v[200:203], v193 offset:33792
	ds_read_b128 v[204:207], v193 offset:34816
	ds_read_b128 v[208:211], v193 offset:35840
	ds_read_b128 v[212:215], v193 offset:36864
	ds_read_b128 v[216:219], v193 offset:37888
	ds_read_b128 v[220:223], v193 offset:38912
	ds_read_b128 v[224:227], v193 offset:39936
	global_load_lds_dwordx4 v[228:229], off
	v_lshl_add_u64 v[228:229], s[42:43], 0, v[174:175]
	s_mov_b32 m0, s51
	s_nop 0
	global_load_lds_dwordx4 v[228:229], off
	s_waitcnt vmcnt(8)
	s_waitcnt lgkmcnt(0)
	s_barrier
; #define PG8_STAGE(bufoff, gbase, voff) do { _Pragma("unroll") for (int _i = 0; _i < 2; ++_i) \
;         __builtin_amdgcn_global_load_lds((const unsigned*)((const char*)(gbase) + (voff)[_i]), (PG8_LAS unsigned*)(lds + (bufoff) + ldsw + _i * 8192), 16, 0, 0); } while (0)
; #define PG8_WAIT_V(n) asm volatile("s_waitcnt vmcnt(" #n ")" ::: "memory")
; #define PG8_WAIT_L(n) asm volatile("s_waitcnt lgkmcnt(" #n ")" ::: "memory")
; #define PG8_BAR __builtin_amdgcn_s_barrier()
; #define PG8_SCHED __builtin_amdgcn_sched_barrier(0)
; template <class Epi, class Sched, bool ALIGN_EPI = true, bool F8 = false>
; __device__ __forceinline__ void gemm_phase(PG8_LAS unsigned char* lds, const Sched& S, const Epi& E) {
;     ...
;             PG8_WAIT_V(8); PG8_WAIT_L(0); PG8_BAR; PG8_MMA(0, 0, At, B0); PG8_MMA(0, 1, At, B1); PG8_BAR; PG8_SCHED;
;             PG8_LDA(At, 1, 1); PG8_STAGE(PG8_SB(1, 0), b3, voffB[0]); PG8_STAGE(PG8_SB(1, 1), b3, voffB[1]); PG8_STAGE(PG8_SA(1, 0), a3, vA2[0]);
;             PG8_WAIT_V(8); PG8_WAIT_L(0); PG8_BAR; PG8_MMA(1, 0, At, B0); PG8_MMA(1, 1, At, B1); PG8_BAR; PG8_SCHED;
	s_setprio 2
	v_mfma_scale_f32_16x16x128_f8f6f4 v[158:161], v[2:9], v[196:203], v[158:161], v194, v194 op_sel_hi:[0,0,0]
	v_mfma_scale_f32_16x16x128_f8f6f4 v[154:157], v[10:17], v[196:203], v[154:157], v194, v194 op_sel_hi:[0,0,0]
	v_mfma_scale_f32_16x16x128_f8f6f4 v[150:153], v[2:9], v[204:211], v[150:153], v194, v194 op_sel_hi:[0,0,0]
	v_mfma_scale_f32_16x16x128_f8f6f4 v[146:149], v[10:17], v[204:211], v[146:149], v194, v194 op_sel_hi:[0,0,0]
	v_mfma_scale_f32_16x16x128_f8f6f4 v[130:133], v[2:9], v[212:219], v[130:133], v194, v194 op_sel_hi:[0,0,0]
	v_mfma_scale_f32_16x16x128_f8f6f4 v[122:125], v[10:17], v[212:219], v[122:125], v194, v194 op_sel_hi:[0,0,0]
	v_mfma_scale_f32_16x16x128_f8f6f4 v[114:117], v[2:9], v[220:227], v[114:117], v194, v194 op_sel_hi:[0,0,0]
	v_mfma_scale_f32_16x16x128_f8f6f4 v[106:109], v[10:17], v[220:227], v[106:109], v194, v194 op_sel_hi:[0,0,0]
	s_nop 3
	s_setprio 0
	s_setprio 2
	v_mfma_scale_f32_16x16x128_f8f6f4 v[142:145], v[18:25], v[196:203], v[142:145], v194, v194 op_sel_hi:[0,0,0]
	v_mfma_scale_f32_16x16x128_f8f6f4 v[138:141], v[26:33], v[196:203], v[138:141], v194, v194 op_sel_hi:[0,0,0]
	v_mfma_scale_f32_16x16x128_f8f6f4 v[134:137], v[18:25], v[204:211], v[134:137], v194, v194 op_sel_hi:[0,0,0]
	v_mfma_scale_f32_16x16x128_f8f6f4 v[126:129], v[26:33], v[204:211], v[126:129], v194, v194 op_sel_hi:[0,0,0]
	v_mfma_scale_f32_16x16x128_f8f6f4 v[118:121], v[18:25], v[212:219], v[118:121], v194, v194 op_sel_hi:[0,0,0]
	v_mfma_scale_f32_16x16x128_f8f6f4 v[110:113], v[26:33], v[212:219], v[110:113], v194, v194 op_sel_hi:[0,0,0]
	v_mfma_scale_f32_16x16x128_f8f6f4 v[102:105], v[18:25], v[220:227], v[102:105], v194, v194 op_sel_hi:[0,0,0]
	v_mfma_scale_f32_16x16x128_f8f6f4 v[98:101], v[26:33], v[220:227], v[98:101], v194, v194 op_sel_hi:[0,0,0]
	s_setprio 0
	s_add_u32 s40, s40, 0x8000
	s_addc_u32 s41, s41, 0
	s_add_i32 s42, s66, s48
	v_lshl_add_u64 v[228:229], s[40:41], 0, v[162:163]
	s_mov_b32 m0, s42
	ds_read_b128 v[196:199], v193 offset:49152
	ds_read_b128 v[200:203], v193 offset:50176
	ds_read_b128 v[204:207], v193 offset:51200
	ds_read_b128 v[208:211], v193 offset:52224
	ds_read_b128 v[212:215], v193 offset:53248
	ds_read_b128 v[216:219], v193 offset:54272
	ds_read_b128 v[220:223], v193 offset:55296
	ds_read_b128 v[224:227], v193 offset:56320
	global_load_lds_dwordx4 v[228:229], off
	v_lshl_add_u64 v[228:229], s[40:41], 0, v[164:165]
	s_add_i32 m0, s42, 0x2000
	s_add_i32 s42, s67, s48
	global_load_lds_dwordx4 v[228:229], off
	v_lshl_add_u64 v[228:229], s[40:41], 0, v[176:177]
	s_mov_b32 m0, s42
	s_nop 0
	global_load_lds_dwordx4 v[228:229], off
	v_lshl_add_u64 v[228:229], s[40:41], 0, v[178:179]
	s_add_i32 m0, s42, 0x2000
	s_nop 0
	global_load_lds_dwordx4 v[228:229], off
	v_lshl_add_u64 v[228:229], s[30:31], 0, v[166:167]
	s_mov_b32 m0, s53
	s_nop 0
	global_load_lds_dwordx4 v[228:229], off
	v_lshl_add_u64 v[228:229], s[30:31], 0, v[168:169]
	s_mov_b32 m0, s58
	s_nop 0
	global_load_lds_dwordx4 v[228:229], off
	s_waitcnt vmcnt(8)
	s_waitcnt lgkmcnt(0)
	s_barrier
	s_setprio 2
	v_mfma_scale_f32_16x16x128_f8f6f4 v[94:97], v[2:9], v[196:203], v[94:97], v194, v194 op_sel_hi:[0,0,0]
	v_mfma_scale_f32_16x16x128_f8f6f4 v[90:93], v[10:17], v[196:203], v[90:93], v194, v194 op_sel_hi:[0,0,0]
	v_mfma_scale_f32_16x16x128_f8f6f4 v[82:85], v[2:9], v[204:211], v[82:85], v194, v194 op_sel_hi:[0,0,0]
	v_mfma_scale_f32_16x16x128_f8f6f4 v[74:77], v[10:17], v[204:211], v[74:77], v194, v194 op_sel_hi:[0,0,0]
	v_mfma_scale_f32_16x16x128_f8f6f4 v[66:69], v[2:9], v[212:219], v[66:69], v194, v194 op_sel_hi:[0,0,0]
	v_mfma_scale_f32_16x16x128_f8f6f4 v[58:61], v[10:17], v[212:219], v[58:61], v194, v194 op_sel_hi:[0,0,0]
	v_mfma_scale_f32_16x16x128_f8f6f4 v[50:53], v[2:9], v[220:227], v[50:53], v194, v194 op_sel_hi:[0,0,0]
	v_mfma_scale_f32_16x16x128_f8f6f4 v[42:45], v[10:17], v[220:227], v[42:45], v194, v194 op_sel_hi:[0,0,0]
	s_nop 3
	s_setprio 0
	s_setprio 2
	v_mfma_scale_f32_16x16x128_f8f6f4 v[86:89], v[18:25], v[196:203], v[86:89], v194, v194 op_sel_hi:[0,0,0]
	v_mfma_scale_f32_16x16x128_f8f6f4 v[78:81], v[26:33], v[196:203], v[78:81], v194, v194 op_sel_hi:[0,0,0]
	v_mfma_scale_f32_16x16x128_f8f6f4 v[70:73], v[18:25], v[204:211], v[70:73], v194, v194 op_sel_hi:[0,0,0]
	v_mfma_scale_f32_16x16x128_f8f6f4 v[62:65], v[26:33], v[204:211], v[62:65], v194, v194 op_sel_hi:[0,0,0]
	v_mfma_scale_f32_16x16x128_f8f6f4 v[54:57], v[18:25], v[212:219], v[54:57], v194, v194 op_sel_hi:[0,0,0]
	v_mfma_scale_f32_16x16x128_f8f6f4 v[46:49], v[26:33], v[212:219], v[46:49], v194, v194 op_sel_hi:[0,0,0]
	v_mfma_scale_f32_16x16x128_f8f6f4 v[38:41], v[18:25], v[220:227], v[38:41], v194, v194 op_sel_hi:[0,0,0]
	v_mfma_scale_f32_16x16x128_f8f6f4 v[34:37], v[26:33], v[220:227], v[34:37], v194, v194 op_sel_hi:[0,0,0]
	s_setprio 0
	s_add_i32 s65, s65, 2
	s_add_u32 s19, s19, 0x10000
	s_addc_u32 s21, s21, 0
	s_add_u32 s28, s28, 0x10000
	s_addc_u32 s29, s29, 0
	s_cmp_gt_u32 s65, 13
	s_cbranch_scc0 .Lh1_911
	s_branch .Lfx_26630

; template <class Epi, class Sched, bool ALIGN_EPI = true, bool F8 = false>
; __device__ __forceinline__ void gemm_phase(PG8_LAS unsigned char* lds, const Sched& S, const Epi& E) {
;     ...
;         for (int a = 0; a < 2; ++a)
; #pragma unroll
;             for (int b = 0; b < 2; ++b)
; #pragma unroll
;                 for (int m = 0; m < 4; ++m)
; #pragma unroll
;                     for (int n = 0; n < 2; ++n) acc[a][b][m][n] = (f32x4){0.f, 0.f, 0.f, 0.f};
;         }
;         cur = nxt; cA = nA; cB = nB; ++ui;
; #pragma unroll
;         for (int h = 0; h < 2; ++h)
; #pragma unroll
;             for (int i = 0; i < 2; ++i) voffA[h][i] = voffAn[h][i];
.LBB0_1051:
	v_mov_b32_e32 v174, v219
	v_mov_b32_e32 v176, v220
	v_mov_b32_e32 v172, v217
	v_mov_b32_e32 v216, v218
	s_mov_b32 s50, s66
	s_mov_b32 s0, s20
	s_mov_b32 s49, s64
	s_mov_b32 s51, s65
	s_mov_b64 s[8:9], s[24:25]
	s_mov_b32 s13, s67

; #define PG8_STAGE(bufoff, gbase, voff) do { _Pragma("unroll") for (int _i = 0; _i < 2; ++_i) \
;         __builtin_amdgcn_global_load_lds((const unsigned*)((const char*)(gbase) + (voff)[_i]), (PG8_LAS unsigned*)(lds + (bufoff) + ldsw + _i * 8192), 16, 0, 0); } while (0)
; #define PG8_WAIT_V(n) asm volatile("s_waitcnt vmcnt(" #n ")" ::: "memory")
; #define PG8_WAIT_L(n) asm volatile("s_waitcnt lgkmcnt(" #n ")" ::: "memory")
; #define PG8_BAR __builtin_amdgcn_s_barrier()
; #define PG8_SCHED __builtin_amdgcn_sched_barrier(0)
; template <class Epi, class Sched, bool ALIGN_EPI = true, bool F8 = false>
; __device__ __forceinline__ void gemm_phase(PG8_LAS unsigned char* lds, const Sched& S, const Epi& E) {
;     ...
;             if constexpr (Sched::GATHER) { if (last && has_next) S.a_off(nxt, Rs, Cs, voffAn); }
;             const char* a1 = cA + (size_t)(t + 1) * kstep;
;             const char* a2 = last ? nA : cA + (size_t)(t + 2) * kstep; const char* b2 = last ? nB : cB + (size_t)(t + 2) * kstepB;
;             const char* a3 = a2 + kstep; const char* b3 = b2 + kstepB;
;             unsigned vA2[2][2];
; #pragma unroll
;             for (int h = 0; h < 2; ++h)
; #pragma unroll
;                 for (int i = 0; i < 2; ++i) { if constexpr (Sched::GATHER) vA2[h][i] = (last && has_next) ? voffAn[h][i] : voffA[h][i]; else vA2[h][i] = voffA[h][i]; }
;             PG8_LDB(B0, 0, 0); PG8_LDB(B1, 0, 1); PG8_SCHED; PG8_LDA(At, 0, 0); PG8_STAGE(PG8_SA(1, 1), a1, voffA[1]);
;             PG8_WAIT_V(8); PG8_WAIT_L(0); PG8_BAR; PG8_MMA(0, 0, At, B0); PG8_MMA(0, 1, At, B1); PG8_BAR; PG8_SCHED;
;             PG8_LDA(At, 0, 1); PG8_STAGE(PG8_SB(0, 0), b2, voffB[0]); PG8_STAGE(PG8_SB(0, 1), b2, voffB[1]); PG8_STAGE(PG8_SA(0, 0), a2, vA2[0]);
;             PG8_WAIT_V(8); PG8_WAIT_L(0); PG8_BAR; PG8_MMA(1, 0, At, B0); PG8_MMA(1, 1, At, B1); PG8_BAR; PG8_SCHED;
.Lpk0_1060:
	v_add_u32_e32 v2, s12, v210
	v_add_u32_e32 v14, s62, v210
	s_add_u32 s28, s30, 0x100
	ds_read_b128 v[18:21], v2
	ds_read_b128 v[22:25], v2 offset:1024
	ds_read_b128 v[26:29], v2 offset:2048
	ds_read_b128 v[30:33], v2 offset:3072
	ds_read_b128 v[2:5], v14
	ds_read_b128 v[6:9], v14 offset:1024
	ds_read_b128 v[10:13], v14 offset:2048
	ds_read_b128 v[14:17], v14 offset:3072
	s_addc_u32 s29, s31, 0
	s_and_b64 s[42:43], s[40:41], exec
	s_cselect_b32 s42, 0, s28
	s_cselect_b32 s43, 0, s29
	s_add_u32 s42, s6, s42
	s_addc_u32 s43, s7, s43
	s_and_b64 s[40:41], s[40:41], exec
	s_cselect_b32 s41, s25, s68
	s_cselect_b32 s40, s24, s21
	v_lshl_add_u64 v[204:205], v[196:197], 0, s[30:31]
	s_add_i32 m0, s52, 0xc000
	ds_read_b128 v[222:225], v213
	ds_read_b128 v[226:229], v213 offset:1024
	ds_read_b128 v[230:233], v213 offset:2048
	ds_read_b128 v[234:237], v213 offset:3072
	ds_read_b128 v[238:241], v213 offset:4096
	ds_read_b128 v[242:245], v213 offset:5120
	ds_read_b128 v[246:249], v213 offset:6144
	ds_read_b128 v[250:253], v213 offset:7168
	global_load_lds_dwordx4 v[204:205], off
	v_lshl_add_u64 v[204:205], v[194:195], 0, s[30:31]
	s_add_i32 m0, s52, 0xe000
	s_nop 0
	global_load_lds_dwordx4 v[204:205], off
	s_waitcnt vmcnt(8)
	s_waitcnt lgkmcnt(0)
	s_setprio 1
	v_mfma_scale_f32_16x16x128_f8f6f4 v[142:145], v[18:25], v[222:229], 0, v214, v214 op_sel_hi:[0,0,0]
	v_mfma_scale_f32_16x16x128_f8f6f4 v[138:141], v[26:33], v[222:229], 0, v214, v214 op_sel_hi:[0,0,0]
	v_mfma_scale_f32_16x16x128_f8f6f4 v[134:137], v[18:25], v[230:237], 0, v214, v214 op_sel_hi:[0,0,0]
	v_mfma_scale_f32_16x16x128_f8f6f4 v[130:133], v[26:33], v[230:237], 0, v214, v214 op_sel_hi:[0,0,0]
	v_mfma_scale_f32_16x16x128_f8f6f4 v[126:129], v[18:25], v[238:245], 0, v214, v214 op_sel_hi:[0,0,0]
	v_mfma_scale_f32_16x16x128_f8f6f4 v[122:125], v[26:33], v[238:245], 0, v214, v214 op_sel_hi:[0,0,0]
	v_mfma_scale_f32_16x16x128_f8f6f4 v[118:121], v[18:25], v[246:253], 0, v214, v214 op_sel_hi:[0,0,0]
	v_mfma_scale_f32_16x16x128_f8f6f4 v[114:117], v[26:33], v[246:253], 0, v214, v214 op_sel_hi:[0,0,0]
	s_nop 3
	s_setprio 0
	s_setprio 1
	v_mfma_scale_f32_16x16x128_f8f6f4 v[110:113], v[2:9], v[222:229], 0, v214, v214 op_sel_hi:[0,0,0]
	v_mfma_scale_f32_16x16x128_f8f6f4 v[106:109], v[10:17], v[222:229], 0, v214, v214 op_sel_hi:[0,0,0]
	v_mfma_scale_f32_16x16x128_f8f6f4 v[102:105], v[2:9], v[230:237], 0, v214, v214 op_sel_hi:[0,0,0]
	v_mfma_scale_f32_16x16x128_f8f6f4 v[98:101], v[10:17], v[230:237], 0, v214, v214 op_sel_hi:[0,0,0]
	v_mfma_scale_f32_16x16x128_f8f6f4 v[94:97], v[2:9], v[238:245], 0, v214, v214 op_sel_hi:[0,0,0]
	v_mfma_scale_f32_16x16x128_f8f6f4 v[90:93], v[10:17], v[238:245], 0, v214, v214 op_sel_hi:[0,0,0]
	v_mfma_scale_f32_16x16x128_f8f6f4 v[86:89], v[2:9], v[246:253], 0, v214, v214 op_sel_hi:[0,0,0]
	v_mfma_scale_f32_16x16x128_f8f6f4 v[82:85], v[10:17], v[246:253], 0, v214, v214 op_sel_hi:[0,0,0]
	s_setprio 0
	s_barrier
	s_add_i32 s30, s12, s48
	v_lshl_add_u64 v[204:205], s[40:41], 0, v[162:163]
	s_mov_b32 m0, s30
	ds_read_b128 v[222:225], v213 offset:16384
	ds_read_b128 v[226:229], v213 offset:17408
	ds_read_b128 v[230:233], v213 offset:18432
	ds_read_b128 v[234:237], v213 offset:19456
	ds_read_b128 v[238:241], v213 offset:20480
	ds_read_b128 v[242:245], v213 offset:21504
	ds_read_b128 v[246:249], v213 offset:22528
	ds_read_b128 v[250:253], v213 offset:23552
	global_load_lds_dwordx4 v[204:205], off
	v_lshl_add_u64 v[204:205], s[40:41], 0, v[164:165]
	s_add_i32 m0, s30, 0x2000
	s_add_i32 s30, s62, s48
	global_load_lds_dwordx4 v[204:205], off
	v_lshl_add_u64 v[204:205], s[40:41], 0, v[166:167]
	s_mov_b32 m0, s30
	v_mov_b32_e32 v203, v171
	global_load_lds_dwordx4 v[204:205], off
	v_lshl_add_u64 v[204:205], s[40:41], 0, v[168:169]
	s_add_i32 m0, s30, 0x2000
	s_nop 0
	global_load_lds_dwordx4 v[204:205], off
	s_mov_b32 m0, s52
	v_lshl_add_u64 v[204:205], s[42:43], 0, v[170:171]
	global_load_lds_dwordx4 v170, s[42:43]
	s_mov_b32 m0, s53
	s_nop 0
	global_load_lds_dwordx4 v202, s[42:43]
	s_waitcnt vmcnt(8)
	s_waitcnt lgkmcnt(0)
	v_lshl_add_u64 v[202:203], s[42:43], 0, v[202:203]
	s_setprio 1
	v_mfma_scale_f32_16x16x128_f8f6f4 v[78:81], v[18:25], v[222:229], 0, v214, v214 op_sel_hi:[0,0,0]
	v_mfma_scale_f32_16x16x128_f8f6f4 v[74:77], v[26:33], v[222:229], 0, v214, v214 op_sel_hi:[0,0,0]
	v_mfma_scale_f32_16x16x128_f8f6f4 v[70:73], v[18:25], v[230:237], 0, v214, v214 op_sel_hi:[0,0,0]
	v_mfma_scale_f32_16x16x128_f8f6f4 v[66:69], v[26:33], v[230:237], 0, v214, v214 op_sel_hi:[0,0,0]
	v_mfma_scale_f32_16x16x128_f8f6f4 v[62:65], v[18:25], v[238:245], 0, v214, v214 op_sel_hi:[0,0,0]
	v_mfma_scale_f32_16x16x128_f8f6f4 v[58:61], v[26:33], v[238:245], 0, v214, v214 op_sel_hi:[0,0,0]
	v_mfma_scale_f32_16x16x128_f8f6f4 v[54:57], v[18:25], v[246:253], 0, v214, v214 op_sel_hi:[0,0,0]
	v_mfma_scale_f32_16x16x128_f8f6f4 v[50:53], v[26:33], v[246:253], 0, v214, v214 op_sel_hi:[0,0,0]
	s_nop 3
	s_setprio 0
	s_setprio 1
	v_mfma_scale_f32_16x16x128_f8f6f4 v[46:49], v[2:9], v[222:229], 0, v214, v214 op_sel_hi:[0,0,0]
	v_mfma_scale_f32_16x16x128_f8f6f4 v[42:45], v[10:17], v[222:229], 0, v214, v214 op_sel_hi:[0,0,0]
	v_mfma_scale_f32_16x16x128_f8f6f4 v[38:41], v[2:9], v[230:237], 0, v214, v214 op_sel_hi:[0,0,0]
	v_mfma_scale_f32_16x16x128_f8f6f4 v[34:37], v[10:17], v[230:237], 0, v214, v214 op_sel_hi:[0,0,0]
	v_mfma_scale_f32_16x16x128_f8f6f4 v[146:149], v[2:9], v[238:245], 0, v214, v214 op_sel_hi:[0,0,0]
	v_mfma_scale_f32_16x16x128_f8f6f4 v[150:153], v[10:17], v[238:245], 0, v214, v214 op_sel_hi:[0,0,0]
	v_mfma_scale_f32_16x16x128_f8f6f4 v[154:157], v[2:9], v[246:253], 0, v214, v214 op_sel_hi:[0,0,0]
	v_mfma_scale_f32_16x16x128_f8f6f4 v[158:161], v[10:17], v[246:253], 0, v214, v214 op_sel_hi:[0,0,0]
	s_setprio 0
	s_barrier
; #define PG8_STAGE(bufoff, gbase, voff) do { _Pragma("unroll") for (int _i = 0; _i < 2; ++_i) \
;         __builtin_amdgcn_global_load_lds((const unsigned*)((const char*)(gbase) + (voff)[_i]), (PG8_LAS unsigned*)(lds + (bufoff) + ldsw + _i * 8192), 16, 0, 0); } while (0)
; #define PG8_WAIT_V(n) asm volatile("s_waitcnt vmcnt(" #n ")" ::: "memory")
; #define PG8_WAIT_L(n) asm volatile("s_waitcnt lgkmcnt(" #n ")" ::: "memory")
; #define PG8_BAR __builtin_amdgcn_s_barrier()
; #define PG8_SCHED __builtin_amdgcn_sched_barrier(0)
; template <class Epi, class Sched, bool ALIGN_EPI = true, bool F8 = false>
; __device__ __forceinline__ void gemm_phase(PG8_LAS unsigned char* lds, const Sched& S, const Epi& E) {
;     ...
;             PG8_LDB(B0, 1, 0); PG8_LDB(B1, 1, 1); PG8_SCHED; PG8_LDA(At, 1, 0); PG8_STAGE(PG8_SA(0, 1), a2, vA2[1]);
;             PG8_WAIT_V(8); PG8_WAIT_L(0); PG8_BAR; PG8_MMA(0, 0, At, B0); PG8_MMA(0, 1, At, B1); PG8_BAR; PG8_SCHED;
;             PG8_LDA(At, 1, 1); PG8_STAGE(PG8_SB(1, 0), b3, voffB[0]); PG8_STAGE(PG8_SB(1, 1), b3, voffB[1]); PG8_STAGE(PG8_SA(1, 0), a3, vA2[0]);
;             PG8_WAIT_V(8); PG8_WAIT_L(0); PG8_BAR; PG8_MMA(1, 0, At, B0); PG8_MMA(1, 1, At, B1); PG8_BAR; PG8_SCHED;
	s_add_i32 s70, 0, 0x18000
	s_add_i32 s71, 0, 0x1c000
	v_add_u32_e32 v14, s70, v210
	v_add_u32_e32 v30, s71, v210
	ds_read_b128 v[2:5], v14
	ds_read_b128 v[6:9], v14 offset:1024
	ds_read_b128 v[10:13], v14 offset:2048
	ds_read_b128 v[14:17], v14 offset:3072
	ds_read_b128 v[18:21], v30
	ds_read_b128 v[22:25], v30 offset:1024
	ds_read_b128 v[26:29], v30 offset:2048
	ds_read_b128 v[30:33], v30 offset:3072
	s_mov_b32 m0, s58
	v_lshl_add_u64 v[200:201], s[42:43], 0, v[200:201]
	ds_read_b128 v[222:225], v213 offset:32768
	ds_read_b128 v[226:229], v213 offset:33792
	ds_read_b128 v[230:233], v213 offset:34816
	ds_read_b128 v[234:237], v213 offset:35840
	ds_read_b128 v[238:241], v213 offset:36864
	ds_read_b128 v[242:245], v213 offset:37888
	ds_read_b128 v[246:249], v213 offset:38912
	ds_read_b128 v[250:253], v213 offset:39936
	global_load_lds_dwordx4 v[200:201], off
	v_lshl_add_u64 v[198:199], s[42:43], 0, v[198:199]
	s_mov_b32 m0, s59
	s_nop 0
	global_load_lds_dwordx4 v[198:199], off
	s_waitcnt vmcnt(8)
	s_waitcnt lgkmcnt(0)
	s_setprio 1
	v_mfma_scale_f32_16x16x128_f8f6f4 v[142:145], v[2:9], v[222:229], v[142:145], v214, v214 op_sel_hi:[0,0,0]
	v_mfma_scale_f32_16x16x128_f8f6f4 v[138:141], v[10:17], v[222:229], v[138:141], v214, v214 op_sel_hi:[0,0,0]
	v_mfma_scale_f32_16x16x128_f8f6f4 v[134:137], v[2:9], v[230:237], v[134:137], v214, v214 op_sel_hi:[0,0,0]
	v_mfma_scale_f32_16x16x128_f8f6f4 v[130:133], v[10:17], v[230:237], v[130:133], v214, v214 op_sel_hi:[0,0,0]
	v_mfma_scale_f32_16x16x128_f8f6f4 v[126:129], v[2:9], v[238:245], v[126:129], v214, v214 op_sel_hi:[0,0,0]
	v_mfma_scale_f32_16x16x128_f8f6f4 v[122:125], v[10:17], v[238:245], v[122:125], v214, v214 op_sel_hi:[0,0,0]
	v_mfma_scale_f32_16x16x128_f8f6f4 v[118:121], v[2:9], v[246:253], v[118:121], v214, v214 op_sel_hi:[0,0,0]
	v_mfma_scale_f32_16x16x128_f8f6f4 v[114:117], v[10:17], v[246:253], v[114:117], v214, v214 op_sel_hi:[0,0,0]
	s_nop 3
	s_setprio 0
	s_setprio 1
	v_mfma_scale_f32_16x16x128_f8f6f4 v[110:113], v[18:25], v[222:229], v[110:113], v214, v214 op_sel_hi:[0,0,0]
	v_mfma_scale_f32_16x16x128_f8f6f4 v[106:109], v[26:33], v[222:229], v[106:109], v214, v214 op_sel_hi:[0,0,0]
	v_mfma_scale_f32_16x16x128_f8f6f4 v[102:105], v[18:25], v[230:237], v[102:105], v214, v214 op_sel_hi:[0,0,0]
	v_mfma_scale_f32_16x16x128_f8f6f4 v[98:101], v[26:33], v[230:237], v[98:101], v214, v214 op_sel_hi:[0,0,0]
	v_mfma_scale_f32_16x16x128_f8f6f4 v[94:97], v[18:25], v[238:245], v[94:97], v214, v214 op_sel_hi:[0,0,0]
	v_mfma_scale_f32_16x16x128_f8f6f4 v[90:93], v[26:33], v[238:245], v[90:93], v214, v214 op_sel_hi:[0,0,0]
	v_mfma_scale_f32_16x16x128_f8f6f4 v[86:89], v[18:25], v[246:253], v[86:89], v214, v214 op_sel_hi:[0,0,0]
	v_mfma_scale_f32_16x16x128_f8f6f4 v[82:85], v[26:33], v[246:253], v[82:85], v214, v214 op_sel_hi:[0,0,0]
	s_setprio 0
	s_barrier
	s_add_u32 s30, s40, 0x8000
	s_addc_u32 s31, s41, 0
	s_add_i32 s40, s70, s48
	v_lshl_add_u64 v[198:199], s[30:31], 0, v[162:163]
	s_mov_b32 m0, s40
	ds_read_b128 v[222:225], v213 offset:49152
	ds_read_b128 v[226:229], v213 offset:50176
	ds_read_b128 v[230:233], v213 offset:51200
	ds_read_b128 v[234:237], v213 offset:52224
	ds_read_b128 v[238:241], v213 offset:53248
	ds_read_b128 v[242:245], v213 offset:54272
	ds_read_b128 v[246:249], v213 offset:55296
	ds_read_b128 v[250:253], v213 offset:56320
	global_load_lds_dwordx4 v[198:199], off
	v_lshl_add_u64 v[198:199], s[30:31], 0, v[164:165]
	s_add_i32 m0, s40, 0x2000
	s_add_i32 s40, s71, s48
	global_load_lds_dwordx4 v[198:199], off
	v_lshl_add_u64 v[198:199], s[30:31], 0, v[166:167]
	s_mov_b32 m0, s40
	s_nop 0
	global_load_lds_dwordx4 v[198:199], off
	v_lshl_add_u64 v[198:199], s[30:31], 0, v[168:169]
	s_add_i32 m0, s40, 0x2000
	s_nop 0
	global_load_lds_dwordx4 v[198:199], off
	v_lshl_add_u64 v[198:199], v[204:205], 0, s[18:19]
	s_mov_b32 m0, s60
	s_nop 0
	global_load_lds_dwordx4 v[198:199], off
	v_lshl_add_u64 v[198:199], v[202:203], 0, s[18:19]
	s_mov_b32 m0, s61
	s_nop 0
	global_load_lds_dwordx4 v[198:199], off
	s_waitcnt vmcnt(8)
	s_waitcnt lgkmcnt(0)
	s_setprio 1
	v_mfma_scale_f32_16x16x128_f8f6f4 v[78:81], v[2:9], v[222:229], v[78:81], v214, v214 op_sel_hi:[0,0,0]
	v_mfma_scale_f32_16x16x128_f8f6f4 v[74:77], v[10:17], v[222:229], v[74:77], v214, v214 op_sel_hi:[0,0,0]
	v_mfma_scale_f32_16x16x128_f8f6f4 v[70:73], v[2:9], v[230:237], v[70:73], v214, v214 op_sel_hi:[0,0,0]
	v_mfma_scale_f32_16x16x128_f8f6f4 v[66:69], v[10:17], v[230:237], v[66:69], v214, v214 op_sel_hi:[0,0,0]
	v_mfma_scale_f32_16x16x128_f8f6f4 v[62:65], v[2:9], v[238:245], v[62:65], v214, v214 op_sel_hi:[0,0,0]
	v_mfma_scale_f32_16x16x128_f8f6f4 v[58:61], v[10:17], v[238:245], v[58:61], v214, v214 op_sel_hi:[0,0,0]
	v_mfma_scale_f32_16x16x128_f8f6f4 v[54:57], v[2:9], v[246:253], v[54:57], v214, v214 op_sel_hi:[0,0,0]
	v_mfma_scale_f32_16x16x128_f8f6f4 v[50:53], v[10:17], v[246:253], v[50:53], v214, v214 op_sel_hi:[0,0,0]
	s_nop 3
	s_setprio 0
	s_setprio 1
	v_mfma_scale_f32_16x16x128_f8f6f4 v[46:49], v[18:25], v[222:229], v[46:49], v214, v214 op_sel_hi:[0,0,0]
	v_mfma_scale_f32_16x16x128_f8f6f4 v[42:45], v[26:33], v[222:229], v[42:45], v214, v214 op_sel_hi:[0,0,0]
	v_mfma_scale_f32_16x16x128_f8f6f4 v[38:41], v[18:25], v[230:237], v[38:41], v214, v214 op_sel_hi:[0,0,0]
	v_mfma_scale_f32_16x16x128_f8f6f4 v[34:37], v[26:33], v[230:237], v[34:37], v214, v214 op_sel_hi:[0,0,0]
	v_mfma_scale_f32_16x16x128_f8f6f4 v[146:149], v[18:25], v[238:245], v[146:149], v214, v214 op_sel_hi:[0,0,0]
	v_mfma_scale_f32_16x16x128_f8f6f4 v[150:153], v[26:33], v[238:245], v[150:153], v214, v214 op_sel_hi:[0,0,0]
	v_mfma_scale_f32_16x16x128_f8f6f4 v[154:157], v[18:25], v[246:253], v[154:157], v214, v214 op_sel_hi:[0,0,0]
	v_mfma_scale_f32_16x16x128_f8f6f4 v[158:161], v[26:33], v[246:253], v[158:161], v214, v214 op_sel_hi:[0,0,0]
	s_setprio 0
	s_barrier
	s_add_i32 s69, s69, 2
	s_add_u32 s21, s21, 0x10000
	s_addc_u32 s68, s68, 0
	s_cmp_gt_u32 s69, 13
	s_cbranch_scc1 .LBB0_1062
	s_mov_b64 s[30:31], s[28:29]
	s_branch .LBB0_1058

; #define PG8_STAGE(bufoff, gbase, voff) do { _Pragma("unroll") for (int _i = 0; _i < 2; ++_i) \
;         __builtin_amdgcn_global_load_lds((const unsigned*)((const char*)(gbase) + (voff)[_i]), (PG8_LAS unsigned*)(lds + (bufoff) + ldsw + _i * 8192), 16, 0, 0); } while (0)
; #define PG8_WAIT_V(n) asm volatile("s_waitcnt vmcnt(" #n ")" ::: "memory")
; #define PG8_WAIT_L(n) asm volatile("s_waitcnt lgkmcnt(" #n ")" ::: "memory")
; #define PG8_BAR __builtin_amdgcn_s_barrier()
; #define PG8_SCHED __builtin_amdgcn_sched_barrier(0)
; template <class Epi, class Sched, bool ALIGN_EPI = true, bool F8 = false>
; __device__ __forceinline__ void gemm_phase(PG8_LAS unsigned char* lds, const Sched& S, const Epi& E) {
;     ...
;             if constexpr (Sched::GATHER) { if (last && has_next) S.a_off(nxt, Rs, Cs, voffAn); }
;             const char* a1 = cA + (size_t)(t + 1) * kstep;
;             const char* a2 = last ? nA : cA + (size_t)(t + 2) * kstep; const char* b2 = last ? nB : cB + (size_t)(t + 2) * kstepB;
;             const char* a3 = a2 + kstep; const char* b3 = b2 + kstepB;
;             unsigned vA2[2][2];
; #pragma unroll
;             for (int h = 0; h < 2; ++h)
; #pragma unroll
;                 for (int i = 0; i < 2; ++i) { if constexpr (Sched::GATHER) vA2[h][i] = (last && has_next) ? voffAn[h][i] : voffA[h][i]; else vA2[h][i] = voffA[h][i]; }
;             PG8_LDB(B0, 0, 0); PG8_LDB(B1, 0, 1); PG8_SCHED; PG8_LDA(At, 0, 0); PG8_STAGE(PG8_SA(1, 1), a1, voffA[1]);
;             PG8_WAIT_V(8); PG8_WAIT_L(0); PG8_BAR; PG8_MMA(0, 0, At, B0); PG8_MMA(0, 1, At, B1); PG8_BAR; PG8_SCHED;
;             PG8_LDA(At, 0, 1); PG8_STAGE(PG8_SB(0, 0), b2, voffB[0]); PG8_STAGE(PG8_SB(0, 1), b2, voffB[1]); PG8_STAGE(PG8_SA(0, 0), a2, vA2[0]);
;             PG8_WAIT_V(8); PG8_WAIT_L(0); PG8_BAR; PG8_MMA(1, 0, At, B0); PG8_MMA(1, 1, At, B1); PG8_BAR; PG8_SCHED;
;             PG8_LDB(B0, 1, 0); PG8_LDB(B1, 1, 1); PG8_SCHED; PG8_LDA(At, 1, 0); PG8_STAGE(PG8_SA(0, 1), a2, vA2[1]);
;             PG8_WAIT_V(8); PG8_WAIT_L(0); PG8_BAR; PG8_MMA(0, 0, At, B0); PG8_MMA(0, 1, At, B1); PG8_BAR; PG8_SCHED;
.Lpk1_1060:
	v_add_u32_e32 v2, s12, v210
	v_add_u32_e32 v14, s62, v210
	s_add_u32 s28, s30, 0x100
	ds_read_b128 v[18:21], v2
	ds_read_b128 v[22:25], v2 offset:1024
	ds_read_b128 v[26:29], v2 offset:2048
	ds_read_b128 v[30:33], v2 offset:3072
	ds_read_b128 v[2:5], v14
	ds_read_b128 v[6:9], v14 offset:1024
	ds_read_b128 v[10:13], v14 offset:2048
	ds_read_b128 v[14:17], v14 offset:3072
	s_addc_u32 s29, s31, 0
	s_and_b64 s[42:43], s[40:41], exec
	s_cselect_b32 s42, 0, s28
	s_cselect_b32 s43, 0, s29
	s_add_u32 s42, s6, s42
	s_addc_u32 s43, s7, s43
	s_and_b64 s[40:41], s[40:41], exec
	s_cselect_b32 s41, s25, s68
	s_cselect_b32 s40, s24, s21
	v_lshl_add_u64 v[204:205], v[196:197], 0, s[30:31]
	s_add_i32 m0, s52, 0xc000
	ds_read_b128 v[222:225], v213
	ds_read_b128 v[226:229], v213 offset:1024
	ds_read_b128 v[230:233], v213 offset:2048
	ds_read_b128 v[234:237], v213 offset:3072
	ds_read_b128 v[238:241], v213 offset:4096
	ds_read_b128 v[242:245], v213 offset:5120
	ds_read_b128 v[246:249], v213 offset:6144
	ds_read_b128 v[250:253], v213 offset:7168
	global_load_lds_dwordx4 v[204:205], off
	v_lshl_add_u64 v[204:205], v[194:195], 0, s[30:31]
	s_add_i32 m0, s52, 0xe000
	s_nop 0
	global_load_lds_dwordx4 v[204:205], off
	s_waitcnt vmcnt(8)
	s_waitcnt lgkmcnt(0)
	s_barrier
	s_setprio 2
	v_mfma_scale_f32_16x16x128_f8f6f4 v[142:145], v[18:25], v[222:229], 0, v214, v214 op_sel_hi:[0,0,0]
	v_mfma_scale_f32_16x16x128_f8f6f4 v[138:141], v[26:33], v[222:229], 0, v214, v214 op_sel_hi:[0,0,0]
	v_mfma_scale_f32_16x16x128_f8f6f4 v[134:137], v[18:25], v[230:237], 0, v214, v214 op_sel_hi:[0,0,0]
	v_mfma_scale_f32_16x16x128_f8f6f4 v[130:133], v[26:33], v[230:237], 0, v214, v214 op_sel_hi:[0,0,0]
	v_mfma_scale_f32_16x16x128_f8f6f4 v[126:129], v[18:25], v[238:245], 0, v214, v214 op_sel_hi:[0,0,0]
	v_mfma_scale_f32_16x16x128_f8f6f4 v[122:125], v[26:33], v[238:245], 0, v214, v214 op_sel_hi:[0,0,0]
	v_mfma_scale_f32_16x16x128_f8f6f4 v[118:121], v[18:25], v[246:253], 0, v214, v214 op_sel_hi:[0,0,0]
	v_mfma_scale_f32_16x16x128_f8f6f4 v[114:117], v[26:33], v[246:253], 0, v214, v214 op_sel_hi:[0,0,0]
	s_nop 3
	s_setprio 0
	s_setprio 2
	v_mfma_scale_f32_16x16x128_f8f6f4 v[110:113], v[2:9], v[222:229], 0, v214, v214 op_sel_hi:[0,0,0]
	v_mfma_scale_f32_16x16x128_f8f6f4 v[106:109], v[10:17], v[222:229], 0, v214, v214 op_sel_hi:[0,0,0]
	v_mfma_scale_f32_16x16x128_f8f6f4 v[102:105], v[2:9], v[230:237], 0, v214, v214 op_sel_hi:[0,0,0]
	v_mfma_scale_f32_16x16x128_f8f6f4 v[98:101], v[10:17], v[230:237], 0, v214, v214 op_sel_hi:[0,0,0]
	v_mfma_scale_f32_16x16x128_f8f6f4 v[94:97], v[2:9], v[238:245], 0, v214, v214 op_sel_hi:[0,0,0]
	v_mfma_scale_f32_16x16x128_f8f6f4 v[90:93], v[10:17], v[238:245], 0, v214, v214 op_sel_hi:[0,0,0]
	v_mfma_scale_f32_16x16x128_f8f6f4 v[86:89], v[2:9], v[246:253], 0, v214, v214 op_sel_hi:[0,0,0]
	v_mfma_scale_f32_16x16x128_f8f6f4 v[82:85], v[10:17], v[246:253], 0, v214, v214 op_sel_hi:[0,0,0]
	s_setprio 0
	s_add_i32 s30, s12, s48
	v_lshl_add_u64 v[204:205], s[40:41], 0, v[162:163]
	s_mov_b32 m0, s30
	ds_read_b128 v[222:225], v213 offset:16384
	ds_read_b128 v[226:229], v213 offset:17408
	ds_read_b128 v[230:233], v213 offset:18432
	ds_read_b128 v[234:237], v213 offset:19456
	ds_read_b128 v[238:241], v213 offset:20480
	ds_read_b128 v[242:245], v213 offset:21504
	ds_read_b128 v[246:249], v213 offset:22528
	ds_read_b128 v[250:253], v213 offset:23552
	global_load_lds_dwordx4 v[204:205], off
	v_lshl_add_u64 v[204:205], s[40:41], 0, v[164:165]
	s_add_i32 m0, s30, 0x2000
	s_add_i32 s30, s62, s48
	global_load_lds_dwordx4 v[204:205], off
	v_lshl_add_u64 v[204:205], s[40:41], 0, v[166:167]
	s_mov_b32 m0, s30
	v_mov_b32_e32 v203, v171
	global_load_lds_dwordx4 v[204:205], off
	v_lshl_add_u64 v[204:205], s[40:41], 0, v[168:169]
	s_add_i32 m0, s30, 0x2000
	s_nop 0
	global_load_lds_dwordx4 v[204:205], off
	s_mov_b32 m0, s52
	v_lshl_add_u64 v[204:205], s[42:43], 0, v[170:171]
	global_load_lds_dwordx4 v170, s[42:43]
	s_mov_b32 m0, s53
	s_nop 0
	global_load_lds_dwordx4 v202, s[42:43]
	s_waitcnt vmcnt(8)
	s_waitcnt lgkmcnt(0)
	v_lshl_add_u64 v[202:203], s[42:43], 0, v[202:203]
	s_barrier
	s_setprio 2
	v_mfma_scale_f32_16x16x128_f8f6f4 v[78:81], v[18:25], v[222:229], 0, v214, v214 op_sel_hi:[0,0,0]
	v_mfma_scale_f32_16x16x128_f8f6f4 v[74:77], v[26:33], v[222:229], 0, v214, v214 op_sel_hi:[0,0,0]
	v_mfma_scale_f32_16x16x128_f8f6f4 v[70:73], v[18:25], v[230:237], 0, v214, v214 op_sel_hi:[0,0,0]
	v_mfma_scale_f32_16x16x128_f8f6f4 v[66:69], v[26:33], v[230:237], 0, v214, v214 op_sel_hi:[0,0,0]
	v_mfma_scale_f32_16x16x128_f8f6f4 v[62:65], v[18:25], v[238:245], 0, v214, v214 op_sel_hi:[0,0,0]
	v_mfma_scale_f32_16x16x128_f8f6f4 v[58:61], v[26:33], v[238:245], 0, v214, v214 op_sel_hi:[0,0,0]
	v_mfma_scale_f32_16x16x128_f8f6f4 v[54:57], v[18:25], v[246:253], 0, v214, v214 op_sel_hi:[0,0,0]
	v_mfma_scale_f32_16x16x128_f8f6f4 v[50:53], v[26:33], v[246:253], 0, v214, v214 op_sel_hi:[0,0,0]
	s_nop 3
	s_setprio 0
	s_setprio 2
	v_mfma_scale_f32_16x16x128_f8f6f4 v[46:49], v[2:9], v[222:229], 0, v214, v214 op_sel_hi:[0,0,0]
	v_mfma_scale_f32_16x16x128_f8f6f4 v[42:45], v[10:17], v[222:229], 0, v214, v214 op_sel_hi:[0,0,0]
	v_mfma_scale_f32_16x16x128_f8f6f4 v[38:41], v[2:9], v[230:237], 0, v214, v214 op_sel_hi:[0,0,0]
	v_mfma_scale_f32_16x16x128_f8f6f4 v[34:37], v[10:17], v[230:237], 0, v214, v214 op_sel_hi:[0,0,0]
	v_mfma_scale_f32_16x16x128_f8f6f4 v[146:149], v[2:9], v[238:245], 0, v214, v214 op_sel_hi:[0,0,0]
	v_mfma_scale_f32_16x16x128_f8f6f4 v[150:153], v[10:17], v[238:245], 0, v214, v214 op_sel_hi:[0,0,0]
	v_mfma_scale_f32_16x16x128_f8f6f4 v[154:157], v[2:9], v[246:253], 0, v214, v214 op_sel_hi:[0,0,0]
	v_mfma_scale_f32_16x16x128_f8f6f4 v[158:161], v[10:17], v[246:253], 0, v214, v214 op_sel_hi:[0,0,0]
	s_setprio 0
	s_add_i32 s70, 0, 0x18000
	s_add_i32 s71, 0, 0x1c000
	v_add_u32_e32 v14, s70, v210
	v_add_u32_e32 v30, s71, v210
	ds_read_b128 v[2:5], v14
	ds_read_b128 v[6:9], v14 offset:1024
	ds_read_b128 v[10:13], v14 offset:2048
	ds_read_b128 v[14:17], v14 offset:3072
	ds_read_b128 v[18:21], v30
	ds_read_b128 v[22:25], v30 offset:1024
	ds_read_b128 v[26:29], v30 offset:2048
	ds_read_b128 v[30:33], v30 offset:3072
	s_mov_b32 m0, s58
	v_lshl_add_u64 v[200:201], s[42:43], 0, v[200:201]
	ds_read_b128 v[222:225], v213 offset:32768
	ds_read_b128 v[226:229], v213 offset:33792
	ds_read_b128 v[230:233], v213 offset:34816
	ds_read_b128 v[234:237], v213 offset:35840
	ds_read_b128 v[238:241], v213 offset:36864
	ds_read_b128 v[242:245], v213 offset:37888
	ds_read_b128 v[246:249], v213 offset:38912
	ds_read_b128 v[250:253], v213 offset:39936
	global_load_lds_dwordx4 v[200:201], off
	v_lshl_add_u64 v[198:199], s[42:43], 0, v[198:199]
	s_mov_b32 m0, s59
	s_nop 0
	global_load_lds_dwordx4 v[198:199], off
	s_waitcnt vmcnt(8)
	s_waitcnt lgkmcnt(0)
	s_barrier
; #define PG8_STAGE(bufoff, gbase, voff) do { _Pragma("unroll") for (int _i = 0; _i < 2; ++_i) \
;         __builtin_amdgcn_global_load_lds((const unsigned*)((const char*)(gbase) + (voff)[_i]), (PG8_LAS unsigned*)(lds + (bufoff) + ldsw + _i * 8192), 16, 0, 0); } while (0)
; #define PG8_WAIT_V(n) asm volatile("s_waitcnt vmcnt(" #n ")" ::: "memory")
; #define PG8_WAIT_L(n) asm volatile("s_waitcnt lgkmcnt(" #n ")" ::: "memory")
; #define PG8_BAR __builtin_amdgcn_s_barrier()
; #define PG8_SCHED __builtin_amdgcn_sched_barrier(0)
; template <class Epi, class Sched, bool ALIGN_EPI = true, bool F8 = false>
; __device__ __forceinline__ void gemm_phase(PG8_LAS unsigned char* lds, const Sched& S, const Epi& E) {
;     ...
;             PG8_WAIT_V(8); PG8_WAIT_L(0); PG8_BAR; PG8_MMA(0, 0, At, B0); PG8_MMA(0, 1, At, B1); PG8_BAR; PG8_SCHED;
;             PG8_LDA(At, 1, 1); PG8_STAGE(PG8_SB(1, 0), b3, voffB[0]); PG8_STAGE(PG8_SB(1, 1), b3, voffB[1]); PG8_STAGE(PG8_SA(1, 0), a3, vA2[0]);
;             PG8_WAIT_V(8); PG8_WAIT_L(0); PG8_BAR; PG8_MMA(1, 0, At, B0); PG8_MMA(1, 1, At, B1); PG8_BAR; PG8_SCHED;
	s_setprio 2
	v_mfma_scale_f32_16x16x128_f8f6f4 v[142:145], v[2:9], v[222:229], v[142:145], v214, v214 op_sel_hi:[0,0,0]
	v_mfma_scale_f32_16x16x128_f8f6f4 v[138:141], v[10:17], v[222:229], v[138:141], v214, v214 op_sel_hi:[0,0,0]
	v_mfma_scale_f32_16x16x128_f8f6f4 v[134:137], v[2:9], v[230:237], v[134:137], v214, v214 op_sel_hi:[0,0,0]
	v_mfma_scale_f32_16x16x128_f8f6f4 v[130:133], v[10:17], v[230:237], v[130:133], v214, v214 op_sel_hi:[0,0,0]
	v_mfma_scale_f32_16x16x128_f8f6f4 v[126:129], v[2:9], v[238:245], v[126:129], v214, v214 op_sel_hi:[0,0,0]
	v_mfma_scale_f32_16x16x128_f8f6f4 v[122:125], v[10:17], v[238:245], v[122:125], v214, v214 op_sel_hi:[0,0,0]
	v_mfma_scale_f32_16x16x128_f8f6f4 v[118:121], v[2:9], v[246:253], v[118:121], v214, v214 op_sel_hi:[0,0,0]
	v_mfma_scale_f32_16x16x128_f8f6f4 v[114:117], v[10:17], v[246:253], v[114:117], v214, v214 op_sel_hi:[0,0,0]
	s_nop 3
	s_setprio 0
	s_setprio 2
	v_mfma_scale_f32_16x16x128_f8f6f4 v[110:113], v[18:25], v[222:229], v[110:113], v214, v214 op_sel_hi:[0,0,0]
	v_mfma_scale_f32_16x16x128_f8f6f4 v[106:109], v[26:33], v[222:229], v[106:109], v214, v214 op_sel_hi:[0,0,0]
	v_mfma_scale_f32_16x16x128_f8f6f4 v[102:105], v[18:25], v[230:237], v[102:105], v214, v214 op_sel_hi:[0,0,0]
	v_mfma_scale_f32_16x16x128_f8f6f4 v[98:101], v[26:33], v[230:237], v[98:101], v214, v214 op_sel_hi:[0,0,0]
	v_mfma_scale_f32_16x16x128_f8f6f4 v[94:97], v[18:25], v[238:245], v[94:97], v214, v214 op_sel_hi:[0,0,0]
	v_mfma_scale_f32_16x16x128_f8f6f4 v[90:93], v[26:33], v[238:245], v[90:93], v214, v214 op_sel_hi:[0,0,0]
	v_mfma_scale_f32_16x16x128_f8f6f4 v[86:89], v[18:25], v[246:253], v[86:89], v214, v214 op_sel_hi:[0,0,0]
	v_mfma_scale_f32_16x16x128_f8f6f4 v[82:85], v[26:33], v[246:253], v[82:85], v214, v214 op_sel_hi:[0,0,0]
	s_setprio 0
	s_add_u32 s30, s40, 0x8000
	s_addc_u32 s31, s41, 0
	s_add_i32 s40, s70, s48
	v_lshl_add_u64 v[198:199], s[30:31], 0, v[162:163]
	s_mov_b32 m0, s40
	ds_read_b128 v[222:225], v213 offset:49152
	ds_read_b128 v[226:229], v213 offset:50176
	ds_read_b128 v[230:233], v213 offset:51200
	ds_read_b128 v[234:237], v213 offset:52224
	ds_read_b128 v[238:241], v213 offset:53248
	ds_read_b128 v[242:245], v213 offset:54272
	ds_read_b128 v[246:249], v213 offset:55296
	ds_read_b128 v[250:253], v213 offset:56320
	global_load_lds_dwordx4 v[198:199], off
	v_lshl_add_u64 v[198:199], s[30:31], 0, v[164:165]
	s_add_i32 m0, s40, 0x2000
	s_add_i32 s40, s71, s48
	global_load_lds_dwordx4 v[198:199], off
	v_lshl_add_u64 v[198:199], s[30:31], 0, v[166:167]
	s_mov_b32 m0, s40
	s_nop 0
	global_load_lds_dwordx4 v[198:199], off
	v_lshl_add_u64 v[198:199], s[30:31], 0, v[168:169]
	s_add_i32 m0, s40, 0x2000
	s_nop 0
	global_load_lds_dwordx4 v[198:199], off
	v_lshl_add_u64 v[198:199], v[204:205], 0, s[18:19]
	s_mov_b32 m0, s60
	s_nop 0
	global_load_lds_dwordx4 v[198:199], off
	v_lshl_add_u64 v[198:199], v[202:203], 0, s[18:19]
	s_mov_b32 m0, s61
	s_nop 0
	global_load_lds_dwordx4 v[198:199], off
	s_waitcnt vmcnt(8)
	s_waitcnt lgkmcnt(0)
	s_barrier
	s_setprio 2
	v_mfma_scale_f32_16x16x128_f8f6f4 v[78:81], v[2:9], v[222:229], v[78:81], v214, v214 op_sel_hi:[0,0,0]
	v_mfma_scale_f32_16x16x128_f8f6f4 v[74:77], v[10:17], v[222:229], v[74:77], v214, v214 op_sel_hi:[0,0,0]
	v_mfma_scale_f32_16x16x128_f8f6f4 v[70:73], v[2:9], v[230:237], v[70:73], v214, v214 op_sel_hi:[0,0,0]
	v_mfma_scale_f32_16x16x128_f8f6f4 v[66:69], v[10:17], v[230:237], v[66:69], v214, v214 op_sel_hi:[0,0,0]
	v_mfma_scale_f32_16x16x128_f8f6f4 v[62:65], v[2:9], v[238:245], v[62:65], v214, v214 op_sel_hi:[0,0,0]
	v_mfma_scale_f32_16x16x128_f8f6f4 v[58:61], v[10:17], v[238:245], v[58:61], v214, v214 op_sel_hi:[0,0,0]
	v_mfma_scale_f32_16x16x128_f8f6f4 v[54:57], v[2:9], v[246:253], v[54:57], v214, v214 op_sel_hi:[0,0,0]
	v_mfma_scale_f32_16x16x128_f8f6f4 v[50:53], v[10:17], v[246:253], v[50:53], v214, v214 op_sel_hi:[0,0,0]
	s_nop 3
	s_setprio 0
	s_setprio 2
	v_mfma_scale_f32_16x16x128_f8f6f4 v[46:49], v[18:25], v[222:229], v[46:49], v214, v214 op_sel_hi:[0,0,0]
	v_mfma_scale_f32_16x16x128_f8f6f4 v[42:45], v[26:33], v[222:229], v[42:45], v214, v214 op_sel_hi:[0,0,0]
	v_mfma_scale_f32_16x16x128_f8f6f4 v[38:41], v[18:25], v[230:237], v[38:41], v214, v214 op_sel_hi:[0,0,0]
	v_mfma_scale_f32_16x16x128_f8f6f4 v[34:37], v[26:33], v[230:237], v[34:37], v214, v214 op_sel_hi:[0,0,0]
	v_mfma_scale_f32_16x16x128_f8f6f4 v[146:149], v[18:25], v[238:245], v[146:149], v214, v214 op_sel_hi:[0,0,0]
	v_mfma_scale_f32_16x16x128_f8f6f4 v[150:153], v[26:33], v[238:245], v[150:153], v214, v214 op_sel_hi:[0,0,0]
	v_mfma_scale_f32_16x16x128_f8f6f4 v[154:157], v[18:25], v[246:253], v[154:157], v214, v214 op_sel_hi:[0,0,0]
	v_mfma_scale_f32_16x16x128_f8f6f4 v[158:161], v[26:33], v[246:253], v[158:161], v214, v214 op_sel_hi:[0,0,0]
	s_setprio 0
	s_add_i32 s69, s69, 2
	s_add_u32 s21, s21, 0x10000
	s_addc_u32 s68, s68, 0
	s_cmp_gt_u32 s69, 13
	s_cbranch_scc1 .LBB0_1062
	s_mov_b64 s[30:31], s[28:29]
	s_branch .Lh1_1058

; #define PG8_STAGE(bufoff, gbase, voff) do { _Pragma("unroll") for (int _i = 0; _i < 2; ++_i) \
;         __builtin_amdgcn_global_load_lds((const unsigned*)((const char*)(gbase) + (voff)[_i]), (PG8_LAS unsigned*)(lds + (bufoff) + ldsw + _i * 8192), 16, 0, 0); } while (0)
; #define PG8_WAIT_V(n) asm volatile("s_waitcnt vmcnt(" #n ")" ::: "memory")
; #define PG8_WAIT_L(n) asm volatile("s_waitcnt lgkmcnt(" #n ")" ::: "memory")
; #define PG8_BAR __builtin_amdgcn_s_barrier()
; #define PG8_SCHED __builtin_amdgcn_sched_barrier(0)
; template <class Epi, class Sched, bool ALIGN_EPI = true, bool F8 = false>
; __device__ __forceinline__ void gemm_phase(PG8_LAS unsigned char* lds, const Sched& S, const Epi& E) {
;     ...
;             PG8_LDB(B0, 0, 0); PG8_LDB(B1, 0, 1); PG8_SCHED; PG8_LDA(At, 0, 0); PG8_STAGE(PG8_SA(1, 1), a1, voffA[1]);
;             PG8_WAIT_V(8); PG8_WAIT_L(0); PG8_BAR; PG8_MMA(0, 0, At, B0); PG8_MMA(0, 1, At, B1); PG8_BAR; PG8_SCHED;
;             PG8_LDA(At, 0, 1); PG8_STAGE(PG8_SB(0, 0), b2, voffB[0]); PG8_STAGE(PG8_SB(0, 1), b2, voffB[1]); PG8_STAGE(PG8_SA(0, 0), a2, vA2[0]);
;             PG8_WAIT_V(8); PG8_WAIT_L(0); PG8_BAR; PG8_MMA(1, 0, At, B0); PG8_MMA(1, 1, At, B1); PG8_BAR; PG8_SCHED;
;     ...
;         for (int a = 0; a < 2; ++a)
; #pragma unroll
;             for (int b = 0; b < 2; ++b)
; #pragma unroll
;                 for (int m = 0; m < 4; ++m)
; #pragma unroll
;                     for (int n = 0; n < 2; ++n) acc[a][b][m][n] = (f32x4){0.f, 0.f, 0.f, 0.f};
.LBB0_1137:
	s_add_u32 s23, s26, 0x10000
	s_addc_u32 s67, s27, 0
	s_add_u32 s24, s24, 0x8000
	s_addc_u32 s25, s25, 0
	s_mov_b32 s68, -2
	s_bitcmp1_b32 s3, 2
	s_cbranch_scc1 .Lh1e_33571
.Lpk0_1138:
	ds_read_b128 v[18:21], v189
	ds_read_b128 v[22:25], v189 offset:1024
	ds_read_b128 v[26:29], v189 offset:2048
	ds_read_b128 v[30:33], v189 offset:3072
	ds_read_b128 v[2:5], v190
	ds_read_b128 v[6:9], v190 offset:1024
	ds_read_b128 v[10:13], v190 offset:2048
	ds_read_b128 v[14:17], v190 offset:3072
	s_add_u32 s26, s24, 0x8000
	s_addc_u32 s27, s25, 0
	s_cmp_eq_u32 s68, 4
	s_cselect_b32 s30, s16, s26
	s_cselect_b32 s31, s17, s27
	s_cselect_b32 s28, s18, s23
	s_cselect_b32 s29, s19, s67
	s_add_u32 s26, s30, 0x8000
	s_addc_u32 s27, s31, 0
	v_lshl_add_u64 v[226:227], s[24:25], 0, v[184:185]
	s_add_i32 m0, s44, 0xc000
	ds_read_b128 v[194:197], v191
	ds_read_b128 v[198:201], v191 offset:1024
	ds_read_b128 v[202:205], v191 offset:2048
	ds_read_b128 v[206:209], v191 offset:3072
	ds_read_b128 v[210:213], v191 offset:4096
	ds_read_b128 v[214:217], v191 offset:5120
	ds_read_b128 v[218:221], v191 offset:6144
	ds_read_b128 v[222:225], v191 offset:7168
	global_load_lds_dwordx4 v[226:227], off
	v_lshl_add_u64 v[226:227], s[24:25], 0, v[182:183]
	s_add_i32 m0, s44, 0xe000
	s_nop 0
	global_load_lds_dwordx4 v[226:227], off
	s_waitcnt vmcnt(8)
	s_waitcnt lgkmcnt(0)
	s_setprio 1
	v_mfma_scale_f32_16x16x128_f8f6f4 v[158:161], v[18:25], v[194:201], 0, v192, v192 op_sel_hi:[0,0,0]
	v_mfma_scale_f32_16x16x128_f8f6f4 v[154:157], v[26:33], v[194:201], 0, v192, v192 op_sel_hi:[0,0,0]
	v_mfma_scale_f32_16x16x128_f8f6f4 v[142:145], v[18:25], v[202:209], 0, v192, v192 op_sel_hi:[0,0,0]
	v_mfma_scale_f32_16x16x128_f8f6f4 v[138:141], v[26:33], v[202:209], 0, v192, v192 op_sel_hi:[0,0,0]
	v_mfma_scale_f32_16x16x128_f8f6f4 v[126:129], v[18:25], v[210:217], 0, v192, v192 op_sel_hi:[0,0,0]
	v_mfma_scale_f32_16x16x128_f8f6f4 v[122:125], v[26:33], v[210:217], 0, v192, v192 op_sel_hi:[0,0,0]
	v_mfma_scale_f32_16x16x128_f8f6f4 v[110:113], v[18:25], v[218:225], 0, v192, v192 op_sel_hi:[0,0,0]
	v_mfma_scale_f32_16x16x128_f8f6f4 v[106:109], v[26:33], v[218:225], 0, v192, v192 op_sel_hi:[0,0,0]
	s_nop 3
	s_setprio 0
	s_setprio 1
	v_mfma_scale_f32_16x16x128_f8f6f4 v[150:153], v[2:9], v[194:201], 0, v192, v192 op_sel_hi:[0,0,0]
	v_mfma_scale_f32_16x16x128_f8f6f4 v[146:149], v[10:17], v[194:201], 0, v192, v192 op_sel_hi:[0,0,0]
	v_mfma_scale_f32_16x16x128_f8f6f4 v[134:137], v[2:9], v[202:209], 0, v192, v192 op_sel_hi:[0,0,0]
	v_mfma_scale_f32_16x16x128_f8f6f4 v[130:133], v[10:17], v[202:209], 0, v192, v192 op_sel_hi:[0,0,0]
	v_mfma_scale_f32_16x16x128_f8f6f4 v[118:121], v[2:9], v[210:217], 0, v192, v192 op_sel_hi:[0,0,0]
	v_mfma_scale_f32_16x16x128_f8f6f4 v[114:117], v[10:17], v[210:217], 0, v192, v192 op_sel_hi:[0,0,0]
	v_mfma_scale_f32_16x16x128_f8f6f4 v[102:105], v[2:9], v[218:225], 0, v192, v192 op_sel_hi:[0,0,0]
	v_mfma_scale_f32_16x16x128_f8f6f4 v[98:101], v[10:17], v[218:225], 0, v192, v192 op_sel_hi:[0,0,0]
	s_setprio 0
	s_barrier
	s_add_i32 s69, s53, s43
	v_lshl_add_u64 v[226:227], s[28:29], 0, v[164:165]
	s_mov_b32 m0, s69
	ds_read_b128 v[194:197], v191 offset:16384
	ds_read_b128 v[198:201], v191 offset:17408
	ds_read_b128 v[202:205], v191 offset:18432
	ds_read_b128 v[206:209], v191 offset:19456
	ds_read_b128 v[210:213], v191 offset:20480
	ds_read_b128 v[214:217], v191 offset:21504
	ds_read_b128 v[218:221], v191 offset:22528
	ds_read_b128 v[222:225], v191 offset:23552
	global_load_lds_dwordx4 v[226:227], off
	v_lshl_add_u64 v[228:229], s[28:29], 0, v[166:167]
	s_add_i32 m0, s69, 0x2000
	s_add_i32 s69, s58, s43
	global_load_lds_dwordx4 v[228:229], off
	v_lshl_add_u64 v[226:227], v[226:227], 0, s[4:5]
	s_mov_b32 m0, s69
	s_nop 0
	global_load_lds_dwordx4 v[226:227], off
	v_lshl_add_u64 v[226:227], v[228:229], 0, s[4:5]
	s_add_i32 m0, s69, 0x2000
	s_nop 0
	global_load_lds_dwordx4 v[226:227], off
	v_lshl_add_u64 v[226:227], s[30:31], 0, v[168:169]
	s_mov_b32 m0, s44
	s_nop 0
	global_load_lds_dwordx4 v[226:227], off
	v_lshl_add_u64 v[226:227], s[30:31], 0, v[170:171]
	s_mov_b32 m0, s45
	s_nop 0
	global_load_lds_dwordx4 v[226:227], off
	s_waitcnt vmcnt(8)
	s_waitcnt lgkmcnt(0)
	s_setprio 1
	v_mfma_scale_f32_16x16x128_f8f6f4 v[94:97], v[18:25], v[194:201], 0, v192, v192 op_sel_hi:[0,0,0]
	v_mfma_scale_f32_16x16x128_f8f6f4 v[90:93], v[26:33], v[194:201], 0, v192, v192 op_sel_hi:[0,0,0]
	v_mfma_scale_f32_16x16x128_f8f6f4 v[78:81], v[18:25], v[202:209], 0, v192, v192 op_sel_hi:[0,0,0]
	v_mfma_scale_f32_16x16x128_f8f6f4 v[74:77], v[26:33], v[202:209], 0, v192, v192 op_sel_hi:[0,0,0]
	v_mfma_scale_f32_16x16x128_f8f6f4 v[62:65], v[18:25], v[210:217], 0, v192, v192 op_sel_hi:[0,0,0]
	v_mfma_scale_f32_16x16x128_f8f6f4 v[58:61], v[26:33], v[210:217], 0, v192, v192 op_sel_hi:[0,0,0]
	v_mfma_scale_f32_16x16x128_f8f6f4 v[46:49], v[18:25], v[218:225], 0, v192, v192 op_sel_hi:[0,0,0]
	v_mfma_scale_f32_16x16x128_f8f6f4 v[42:45], v[26:33], v[218:225], 0, v192, v192 op_sel_hi:[0,0,0]
	s_nop 3
	s_setprio 0
	s_setprio 1
	v_mfma_scale_f32_16x16x128_f8f6f4 v[86:89], v[2:9], v[194:201], 0, v192, v192 op_sel_hi:[0,0,0]
	v_mfma_scale_f32_16x16x128_f8f6f4 v[82:85], v[10:17], v[194:201], 0, v192, v192 op_sel_hi:[0,0,0]
	v_mfma_scale_f32_16x16x128_f8f6f4 v[70:73], v[2:9], v[202:209], 0, v192, v192 op_sel_hi:[0,0,0]
	v_mfma_scale_f32_16x16x128_f8f6f4 v[66:69], v[10:17], v[202:209], 0, v192, v192 op_sel_hi:[0,0,0]
	v_mfma_scale_f32_16x16x128_f8f6f4 v[54:57], v[2:9], v[210:217], 0, v192, v192 op_sel_hi:[0,0,0]
	v_mfma_scale_f32_16x16x128_f8f6f4 v[50:53], v[10:17], v[210:217], 0, v192, v192 op_sel_hi:[0,0,0]
	v_mfma_scale_f32_16x16x128_f8f6f4 v[38:41], v[2:9], v[218:225], 0, v192, v192 op_sel_hi:[0,0,0]
	v_mfma_scale_f32_16x16x128_f8f6f4 v[34:37], v[10:17], v[218:225], 0, v192, v192 op_sel_hi:[0,0,0]
	s_setprio 0
	s_barrier
; #define PG8_STAGE(bufoff, gbase, voff) do { _Pragma("unroll") for (int _i = 0; _i < 2; ++_i) \
;         __builtin_amdgcn_global_load_lds((const unsigned*)((const char*)(gbase) + (voff)[_i]), (PG8_LAS unsigned*)(lds + (bufoff) + ldsw + _i * 8192), 16, 0, 0); } while (0)
; #define PG8_WAIT_V(n) asm volatile("s_waitcnt vmcnt(" #n ")" ::: "memory")
; #define PG8_WAIT_L(n) asm volatile("s_waitcnt lgkmcnt(" #n ")" ::: "memory")
; template <class Epi, class Sched, bool ALIGN_EPI = true, bool F8 = false>
; __device__ __forceinline__ void gemm_phase(PG8_LAS unsigned char* lds, const Sched& S, const Epi& E) {
;     ...
;         for (int t = 0; t < nt; t += 2) {
;             const bool last = (t == nt - 2);
;             if constexpr (Sched::GATHER) { if (last && has_next) S.a_off(nxt, Rs, Cs, voffAn); }
;             const char* a1 = cA + (size_t)(t + 1) * kstep;
;             const char* a2 = last ? nA : cA + (size_t)(t + 2) * kstep; const char* b2 = last ? nB : cB + (size_t)(t + 2) * kstepB;
;             const char* a3 = a2 + kstep; const char* b3 = b2 + kstepB;
;             unsigned vA2[2][2];
; #pragma unroll
;             for (int h = 0; h < 2; ++h)
; #pragma unroll
;                 for (int i = 0; i < 2; ++i) { if constexpr (Sched::GATHER) vA2[h][i] = (last && has_next) ? voffAn[h][i] : voffA[h][i]; else vA2[h][i] = voffA[h][i]; }
;             PG8_LDB(B0, 0, 0); PG8_LDB(B1, 0, 1); PG8_SCHED; PG8_LDA(At, 0, 0); PG8_STAGE(PG8_SA(1, 1), a1, voffA[1]);
;             PG8_WAIT_V(8); PG8_WAIT_L(0); PG8_BAR; PG8_MMA(0, 0, At, B0); PG8_MMA(0, 1, At, B1); PG8_BAR; PG8_SCHED;
;             PG8_LDA(At, 0, 1); PG8_STAGE(PG8_SB(0, 0), b2, voffB[0]); PG8_STAGE(PG8_SB(0, 1), b2, voffB[1]); PG8_STAGE(PG8_SA(0, 0), a2, vA2[0]);
;             PG8_WAIT_V(8); PG8_WAIT_L(0); PG8_BAR; PG8_MMA(1, 0, At, B0); PG8_MMA(1, 1, At, B1); PG8_BAR; PG8_SCHED;
;             PG8_LDB(B0, 1, 0); PG8_LDB(B1, 1, 1); PG8_SCHED; PG8_LDA(At, 1, 0); PG8_STAGE(PG8_SA(0, 1), a2, vA2[1]);
;             PG8_WAIT_V(8); PG8_WAIT_L(0); PG8_BAR; PG8_MMA(0, 0, At, B0); PG8_MMA(0, 1, At, B1); PG8_BAR; PG8_SCHED;
;             PG8_LDA(At, 1, 1); PG8_STAGE(PG8_SB(1, 0), b3, voffB[0]); PG8_STAGE(PG8_SB(1, 1), b3, voffB[1]); PG8_STAGE(PG8_SA(1, 0), a3, vA2[0]);
;             PG8_WAIT_V(8); PG8_WAIT_L(0); PG8_BAR; PG8_MMA(1, 0, At, B0); PG8_MMA(1, 1, At, B1); PG8_BAR; PG8_SCHED;
	s_add_i32 s69, 0, 0x18000
	s_add_i32 s70, 0, 0x1c000
	v_add_u32_e32 v14, s69, v187
	v_add_u32_e32 v30, s70, v187
	ds_read_b128 v[2:5], v14
	ds_read_b128 v[6:9], v14 offset:1024
	ds_read_b128 v[10:13], v14 offset:2048
	ds_read_b128 v[14:17], v14 offset:3072
	ds_read_b128 v[18:21], v30
	ds_read_b128 v[22:25], v30 offset:1024
	ds_read_b128 v[26:29], v30 offset:2048
	ds_read_b128 v[30:33], v30 offset:3072
	s_mov_b32 m0, s46
	v_lshl_add_u64 v[226:227], s[30:31], 0, v[172:173]
	ds_read_b128 v[194:197], v191 offset:32768
	ds_read_b128 v[198:201], v191 offset:33792
	ds_read_b128 v[202:205], v191 offset:34816
	ds_read_b128 v[206:209], v191 offset:35840
	ds_read_b128 v[210:213], v191 offset:36864
	ds_read_b128 v[214:217], v191 offset:37888
	ds_read_b128 v[218:221], v191 offset:38912
	ds_read_b128 v[222:225], v191 offset:39936
	global_load_lds_dwordx4 v[226:227], off
	v_lshl_add_u64 v[226:227], s[30:31], 0, v[174:175]
	s_mov_b32 m0, s47
	s_nop 0
	global_load_lds_dwordx4 v[226:227], off
	s_waitcnt vmcnt(8)
	s_waitcnt lgkmcnt(0)
	s_setprio 1
	v_mfma_scale_f32_16x16x128_f8f6f4 v[158:161], v[2:9], v[194:201], v[158:161], v192, v192 op_sel_hi:[0,0,0]
	v_mfma_scale_f32_16x16x128_f8f6f4 v[154:157], v[10:17], v[194:201], v[154:157], v192, v192 op_sel_hi:[0,0,0]
	v_mfma_scale_f32_16x16x128_f8f6f4 v[142:145], v[2:9], v[202:209], v[142:145], v192, v192 op_sel_hi:[0,0,0]
	v_mfma_scale_f32_16x16x128_f8f6f4 v[138:141], v[10:17], v[202:209], v[138:141], v192, v192 op_sel_hi:[0,0,0]
	v_mfma_scale_f32_16x16x128_f8f6f4 v[126:129], v[2:9], v[210:217], v[126:129], v192, v192 op_sel_hi:[0,0,0]
	v_mfma_scale_f32_16x16x128_f8f6f4 v[122:125], v[10:17], v[210:217], v[122:125], v192, v192 op_sel_hi:[0,0,0]
	v_mfma_scale_f32_16x16x128_f8f6f4 v[110:113], v[2:9], v[218:225], v[110:113], v192, v192 op_sel_hi:[0,0,0]
	v_mfma_scale_f32_16x16x128_f8f6f4 v[106:109], v[10:17], v[218:225], v[106:109], v192, v192 op_sel_hi:[0,0,0]
	s_nop 3
	s_setprio 0
	s_setprio 1
	v_mfma_scale_f32_16x16x128_f8f6f4 v[150:153], v[18:25], v[194:201], v[150:153], v192, v192 op_sel_hi:[0,0,0]
	v_mfma_scale_f32_16x16x128_f8f6f4 v[146:149], v[26:33], v[194:201], v[146:149], v192, v192 op_sel_hi:[0,0,0]
	v_mfma_scale_f32_16x16x128_f8f6f4 v[134:137], v[18:25], v[202:209], v[134:137], v192, v192 op_sel_hi:[0,0,0]
	v_mfma_scale_f32_16x16x128_f8f6f4 v[130:133], v[26:33], v[202:209], v[130:133], v192, v192 op_sel_hi:[0,0,0]
	v_mfma_scale_f32_16x16x128_f8f6f4 v[118:121], v[18:25], v[210:217], v[118:121], v192, v192 op_sel_hi:[0,0,0]
	v_mfma_scale_f32_16x16x128_f8f6f4 v[114:117], v[26:33], v[210:217], v[114:117], v192, v192 op_sel_hi:[0,0,0]
	v_mfma_scale_f32_16x16x128_f8f6f4 v[102:105], v[18:25], v[218:225], v[102:105], v192, v192 op_sel_hi:[0,0,0]
	v_mfma_scale_f32_16x16x128_f8f6f4 v[98:101], v[26:33], v[218:225], v[98:101], v192, v192 op_sel_hi:[0,0,0]
	s_setprio 0
	s_barrier
	s_add_u32 s28, s28, 0x8000
	s_addc_u32 s29, s29, 0
	s_add_i32 s30, s69, s43
	v_lshl_add_u64 v[226:227], s[28:29], 0, v[164:165]
	s_mov_b32 m0, s30
	ds_read_b128 v[194:197], v191 offset:49152
	ds_read_b128 v[198:201], v191 offset:50176
	ds_read_b128 v[202:205], v191 offset:51200
	ds_read_b128 v[206:209], v191 offset:52224
	ds_read_b128 v[210:213], v191 offset:53248
	ds_read_b128 v[214:217], v191 offset:54272
	ds_read_b128 v[218:221], v191 offset:55296
	ds_read_b128 v[222:225], v191 offset:56320
	global_load_lds_dwordx4 v[226:227], off
	v_lshl_add_u64 v[226:227], s[28:29], 0, v[166:167]
	s_add_i32 m0, s30, 0x2000
	s_add_i32 s30, s70, s43
	global_load_lds_dwordx4 v[226:227], off
	v_lshl_add_u64 v[226:227], s[28:29], 0, v[178:179]
	s_mov_b32 m0, s30
	s_nop 0
	global_load_lds_dwordx4 v[226:227], off
	v_lshl_add_u64 v[226:227], s[28:29], 0, v[180:181]
	s_add_i32 m0, s30, 0x2000
	s_nop 0
	global_load_lds_dwordx4 v[226:227], off
	v_lshl_add_u64 v[226:227], s[26:27], 0, v[168:169]
	s_mov_b32 m0, s51
	s_nop 0
	global_load_lds_dwordx4 v[226:227], off
	v_lshl_add_u64 v[226:227], s[26:27], 0, v[170:171]
	s_mov_b32 m0, s52
	s_nop 0
	global_load_lds_dwordx4 v[226:227], off
	s_waitcnt vmcnt(8)
	s_waitcnt lgkmcnt(0)
	s_setprio 1
	v_mfma_scale_f32_16x16x128_f8f6f4 v[94:97], v[2:9], v[194:201], v[94:97], v192, v192 op_sel_hi:[0,0,0]
	v_mfma_scale_f32_16x16x128_f8f6f4 v[90:93], v[10:17], v[194:201], v[90:93], v192, v192 op_sel_hi:[0,0,0]
	v_mfma_scale_f32_16x16x128_f8f6f4 v[78:81], v[2:9], v[202:209], v[78:81], v192, v192 op_sel_hi:[0,0,0]
	v_mfma_scale_f32_16x16x128_f8f6f4 v[74:77], v[10:17], v[202:209], v[74:77], v192, v192 op_sel_hi:[0,0,0]
	v_mfma_scale_f32_16x16x128_f8f6f4 v[62:65], v[2:9], v[210:217], v[62:65], v192, v192 op_sel_hi:[0,0,0]
	v_mfma_scale_f32_16x16x128_f8f6f4 v[58:61], v[10:17], v[210:217], v[58:61], v192, v192 op_sel_hi:[0,0,0]
	v_mfma_scale_f32_16x16x128_f8f6f4 v[46:49], v[2:9], v[218:225], v[46:49], v192, v192 op_sel_hi:[0,0,0]
	v_mfma_scale_f32_16x16x128_f8f6f4 v[42:45], v[10:17], v[218:225], v[42:45], v192, v192 op_sel_hi:[0,0,0]
	s_nop 3
	s_setprio 0
	s_setprio 1
	v_mfma_scale_f32_16x16x128_f8f6f4 v[86:89], v[18:25], v[194:201], v[86:89], v192, v192 op_sel_hi:[0,0,0]
	v_mfma_scale_f32_16x16x128_f8f6f4 v[82:85], v[26:33], v[194:201], v[82:85], v192, v192 op_sel_hi:[0,0,0]
	v_mfma_scale_f32_16x16x128_f8f6f4 v[70:73], v[18:25], v[202:209], v[70:73], v192, v192 op_sel_hi:[0,0,0]
	v_mfma_scale_f32_16x16x128_f8f6f4 v[66:69], v[26:33], v[202:209], v[66:69], v192, v192 op_sel_hi:[0,0,0]
	v_mfma_scale_f32_16x16x128_f8f6f4 v[54:57], v[18:25], v[210:217], v[54:57], v192, v192 op_sel_hi:[0,0,0]
	v_mfma_scale_f32_16x16x128_f8f6f4 v[50:53], v[26:33], v[210:217], v[50:53], v192, v192 op_sel_hi:[0,0,0]
	v_mfma_scale_f32_16x16x128_f8f6f4 v[38:41], v[18:25], v[218:225], v[38:41], v192, v192 op_sel_hi:[0,0,0]
	v_mfma_scale_f32_16x16x128_f8f6f4 v[34:37], v[26:33], v[218:225], v[34:37], v192, v192 op_sel_hi:[0,0,0]
	s_setprio 0
	s_barrier
	s_add_i32 s68, s68, 2
	s_add_u32 s23, s23, 0x10000
	s_addc_u32 s67, s67, 0
	s_add_u32 s24, s24, 0x10000
	s_addc_u32 s25, s25, 0
	s_cmp_gt_u32 s68, 5
	s_cbranch_scc0 .LBB0_1138
	s_branch .Lfx_33571

; #define PG8_STAGE(bufoff, gbase, voff) do { _Pragma("unroll") for (int _i = 0; _i < 2; ++_i) \
;         __builtin_amdgcn_global_load_lds((const unsigned*)((const char*)(gbase) + (voff)[_i]), (PG8_LAS unsigned*)(lds + (bufoff) + ldsw + _i * 8192), 16, 0, 0); } while (0)
; #define PG8_WAIT_V(n) asm volatile("s_waitcnt vmcnt(" #n ")" ::: "memory")
; #define PG8_WAIT_L(n) asm volatile("s_waitcnt lgkmcnt(" #n ")" ::: "memory")
; #define PG8_BAR __builtin_amdgcn_s_barrier()
; #define PG8_SCHED __builtin_amdgcn_sched_barrier(0)
; template <class Epi, class Sched, bool ALIGN_EPI = true, bool F8 = false>
; __device__ __forceinline__ void gemm_phase(PG8_LAS unsigned char* lds, const Sched& S, const Epi& E) {
;     ...
;             PG8_LDB(B0, 0, 0); PG8_LDB(B1, 0, 1); PG8_SCHED; PG8_LDA(At, 0, 0); PG8_STAGE(PG8_SA(1, 1), a1, voffA[1]);
;             PG8_WAIT_V(8); PG8_WAIT_L(0); PG8_BAR; PG8_MMA(0, 0, At, B0); PG8_MMA(0, 1, At, B1); PG8_BAR; PG8_SCHED;
;             PG8_LDA(At, 0, 1); PG8_STAGE(PG8_SB(0, 0), b2, voffB[0]); PG8_STAGE(PG8_SB(0, 1), b2, voffB[1]); PG8_STAGE(PG8_SA(0, 0), a2, vA2[0]);
;             PG8_WAIT_V(8); PG8_WAIT_L(0); PG8_BAR; PG8_MMA(1, 0, At, B0); PG8_MMA(1, 1, At, B1); PG8_BAR; PG8_SCHED;
;             PG8_LDB(B0, 1, 0); PG8_LDB(B1, 1, 1); PG8_SCHED; PG8_LDA(At, 1, 0); PG8_STAGE(PG8_SA(0, 1), a2, vA2[1]);
;             PG8_WAIT_V(8); PG8_WAIT_L(0); PG8_BAR; PG8_MMA(0, 0, At, B0); PG8_MMA(0, 1, At, B1); PG8_BAR; PG8_SCHED;
;             PG8_LDA(At, 1, 1); PG8_STAGE(PG8_SB(1, 0), b3, voffB[0]); PG8_STAGE(PG8_SB(1, 1), b3, voffB[1]); PG8_STAGE(PG8_SA(1, 0), a3, vA2[0]);
;             PG8_WAIT_V(8); PG8_WAIT_L(0); PG8_BAR; PG8_MMA(1, 0, At, B0); PG8_MMA(1, 1, At, B1); PG8_BAR; PG8_SCHED;
.Lh1e_33571:
.Lpk1_1138:
	ds_read_b128 v[18:21], v189
	ds_read_b128 v[22:25], v189 offset:1024
	ds_read_b128 v[26:29], v189 offset:2048
	ds_read_b128 v[30:33], v189 offset:3072
	ds_read_b128 v[2:5], v190
	ds_read_b128 v[6:9], v190 offset:1024
	ds_read_b128 v[10:13], v190 offset:2048
	ds_read_b128 v[14:17], v190 offset:3072
	s_add_u32 s26, s24, 0x8000
	s_addc_u32 s27, s25, 0
	s_cmp_eq_u32 s68, 4
	s_cselect_b32 s30, s16, s26
	s_cselect_b32 s31, s17, s27
	s_cselect_b32 s28, s18, s23
	s_cselect_b32 s29, s19, s67
	s_add_u32 s26, s30, 0x8000
	s_addc_u32 s27, s31, 0
	v_lshl_add_u64 v[226:227], s[24:25], 0, v[184:185]
	s_add_i32 m0, s44, 0xc000
	ds_read_b128 v[194:197], v191
	ds_read_b128 v[198:201], v191 offset:1024
	ds_read_b128 v[202:205], v191 offset:2048
	ds_read_b128 v[206:209], v191 offset:3072
	ds_read_b128 v[210:213], v191 offset:4096
	ds_read_b128 v[214:217], v191 offset:5120
	ds_read_b128 v[218:221], v191 offset:6144
	ds_read_b128 v[222:225], v191 offset:7168
	global_load_lds_dwordx4 v[226:227], off
	v_lshl_add_u64 v[226:227], s[24:25], 0, v[182:183]
	s_add_i32 m0, s44, 0xe000
	s_nop 0
	global_load_lds_dwordx4 v[226:227], off
	s_waitcnt vmcnt(8)
	s_waitcnt lgkmcnt(0)
	s_barrier
	s_setprio 2
	v_mfma_scale_f32_16x16x128_f8f6f4 v[158:161], v[18:25], v[194:201], 0, v192, v192 op_sel_hi:[0,0,0]
	v_mfma_scale_f32_16x16x128_f8f6f4 v[154:157], v[26:33], v[194:201], 0, v192, v192 op_sel_hi:[0,0,0]
	v_mfma_scale_f32_16x16x128_f8f6f4 v[142:145], v[18:25], v[202:209], 0, v192, v192 op_sel_hi:[0,0,0]
	v_mfma_scale_f32_16x16x128_f8f6f4 v[138:141], v[26:33], v[202:209], 0, v192, v192 op_sel_hi:[0,0,0]
	v_mfma_scale_f32_16x16x128_f8f6f4 v[126:129], v[18:25], v[210:217], 0, v192, v192 op_sel_hi:[0,0,0]
	v_mfma_scale_f32_16x16x128_f8f6f4 v[122:125], v[26:33], v[210:217], 0, v192, v192 op_sel_hi:[0,0,0]
	v_mfma_scale_f32_16x16x128_f8f6f4 v[110:113], v[18:25], v[218:225], 0, v192, v192 op_sel_hi:[0,0,0]
	v_mfma_scale_f32_16x16x128_f8f6f4 v[106:109], v[26:33], v[218:225], 0, v192, v192 op_sel_hi:[0,0,0]
	s_nop 3
	s_setprio 0
	s_setprio 2
	v_mfma_scale_f32_16x16x128_f8f6f4 v[150:153], v[2:9], v[194:201], 0, v192, v192 op_sel_hi:[0,0,0]
	v_mfma_scale_f32_16x16x128_f8f6f4 v[146:149], v[10:17], v[194:201], 0, v192, v192 op_sel_hi:[0,0,0]
	v_mfma_scale_f32_16x16x128_f8f6f4 v[134:137], v[2:9], v[202:209], 0, v192, v192 op_sel_hi:[0,0,0]
	v_mfma_scale_f32_16x16x128_f8f6f4 v[130:133], v[10:17], v[202:209], 0, v192, v192 op_sel_hi:[0,0,0]
	v_mfma_scale_f32_16x16x128_f8f6f4 v[118:121], v[2:9], v[210:217], 0, v192, v192 op_sel_hi:[0,0,0]
	v_mfma_scale_f32_16x16x128_f8f6f4 v[114:117], v[10:17], v[210:217], 0, v192, v192 op_sel_hi:[0,0,0]
	v_mfma_scale_f32_16x16x128_f8f6f4 v[102:105], v[2:9], v[218:225], 0, v192, v192 op_sel_hi:[0,0,0]
	v_mfma_scale_f32_16x16x128_f8f6f4 v[98:101], v[10:17], v[218:225], 0, v192, v192 op_sel_hi:[0,0,0]
	s_setprio 0
	s_add_i32 s69, s53, s43
	v_lshl_add_u64 v[226:227], s[28:29], 0, v[164:165]
	s_mov_b32 m0, s69
	ds_read_b128 v[194:197], v191 offset:16384
	ds_read_b128 v[198:201], v191 offset:17408
	ds_read_b128 v[202:205], v191 offset:18432
	ds_read_b128 v[206:209], v191 offset:19456
	ds_read_b128 v[210:213], v191 offset:20480
	ds_read_b128 v[214:217], v191 offset:21504
	ds_read_b128 v[218:221], v191 offset:22528
	ds_read_b128 v[222:225], v191 offset:23552
	global_load_lds_dwordx4 v[226:227], off
	v_lshl_add_u64 v[228:229], s[28:29], 0, v[166:167]
	s_add_i32 m0, s69, 0x2000
	s_add_i32 s69, s58, s43
	global_load_lds_dwordx4 v[228:229], off
	v_lshl_add_u64 v[226:227], v[226:227], 0, s[4:5]
	s_mov_b32 m0, s69
	s_nop 0
	global_load_lds_dwordx4 v[226:227], off
	v_lshl_add_u64 v[226:227], v[228:229], 0, s[4:5]
	s_add_i32 m0, s69, 0x2000
	s_nop 0
	global_load_lds_dwordx4 v[226:227], off
	v_lshl_add_u64 v[226:227], s[30:31], 0, v[168:169]
	s_mov_b32 m0, s44
	s_nop 0
	global_load_lds_dwordx4 v[226:227], off
	v_lshl_add_u64 v[226:227], s[30:31], 0, v[170:171]
	s_mov_b32 m0, s45
	s_nop 0
	global_load_lds_dwordx4 v[226:227], off
	s_waitcnt vmcnt(8)
	s_waitcnt lgkmcnt(0)
	s_barrier
	s_setprio 2
	v_mfma_scale_f32_16x16x128_f8f6f4 v[94:97], v[18:25], v[194:201], 0, v192, v192 op_sel_hi:[0,0,0]
	v_mfma_scale_f32_16x16x128_f8f6f4 v[90:93], v[26:33], v[194:201], 0, v192, v192 op_sel_hi:[0,0,0]
	v_mfma_scale_f32_16x16x128_f8f6f4 v[78:81], v[18:25], v[202:209], 0, v192, v192 op_sel_hi:[0,0,0]
	v_mfma_scale_f32_16x16x128_f8f6f4 v[74:77], v[26:33], v[202:209], 0, v192, v192 op_sel_hi:[0,0,0]
	v_mfma_scale_f32_16x16x128_f8f6f4 v[62:65], v[18:25], v[210:217], 0, v192, v192 op_sel_hi:[0,0,0]
	v_mfma_scale_f32_16x16x128_f8f6f4 v[58:61], v[26:33], v[210:217], 0, v192, v192 op_sel_hi:[0,0,0]
	v_mfma_scale_f32_16x16x128_f8f6f4 v[46:49], v[18:25], v[218:225], 0, v192, v192 op_sel_hi:[0,0,0]
	v_mfma_scale_f32_16x16x128_f8f6f4 v[42:45], v[26:33], v[218:225], 0, v192, v192 op_sel_hi:[0,0,0]
	s_nop 3
	s_setprio 0
	s_setprio 2
	v_mfma_scale_f32_16x16x128_f8f6f4 v[86:89], v[2:9], v[194:201], 0, v192, v192 op_sel_hi:[0,0,0]
	v_mfma_scale_f32_16x16x128_f8f6f4 v[82:85], v[10:17], v[194:201], 0, v192, v192 op_sel_hi:[0,0,0]
	v_mfma_scale_f32_16x16x128_f8f6f4 v[70:73], v[2:9], v[202:209], 0, v192, v192 op_sel_hi:[0,0,0]
	v_mfma_scale_f32_16x16x128_f8f6f4 v[66:69], v[10:17], v[202:209], 0, v192, v192 op_sel_hi:[0,0,0]
	v_mfma_scale_f32_16x16x128_f8f6f4 v[54:57], v[2:9], v[210:217], 0, v192, v192 op_sel_hi:[0,0,0]
	v_mfma_scale_f32_16x16x128_f8f6f4 v[50:53], v[10:17], v[210:217], 0, v192, v192 op_sel_hi:[0,0,0]
	v_mfma_scale_f32_16x16x128_f8f6f4 v[38:41], v[2:9], v[218:225], 0, v192, v192 op_sel_hi:[0,0,0]
	v_mfma_scale_f32_16x16x128_f8f6f4 v[34:37], v[10:17], v[218:225], 0, v192, v192 op_sel_hi:[0,0,0]
	s_setprio 0
	s_add_i32 s69, 0, 0x18000
	s_add_i32 s70, 0, 0x1c000
	v_add_u32_e32 v14, s69, v187
	v_add_u32_e32 v30, s70, v187
	ds_read_b128 v[2:5], v14
	ds_read_b128 v[6:9], v14 offset:1024
	ds_read_b128 v[10:13], v14 offset:2048
	ds_read_b128 v[14:17], v14 offset:3072
	ds_read_b128 v[18:21], v30
	ds_read_b128 v[22:25], v30 offset:1024
	ds_read_b128 v[26:29], v30 offset:2048
	ds_read_b128 v[30:33], v30 offset:3072
	s_mov_b32 m0, s46
	v_lshl_add_u64 v[226:227], s[30:31], 0, v[172:173]
	ds_read_b128 v[194:197], v191 offset:32768
	ds_read_b128 v[198:201], v191 offset:33792
	ds_read_b128 v[202:205], v191 offset:34816
	ds_read_b128 v[206:209], v191 offset:35840
	ds_read_b128 v[210:213], v191 offset:36864
	ds_read_b128 v[214:217], v191 offset:37888
	ds_read_b128 v[218:221], v191 offset:38912
	ds_read_b128 v[222:225], v191 offset:39936
	global_load_lds_dwordx4 v[226:227], off
	v_lshl_add_u64 v[226:227], s[30:31], 0, v[174:175]
	s_mov_b32 m0, s47
	s_nop 0
	global_load_lds_dwordx4 v[226:227], off
	s_waitcnt vmcnt(8)
	s_waitcnt lgkmcnt(0)
	s_barrier
; #define PG8_STAGE(bufoff, gbase, voff) do { _Pragma("unroll") for (int _i = 0; _i < 2; ++_i) \
;         __builtin_amdgcn_global_load_lds((const unsigned*)((const char*)(gbase) + (voff)[_i]), (PG8_LAS unsigned*)(lds + (bufoff) + ldsw + _i * 8192), 16, 0, 0); } while (0)
; #define PG8_WAIT_V(n) asm volatile("s_waitcnt vmcnt(" #n ")" ::: "memory")
; #define PG8_WAIT_L(n) asm volatile("s_waitcnt lgkmcnt(" #n ")" ::: "memory")
; template <class Epi, class Sched, bool ALIGN_EPI = true, bool F8 = false>
; __device__ __forceinline__ void gemm_phase(PG8_LAS unsigned char* lds, const Sched& S, const Epi& E) {
;     ...
;         for (int t = 0; t < nt; t += 2) {
;             const bool last = (t == nt - 2);
;             if constexpr (Sched::GATHER) { if (last && has_next) S.a_off(nxt, Rs, Cs, voffAn); }
;             const char* a1 = cA + (size_t)(t + 1) * kstep;
;             const char* a2 = last ? nA : cA + (size_t)(t + 2) * kstep; const char* b2 = last ? nB : cB + (size_t)(t + 2) * kstepB;
;             const char* a3 = a2 + kstep; const char* b3 = b2 + kstepB;
;             unsigned vA2[2][2];
; #pragma unroll
;             for (int h = 0; h < 2; ++h)
; #pragma unroll
;                 for (int i = 0; i < 2; ++i) { if constexpr (Sched::GATHER) vA2[h][i] = (last && has_next) ? voffAn[h][i] : voffA[h][i]; else vA2[h][i] = voffA[h][i]; }
;             PG8_LDB(B0, 0, 0); PG8_LDB(B1, 0, 1); PG8_SCHED; PG8_LDA(At, 0, 0); PG8_STAGE(PG8_SA(1, 1), a1, voffA[1]);
;             PG8_WAIT_V(8); PG8_WAIT_L(0); PG8_BAR; PG8_MMA(0, 0, At, B0); PG8_MMA(0, 1, At, B1); PG8_BAR; PG8_SCHED;
;             PG8_LDA(At, 0, 1); PG8_STAGE(PG8_SB(0, 0), b2, voffB[0]); PG8_STAGE(PG8_SB(0, 1), b2, voffB[1]); PG8_STAGE(PG8_SA(0, 0), a2, vA2[0]);
;             PG8_WAIT_V(8); PG8_WAIT_L(0); PG8_BAR; PG8_MMA(1, 0, At, B0); PG8_MMA(1, 1, At, B1); PG8_BAR; PG8_SCHED;
;             PG8_LDB(B0, 1, 0); PG8_LDB(B1, 1, 1); PG8_SCHED; PG8_LDA(At, 1, 0); PG8_STAGE(PG8_SA(0, 1), a2, vA2[1]);
;             PG8_WAIT_V(8); PG8_WAIT_L(0); PG8_BAR; PG8_MMA(0, 0, At, B0); PG8_MMA(0, 1, At, B1); PG8_BAR; PG8_SCHED;
;             PG8_LDA(At, 1, 1); PG8_STAGE(PG8_SB(1, 0), b3, voffB[0]); PG8_STAGE(PG8_SB(1, 1), b3, voffB[1]); PG8_STAGE(PG8_SA(1, 0), a3, vA2[0]);
;             PG8_WAIT_V(8); PG8_WAIT_L(0); PG8_BAR; PG8_MMA(1, 0, At, B0); PG8_MMA(1, 1, At, B1); PG8_BAR; PG8_SCHED;
	s_setprio 2
	v_mfma_scale_f32_16x16x128_f8f6f4 v[158:161], v[2:9], v[194:201], v[158:161], v192, v192 op_sel_hi:[0,0,0]
	v_mfma_scale_f32_16x16x128_f8f6f4 v[154:157], v[10:17], v[194:201], v[154:157], v192, v192 op_sel_hi:[0,0,0]
	v_mfma_scale_f32_16x16x128_f8f6f4 v[142:145], v[2:9], v[202:209], v[142:145], v192, v192 op_sel_hi:[0,0,0]
	v_mfma_scale_f32_16x16x128_f8f6f4 v[138:141], v[10:17], v[202:209], v[138:141], v192, v192 op_sel_hi:[0,0,0]
	v_mfma_scale_f32_16x16x128_f8f6f4 v[126:129], v[2:9], v[210:217], v[126:129], v192, v192 op_sel_hi:[0,0,0]
	v_mfma_scale_f32_16x16x128_f8f6f4 v[122:125], v[10:17], v[210:217], v[122:125], v192, v192 op_sel_hi:[0,0,0]
	v_mfma_scale_f32_16x16x128_f8f6f4 v[110:113], v[2:9], v[218:225], v[110:113], v192, v192 op_sel_hi:[0,0,0]
	v_mfma_scale_f32_16x16x128_f8f6f4 v[106:109], v[10:17], v[218:225], v[106:109], v192, v192 op_sel_hi:[0,0,0]
	s_nop 3
	s_setprio 0
	s_setprio 2
	v_mfma_scale_f32_16x16x128_f8f6f4 v[150:153], v[18:25], v[194:201], v[150:153], v192, v192 op_sel_hi:[0,0,0]
	v_mfma_scale_f32_16x16x128_f8f6f4 v[146:149], v[26:33], v[194:201], v[146:149], v192, v192 op_sel_hi:[0,0,0]
	v_mfma_scale_f32_16x16x128_f8f6f4 v[134:137], v[18:25], v[202:209], v[134:137], v192, v192 op_sel_hi:[0,0,0]
	v_mfma_scale_f32_16x16x128_f8f6f4 v[130:133], v[26:33], v[202:209], v[130:133], v192, v192 op_sel_hi:[0,0,0]
	v_mfma_scale_f32_16x16x128_f8f6f4 v[118:121], v[18:25], v[210:217], v[118:121], v192, v192 op_sel_hi:[0,0,0]
	v_mfma_scale_f32_16x16x128_f8f6f4 v[114:117], v[26:33], v[210:217], v[114:117], v192, v192 op_sel_hi:[0,0,0]
	v_mfma_scale_f32_16x16x128_f8f6f4 v[102:105], v[18:25], v[218:225], v[102:105], v192, v192 op_sel_hi:[0,0,0]
	v_mfma_scale_f32_16x16x128_f8f6f4 v[98:101], v[26:33], v[218:225], v[98:101], v192, v192 op_sel_hi:[0,0,0]
	s_setprio 0
	s_add_u32 s28, s28, 0x8000
	s_addc_u32 s29, s29, 0
	s_add_i32 s30, s69, s43
	v_lshl_add_u64 v[226:227], s[28:29], 0, v[164:165]
	s_mov_b32 m0, s30
	ds_read_b128 v[194:197], v191 offset:49152
	ds_read_b128 v[198:201], v191 offset:50176
	ds_read_b128 v[202:205], v191 offset:51200
	ds_read_b128 v[206:209], v191 offset:52224
	ds_read_b128 v[210:213], v191 offset:53248
	ds_read_b128 v[214:217], v191 offset:54272
	ds_read_b128 v[218:221], v191 offset:55296
	ds_read_b128 v[222:225], v191 offset:56320
	global_load_lds_dwordx4 v[226:227], off
	v_lshl_add_u64 v[226:227], s[28:29], 0, v[166:167]
	s_add_i32 m0, s30, 0x2000
	s_add_i32 s30, s70, s43
	global_load_lds_dwordx4 v[226:227], off
	v_lshl_add_u64 v[226:227], s[28:29], 0, v[178:179]
	s_mov_b32 m0, s30
	s_nop 0
	global_load_lds_dwordx4 v[226:227], off
	v_lshl_add_u64 v[226:227], s[28:29], 0, v[180:181]
	s_add_i32 m0, s30, 0x2000
	s_nop 0
	global_load_lds_dwordx4 v[226:227], off
	v_lshl_add_u64 v[226:227], s[26:27], 0, v[168:169]
	s_mov_b32 m0, s51
	s_nop 0
	global_load_lds_dwordx4 v[226:227], off
	v_lshl_add_u64 v[226:227], s[26:27], 0, v[170:171]
	s_mov_b32 m0, s52
	s_nop 0
	global_load_lds_dwordx4 v[226:227], off
	s_waitcnt vmcnt(8)
	s_waitcnt lgkmcnt(0)
	s_barrier
	s_setprio 2
	v_mfma_scale_f32_16x16x128_f8f6f4 v[94:97], v[2:9], v[194:201], v[94:97], v192, v192 op_sel_hi:[0,0,0]
	v_mfma_scale_f32_16x16x128_f8f6f4 v[90:93], v[10:17], v[194:201], v[90:93], v192, v192 op_sel_hi:[0,0,0]
	v_mfma_scale_f32_16x16x128_f8f6f4 v[78:81], v[2:9], v[202:209], v[78:81], v192, v192 op_sel_hi:[0,0,0]
	v_mfma_scale_f32_16x16x128_f8f6f4 v[74:77], v[10:17], v[202:209], v[74:77], v192, v192 op_sel_hi:[0,0,0]
	v_mfma_scale_f32_16x16x128_f8f6f4 v[62:65], v[2:9], v[210:217], v[62:65], v192, v192 op_sel_hi:[0,0,0]
	v_mfma_scale_f32_16x16x128_f8f6f4 v[58:61], v[10:17], v[210:217], v[58:61], v192, v192 op_sel_hi:[0,0,0]
	v_mfma_scale_f32_16x16x128_f8f6f4 v[46:49], v[2:9], v[218:225], v[46:49], v192, v192 op_sel_hi:[0,0,0]
	v_mfma_scale_f32_16x16x128_f8f6f4 v[42:45], v[10:17], v[218:225], v[42:45], v192, v192 op_sel_hi:[0,0,0]
	s_nop 3
	s_setprio 0
	s_setprio 2
	v_mfma_scale_f32_16x16x128_f8f6f4 v[86:89], v[18:25], v[194:201], v[86:89], v192, v192 op_sel_hi:[0,0,0]
	v_mfma_scale_f32_16x16x128_f8f6f4 v[82:85], v[26:33], v[194:201], v[82:85], v192, v192 op_sel_hi:[0,0,0]
	v_mfma_scale_f32_16x16x128_f8f6f4 v[70:73], v[18:25], v[202:209], v[70:73], v192, v192 op_sel_hi:[0,0,0]
	v_mfma_scale_f32_16x16x128_f8f6f4 v[66:69], v[26:33], v[202:209], v[66:69], v192, v192 op_sel_hi:[0,0,0]
	v_mfma_scale_f32_16x16x128_f8f6f4 v[54:57], v[18:25], v[210:217], v[54:57], v192, v192 op_sel_hi:[0,0,0]
	v_mfma_scale_f32_16x16x128_f8f6f4 v[50:53], v[26:33], v[210:217], v[50:53], v192, v192 op_sel_hi:[0,0,0]
	v_mfma_scale_f32_16x16x128_f8f6f4 v[38:41], v[18:25], v[218:225], v[38:41], v192, v192 op_sel_hi:[0,0,0]
	v_mfma_scale_f32_16x16x128_f8f6f4 v[34:37], v[26:33], v[218:225], v[34:37], v192, v192 op_sel_hi:[0,0,0]
	s_setprio 0
	s_add_i32 s68, s68, 2
	s_add_u32 s23, s23, 0x10000
	s_addc_u32 s67, s67, 0
	s_add_u32 s24, s24, 0x10000
	s_addc_u32 s25, s25, 0
	s_cmp_gt_u32 s68, 5
	s_cbranch_scc0 .Lh1_1138
	s_branch .Lfx_33571
